# residual GEMM epilogue: B fragments read column-permuted from LDS so each lane holds 8 consecutive columns; residual loads/stores 16 B per lane; differential-attention scratch slabs lane-contiguous
# speedup vs baseline: 1.0340x; 1.0106x over previous
; #define LAS __attribute__((address_space(3)))
; __device__ __forceinline__ s16x4 tr_read(LAS const unsigned char* p) { return __builtin_bit_cast(s16x4, __builtin_amdgcn_ds_read_tr16_b64_v4i16((LAS v4i16_t*)p)); }
; __device__ __forceinline__ void partialSM(f32x16& p0, f32x16& p1, float& m_reg, float& mn, float& alpha, int dq, float slopeL, bool diag, bool rowmasked) {
;     ...
;     for (int r = 0; r < 16; ++r) { p0[r] = p0[r] - mn; p1[r] = p1[r] - mn; }
; #pragma unroll
;     for (int r = 0; r < 16; ++r) p0[r] = __builtin_amdgcn_exp2f(p0[r]);
; }
; __device__ __forceinline__ void finishSM(f32x16& p0, f32x16& p1, float alpha, float& l_reg, bf16x8& pa0, bf16x8& pa1, bf16x8& pa2, bf16x8& pa3) {
; #pragma unroll
;     for (int r = 0; r < 16; ++r) p1[r] = __builtin_amdgcn_exp2f(p1[r]);
;     float ps = 0;
; #pragma unroll
;     for (int r = 0; r < 16; ++r) ps += p0[r];
; #pragma unroll
;     for (int r = 0; r < 16; ++r) ps += p1[r];
;     { auto rr = __builtin_amdgcn_permlane32_swap(__float_as_uint(ps), __float_as_uint(ps), false, false);
;       ps = __uint_as_float(rr[0]) + __uint_as_float(rr[1]); }
;     l_reg = l_reg * alpha + ps;
;     ...
;     ATT_PK4(p0, 0, pa0); ATT_PK4(p0, 8, pa1); ATT_PK4(p1, 0, pa2); ATT_PK4(p1, 8, pa3);
;     ...
; }
; template <int D0> __device__ __forceinline__ void pv_one(f32x16& od, LAS const unsigned char* vb, bf16x8 pa0, bf16x8 pa1, bf16x8 pa2, bf16x8 pa3) {
;     const s16x4 l0 = tr_read(vb + v_rd_off(D0, 0, 0)), h0 = tr_read(vb + v_rd_off(D0, 0, 1)), l1 = tr_read(vb + v_rd_off(D0, 1, 0)), h1 = tr_read(vb + v_rd_off(D0, 1, 1));
;     const s16x4 l2 = tr_read(vb + v_rd_off(D0, 2, 0)), h2 = tr_read(vb + v_rd_off(D0, 2, 1)), l3 = tr_read(vb + v_rd_off(D0, 3, 0)), h3 = tr_read(vb + v_rd_off(D0, 3, 1));
;     ...
;     od = __builtin_amdgcn_mfma_f32_32x32x16_bf16(pa0, ATT_PK(l0, h0), od, 0, 0, 0);
;     od = __builtin_amdgcn_mfma_f32_32x32x16_bf16(pa1, ATT_PK(l1, h1), od, 0, 0, 0);
;     od = __builtin_amdgcn_mfma_f32_32x32x16_bf16(pa2, ATT_PK(l2, h2), od, 0, 0, 0);
;     od = __builtin_amdgcn_mfma_f32_32x32x16_bf16(pa3, ATT_PK(l3, h3), od, 0, 0, 0);
.LBB0_850:
	v_cndmask_b32_e64 v101, v101, v220, s[0:1]
	v_sub_f32_e32 v72, v72, v101
	v_sub_f32_e32 v73, v73, v101
	v_sub_f32_e32 v104, v76, v101
	v_exp_f32_e32 v76, v72
	v_sub_f32_e32 v96, v96, v101
	v_sub_f32_e32 v105, v77, v101
	v_exp_f32_e32 v77, v73
	v_sub_f32_e32 v97, v97, v101
	v_sub_f32_e32 v102, v94, v101
	v_exp_f32_e32 v94, v96
	v_sub_f32_e32 v98, v98, v101
	v_sub_f32_e32 v103, v95, v101
	v_exp_f32_e32 v95, v97
	v_sub_f32_e32 v78, v78, v101
	v_sub_f32_e32 v99, v99, v101
	v_sub_f32_e32 v74, v74, v101
	v_sub_f32_e32 v75, v75, v101
	v_sub_f32_e32 v106, v70, v101
	v_sub_f32_e32 v107, v71, v101
	v_sub_f32_e32 v108, v68, v101
	v_sub_f32_e32 v109, v69, v101
	v_exp_f32_e32 v96, v98
	v_sub_f32_e32 v79, v79, v101
	v_sub_f32_e32 v80, v80, v101
	v_sub_f32_e32 v81, v81, v101
	v_sub_f32_e32 v82, v82, v101
	v_sub_f32_e32 v83, v83, v101
	v_sub_f32_e32 v84, v84, v101
	v_sub_f32_e32 v85, v85, v101
	v_sub_f32_e32 v86, v86, v101
	v_sub_f32_e32 v87, v87, v101
	v_sub_f32_e32 v88, v88, v101
	v_sub_f32_e32 v89, v89, v101
	v_sub_f32_e32 v90, v90, v101
	v_sub_f32_e32 v91, v91, v101
	v_sub_f32_e32 v92, v92, v101
	v_sub_f32_e32 v93, v93, v101
	v_exp_f32_e32 v101, v78
	v_add_f32_e32 v78, 0, v76
	v_exp_f32_e32 v97, v99
	v_add_f32_e32 v78, v77, v78
	v_exp_f32_e32 v98, v102
	v_add_f32_e32 v78, v94, v78
	v_exp_f32_e32 v99, v103
	v_add_f32_e32 v78, v95, v78
	v_exp_f32_e32 v68, v104
	v_add_f32_e32 v78, v96, v78
	v_exp_f32_e32 v69, v105
	v_add_f32_e32 v78, v97, v78
	v_exp_f32_e32 v70, v74
	v_add_f32_e32 v78, v98, v78
	v_exp_f32_e32 v71, v75
	v_add_f32_e32 v78, v99, v78
	v_exp_f32_e32 v72, v106
	v_add_f32_e32 v78, v68, v78
	v_exp_f32_e32 v73, v107
	v_add_f32_e32 v78, v69, v78
	v_exp_f32_e32 v74, v108
	v_add_f32_e32 v78, v70, v78
	v_exp_f32_e32 v75, v109
	v_add_f32_e32 v78, v71, v78
	v_add_f32_e32 v78, v72, v78
	v_exp_f32_e32 v102, v79
	v_add_f32_e32 v78, v73, v78
	v_exp_f32_e32 v103, v80
	v_add_f32_e32 v78, v74, v78
	v_exp_f32_e32 v104, v81
	v_add_f32_e32 v78, v75, v78
	v_exp_f32_e32 v105, v82
	v_add_f32_e32 v78, v101, v78
	v_exp_f32_e32 v106, v83
	v_add_f32_e32 v78, v102, v78
	v_exp_f32_e32 v107, v84
	v_add_f32_e32 v78, v103, v78
	v_exp_f32_e32 v108, v85
	v_add_f32_e32 v78, v104, v78
	v_exp_f32_e32 v86, v86
	v_add_f32_e32 v78, v105, v78
	v_exp_f32_e32 v87, v87
	v_add_f32_e32 v78, v106, v78
	v_exp_f32_e32 v88, v88
	v_add_f32_e32 v78, v107, v78
	v_exp_f32_e32 v89, v89
	v_add_f32_e32 v78, v108, v78
	v_exp_f32_e32 v90, v90
	v_add_f32_e32 v78, v86, v78
	v_exp_f32_e32 v91, v91
	v_add_f32_e32 v78, v87, v78
	v_exp_f32_e32 v92, v92
	v_add_f32_e32 v78, v88, v78
	v_exp_f32_e32 v93, v93
	v_add_f32_e32 v78, v89, v78
	v_add_f32_e32 v78, v90, v78
	v_add_f32_e32 v78, v91, v78
	v_add_f32_e32 v78, v92, v78
	v_add_f32_e32 v84, v93, v78
	v_mov_b32_e32 v85, v84
	s_nop 1
	v_permlane32_swap_b32_e32 v84, v85
	v_cvt_pk_bf16_f32 v80, v76, v77
	v_cvt_pk_bf16_f32 v81, v94, v95
	v_cvt_pk_bf16_f32 v82, v96, v97
	v_cvt_pk_bf16_f32 v83, v98, v99
	v_cvt_pk_bf16_f32 v76, v68, v69
	v_cvt_pk_bf16_f32 v77, v70, v71
	v_cvt_pk_bf16_f32 v78, v72, v73
	v_cvt_pk_bf16_f32 v79, v74, v75
	v_cvt_pk_bf16_f32 v72, v101, v102
	v_cvt_pk_bf16_f32 v73, v103, v104
	v_cvt_pk_bf16_f32 v74, v105, v106
	v_cvt_pk_bf16_f32 v75, v107, v108
	v_cvt_pk_bf16_f32 v68, v86, v87
	v_cvt_pk_bf16_f32 v69, v88, v89
	v_cvt_pk_bf16_f32 v70, v90, v91
	v_cvt_pk_bf16_f32 v71, v92, v93
	v_permlane32_swap_b32_e32 v80, v82
	v_permlane32_swap_b32_e32 v81, v83
	v_permlane32_swap_b32_e32 v76, v78
	v_permlane32_swap_b32_e32 v77, v79
	v_permlane32_swap_b32_e32 v72, v74
	v_permlane32_swap_b32_e32 v73, v75
	v_permlane32_swap_b32_e32 v68, v70
	v_permlane32_swap_b32_e32 v69, v71
	ds_read_b64_tr_b16 v[86:87], v188 offset:16384
	ds_read_b64_tr_b16 v[88:89], v188 offset:18432
	v_cmp_gt_u32_e32 vcc, 32, v186
	s_waitcnt lgkmcnt(0)
	v_mfma_f32_32x32x16_bf16 v[36:51], v[80:83], v[86:89], v[36:51]
	ds_read_b64_tr_b16 v[86:87], v188 offset:20480
	ds_read_b64_tr_b16 v[88:89], v188 offset:22528
	s_waitcnt lgkmcnt(0)
	v_mfma_f32_32x32x16_bf16 v[36:51], v[76:79], v[86:89], v[36:51]
	ds_read_b64_tr_b16 v[86:87], v188 offset:24576
	ds_read_b64_tr_b16 v[88:89], v188 offset:26624
	s_waitcnt lgkmcnt(0)
	v_mfma_f32_32x32x16_bf16 v[36:51], v[72:75], v[86:89], v[36:51]
	ds_read_b64_tr_b16 v[86:87], v188 offset:28672
	ds_read_b64_tr_b16 v[88:89], v188 offset:30720
	s_waitcnt lgkmcnt(0)
	v_mfma_f32_32x32x16_bf16 v[36:51], v[68:71], v[86:89], v[36:51]
	ds_read_b64_tr_b16 v[86:87], v188 offset:16896
	ds_read_b64_tr_b16 v[88:89], v188 offset:18944
	s_waitcnt lgkmcnt(0)
	v_mfma_f32_32x32x16_bf16 v[20:35], v[80:83], v[86:89], v[20:35]
	ds_read_b64_tr_b16 v[86:87], v188 offset:20992
	ds_read_b64_tr_b16 v[88:89], v188 offset:23040
	s_waitcnt lgkmcnt(0)
	v_mfma_f32_32x32x16_bf16 v[20:35], v[76:79], v[86:89], v[20:35]
	ds_read_b64_tr_b16 v[86:87], v188 offset:25088
	ds_read_b64_tr_b16 v[88:89], v188 offset:27136
	s_waitcnt lgkmcnt(0)
	v_mfma_f32_32x32x16_bf16 v[20:35], v[72:75], v[86:89], v[20:35]
	ds_read_b64_tr_b16 v[86:87], v188 offset:29184
	ds_read_b64_tr_b16 v[88:89], v188 offset:31232
	s_waitcnt lgkmcnt(0)
	v_mfma_f32_32x32x16_bf16 v[20:35], v[68:71], v[86:89], v[20:35]
	ds_read_b64_tr_b16 v[86:87], v188 offset:17408
	ds_read_b64_tr_b16 v[88:89], v188 offset:19456
	s_waitcnt lgkmcnt(0)
	v_mfma_f32_32x32x16_bf16 v[52:67], v[80:83], v[86:89], v[52:67]
	ds_read_b64_tr_b16 v[86:87], v188 offset:21504
	ds_read_b64_tr_b16 v[88:89], v188 offset:23552
	s_waitcnt lgkmcnt(0)
	v_mfma_f32_32x32x16_bf16 v[52:67], v[76:79], v[86:89], v[52:67]
	ds_read_b64_tr_b16 v[86:87], v188 offset:25600
	ds_read_b64_tr_b16 v[88:89], v188 offset:27648
	s_waitcnt lgkmcnt(0)
; #define ATT_SBAR() __builtin_amdgcn_sched_barrier(0)
; __device__ __forceinline__ int crow(int r, int hi) { return (r & 3) + 8 * (r >> 2) + 4 * hi; }
; #define ATT_RESC(a) do { if (__any((a) < 1.f)) { if (hi == 0) al_l[r32] = (a); asm volatile("s_waitcnt lgkmcnt(0)" ::: "memory"); \
;     _Pragma("unroll") for (int d_ = 0; d_ < 4; ++d_) _Pragma("unroll") for (int r = 0; r < 16; ++r) o[d_][r] *= al_l[crow(r, hi)]; } } while (0)
; #define ATT_PSM(P0, P1, MN, AL, t) partialSM(P0, P1, m_reg, MN, AL, qpos - (t) * KVBLK - 4 * hi, U.slopeL, (t) * KVBLK + KVBLK - 1 > qlo, MOBA && ((t) >> 2) < U.moba_j && !((sel >> ((t) >> 2)) & 1u))
; template <bool MOBA>
; __device__ __forceinline__ void run_unit(const UnitDesc& U, LAS unsigned char* lds, f32x16 (&o)[4], float (&rli)[16]) {
;     ...
;     pv_d0(o, vb0, pa0, pa1, pa2, pa3); ATT_PSM(pB0, pB1, mnB, alB, NT - 1);
;     __syncthreads(); ATT_RESC(alB);
;     finishSM(pB0, pB1, alB, l_reg, pa0, pa1, pa2, pa3); ATT_SBAR();
;     pv_d0(o, vb0 + SHM_V, pa0, pa1, pa2, pa3);
;     if (hi == 0) li_l[r32] = l_reg;
;     asm volatile("s_waitcnt lgkmcnt(0)" ::: "memory");
; #pragma unroll
;     for (int r = 0; r < 16; ++r) rli[r] = 1.0f / li_l[crow(r, hi)];
;     __syncthreads();
	v_mfma_f32_32x32x16_bf16 v[52:67], v[72:75], v[86:89], v[52:67]
	ds_read_b64_tr_b16 v[86:87], v188 offset:29696
	ds_read_b64_tr_b16 v[88:89], v188 offset:31744
	s_waitcnt lgkmcnt(0)
	v_mfma_f32_32x32x16_bf16 v[52:67], v[68:71], v[86:89], v[52:67]
	ds_read_b64_tr_b16 v[86:87], v188 offset:17920
	ds_read_b64_tr_b16 v[88:89], v188 offset:19968
	s_waitcnt lgkmcnt(0)
	v_mfma_f32_32x32x16_bf16 v[4:19], v[80:83], v[86:89], v[4:19]
	ds_read_b64_tr_b16 v[80:81], v188 offset:22016
	ds_read_b64_tr_b16 v[82:83], v188 offset:24064
	s_waitcnt lgkmcnt(0)
	v_mfma_f32_32x32x16_bf16 v[4:19], v[76:79], v[80:83], v[4:19]
	ds_read_b64_tr_b16 v[76:77], v188 offset:26112
	ds_read_b64_tr_b16 v[78:79], v188 offset:28160
	s_waitcnt lgkmcnt(0)
	v_mfma_f32_32x32x16_bf16 v[4:19], v[72:75], v[76:79], v[4:19]
	ds_read_b64_tr_b16 v[72:73], v188 offset:30208
	ds_read_b64_tr_b16 v[74:75], v188 offset:32256
	s_waitcnt lgkmcnt(0)
	v_mfma_f32_32x32x16_bf16 v[4:19], v[68:71], v[72:75], v[4:19]
	s_and_saveexec_b64 s[0:1], vcc
	v_add_f32_e32 v1, v1, v2
	v_fmac_f32_e32 v1, v191, v178
	v_add_f32_e32 v2, v84, v85
	v_fmac_f32_e32 v2, v1, v100
	ds_write_b32 v189, v2
	s_or_b64 exec, exec, s[0:1]
	s_waitcnt lgkmcnt(0)
	ds_read_b128 v[72:75], v187
	ds_read_b128 v[68:71], v187 offset:32
	v_mov_b32_e32 v238, v219
	s_cmp_lg_u32 s2, 0
	s_waitcnt lgkmcnt(1)
	v_div_scale_f32 v1, s[0:1], v72, v72, 1.0
	v_rcp_f32_e32 v2, v1
	s_nop 0
	v_fma_f32 v76, -v1, v2, 1.0
	v_fmac_f32_e32 v2, v76, v2
	v_div_scale_f32 v76, vcc, 1.0, v72, 1.0
	v_mul_f32_e32 v77, v76, v2
	v_fma_f32 v78, -v1, v77, v76
	v_fmac_f32_e32 v77, v78, v2
	v_fma_f32 v1, -v1, v77, v76
	v_div_fmas_f32 v1, v1, v2, v77
	v_div_fixup_f32 v202, v1, v72, 1.0
	v_div_scale_f32 v1, s[0:1], v73, v73, 1.0
	v_rcp_f32_e32 v2, v1
	s_nop 0
	v_fma_f32 v72, -v1, v2, 1.0
	v_fmac_f32_e32 v2, v72, v2
	v_div_scale_f32 v72, vcc, 1.0, v73, 1.0
	v_mul_f32_e32 v76, v72, v2
	v_fma_f32 v77, -v1, v76, v72
	v_fmac_f32_e32 v76, v77, v2
	v_fma_f32 v1, -v1, v76, v72
	v_div_fmas_f32 v1, v1, v2, v76
	v_div_fixup_f32 v204, v1, v73, 1.0
	v_div_scale_f32 v1, s[0:1], v74, v74, 1.0
	v_rcp_f32_e32 v2, v1
	s_nop 0
	v_fma_f32 v72, -v1, v2, 1.0
	v_fmac_f32_e32 v2, v72, v2
	v_div_scale_f32 v72, vcc, 1.0, v74, 1.0
	v_mul_f32_e32 v73, v72, v2
	v_fma_f32 v76, -v1, v73, v72
	v_fmac_f32_e32 v73, v76, v2
	v_fma_f32 v1, -v1, v73, v72
	v_div_fmas_f32 v1, v1, v2, v73
	v_div_fixup_f32 v206, v1, v74, 1.0
	v_div_scale_f32 v1, s[0:1], v75, v75, 1.0
	v_rcp_f32_e32 v2, v1
	s_nop 0
	v_fma_f32 v72, -v1, v2, 1.0
	v_fmac_f32_e32 v2, v72, v2
	v_div_scale_f32 v72, vcc, 1.0, v75, 1.0
	v_mul_f32_e32 v73, v72, v2
	v_fma_f32 v74, -v1, v73, v72
	v_fmac_f32_e32 v73, v74, v2
	v_fma_f32 v1, -v1, v73, v72
	v_div_fmas_f32 v1, v1, v2, v73
	v_div_fixup_f32 v208, v1, v75, 1.0
	s_waitcnt lgkmcnt(0)
	v_div_scale_f32 v1, s[0:1], v68, v68, 1.0
	v_rcp_f32_e32 v2, v1
	s_nop 0
	v_fma_f32 v72, -v1, v2, 1.0
	v_fmac_f32_e32 v2, v72, v2
	v_div_scale_f32 v72, vcc, 1.0, v68, 1.0
	v_mul_f32_e32 v73, v72, v2
	v_fma_f32 v74, -v1, v73, v72
	v_fmac_f32_e32 v73, v74, v2
	v_fma_f32 v1, -v1, v73, v72
	v_div_fmas_f32 v1, v1, v2, v73
	v_div_fixup_f32 v210, v1, v68, 1.0
	v_div_scale_f32 v1, s[0:1], v69, v69, 1.0
	v_rcp_f32_e32 v2, v1
	s_nop 0
	v_fma_f32 v68, -v1, v2, 1.0
	v_fmac_f32_e32 v2, v68, v2
	v_div_scale_f32 v68, vcc, 1.0, v69, 1.0
	v_mul_f32_e32 v72, v68, v2
	v_fma_f32 v73, -v1, v72, v68
	v_fmac_f32_e32 v72, v73, v2
	v_fma_f32 v1, -v1, v72, v68
	v_div_fmas_f32 v1, v1, v2, v72
	v_div_fixup_f32 v212, v1, v69, 1.0
	v_div_scale_f32 v1, s[0:1], v70, v70, 1.0
	v_rcp_f32_e32 v2, v1
	s_nop 0
	v_fma_f32 v68, -v1, v2, 1.0
	v_fmac_f32_e32 v2, v68, v2
	v_div_scale_f32 v68, vcc, 1.0, v70, 1.0
	v_mul_f32_e32 v69, v68, v2
	v_fma_f32 v72, -v1, v69, v68
	v_fmac_f32_e32 v69, v72, v2
	v_fma_f32 v1, -v1, v69, v68
	v_div_fmas_f32 v1, v1, v2, v69
	v_div_fixup_f32 v214, v1, v70, 1.0
	v_div_scale_f32 v1, s[0:1], v71, v71, 1.0
	v_rcp_f32_e32 v2, v1
	s_nop 0
	v_fma_f32 v68, -v1, v2, 1.0
	v_fmac_f32_e32 v2, v68, v2
	v_div_scale_f32 v68, vcc, 1.0, v71, 1.0
	v_mul_f32_e32 v69, v68, v2
	v_fma_f32 v70, -v1, v69, v68
	v_fmac_f32_e32 v69, v70, v2
	v_fma_f32 v1, -v1, v69, v68
	v_div_fmas_f32 v1, v1, v2, v69
	v_div_fixup_f32 v216, v1, v71, 1.0
	ds_read_b128 v[68:71], v187 offset:64
	s_waitcnt lgkmcnt(0)
	v_div_scale_f32 v1, s[0:1], v68, v68, 1.0
	v_rcp_f32_e32 v2, v1
	s_nop 0
	v_fma_f32 v72, -v1, v2, 1.0
	v_fmac_f32_e32 v2, v72, v2
	v_div_scale_f32 v72, vcc, 1.0, v68, 1.0
	v_mul_f32_e32 v73, v72, v2
	v_fma_f32 v74, -v1, v73, v72
	v_fmac_f32_e32 v73, v74, v2
	v_fma_f32 v1, -v1, v73, v72
	v_div_fmas_f32 v1, v1, v2, v73
	v_div_fixup_f32 v218, v1, v68, 1.0
	v_div_scale_f32 v1, s[0:1], v69, v69, 1.0
	v_rcp_f32_e32 v2, v1
	s_nop 0
	v_fma_f32 v68, -v1, v2, 1.0
	v_fmac_f32_e32 v2, v68, v2
	v_div_scale_f32 v68, vcc, 1.0, v69, 1.0
	v_mul_f32_e32 v72, v68, v2
	v_fma_f32 v73, -v1, v72, v68
	v_fmac_f32_e32 v72, v73, v2
	v_fma_f32 v1, -v1, v72, v68
	v_div_fmas_f32 v1, v1, v2, v72
	v_div_fixup_f32 v220, v1, v69, 1.0
	v_div_scale_f32 v1, s[0:1], v70, v70, 1.0
	v_rcp_f32_e32 v2, v1
	s_nop 0
	v_fma_f32 v68, -v1, v2, 1.0
	v_fmac_f32_e32 v2, v68, v2
	v_div_scale_f32 v68, vcc, 1.0, v70, 1.0
	v_mul_f32_e32 v69, v68, v2
	v_fma_f32 v72, -v1, v69, v68
	v_fmac_f32_e32 v69, v72, v2
	v_fma_f32 v1, -v1, v69, v68
	v_div_fmas_f32 v1, v1, v2, v69
	v_div_fixup_f32 v222, v1, v70, 1.0
	v_div_scale_f32 v1, s[0:1], v71, v71, 1.0
	v_rcp_f32_e32 v2, v1
	s_nop 0
	v_fma_f32 v68, -v1, v2, 1.0
	v_fmac_f32_e32 v2, v68, v2
	v_div_scale_f32 v68, vcc, 1.0, v71, 1.0
	v_mul_f32_e32 v69, v68, v2
	v_fma_f32 v70, -v1, v69, v68
	v_fmac_f32_e32 v69, v70, v2
	v_fma_f32 v1, -v1, v69, v68
	v_div_fmas_f32 v1, v1, v2, v69
	v_div_fixup_f32 v224, v1, v71, 1.0
	ds_read_b128 v[68:71], v187 offset:96
	s_waitcnt lgkmcnt(0)
	s_barrier
; __device__ __forceinline__ int crow(int r, int hi) { return (r & 3) + 8 * (r >> 2) + 4 * hi; }
; #define INP(k) launder_p(args.in[k])
; template <bool MOBA>
; __device__ __forceinline__ void run_unit(const UnitDesc& U, LAS unsigned char* lds, f32x16 (&o)[4], float (&rli)[16]) {
;     ...
;     for (int r = 0; r < 16; ++r) rli[r] = 1.0f / li_l[crow(r, hi)];
;     __syncthreads();
; __global__ void __launch_bounds__(NWAVES * 64, 2) mega_fwd(Args args) {
;     ...
;                         int lane_p = threadIdx.x & 63; asm volatile("" : "+v"(lane_p)); const int r32 = lane_p & 31, hi = lane_p >> 5;
;                         float* sp = S1 + (size_t)(wave * 64 + lane_p) * 64;
;                         if (mp == 0) {
; #pragma unroll
;                             for (int r = 0; r < 16; ++r) *(f32x4*)(sp + r * 4) = (f32x4){o[0][r], o[1][r], o[2][r], o[3][r]} * rli[r];
;                         } else {
;                             const float* q1 = INP(6) + l * 128; const float* k1 = INP(7) + l * 128; const float* q2 = INP(8) + l * 128; const float* k2 = INP(9) + l * 128;
;                             const float s1 = wave_sum(q1[lane_p] * k1[lane_p] + q1[lane_p + 64] * k1[lane_p + 64]), s2 = wave_sum(q2[lane_p] * k2[lane_p] + q2[lane_p + 64] * k2[lane_p + 64]);
;                             const float lam = expf(s1) - expf(s2) + lam_init;
;                             asm volatile("s_waitcnt vmcnt(0)" ::: "memory");
	v_div_scale_f32 v1, s[0:1], v68, v68, 1.0
	v_rcp_f32_e32 v2, v1
	s_nop 0
	v_fma_f32 v72, -v1, v2, 1.0
	v_fmac_f32_e32 v2, v72, v2
	v_div_scale_f32 v72, vcc, 1.0, v68, 1.0
	v_mul_f32_e32 v73, v72, v2
	v_fma_f32 v74, -v1, v73, v72
	v_fmac_f32_e32 v73, v74, v2
	v_fma_f32 v1, -v1, v73, v72
	v_div_fmas_f32 v1, v1, v2, v73
	v_div_fixup_f32 v226, v1, v68, 1.0
	v_div_scale_f32 v1, s[0:1], v69, v69, 1.0
	v_rcp_f32_e32 v2, v1
	s_nop 0
	v_fma_f32 v68, -v1, v2, 1.0
	v_fmac_f32_e32 v2, v68, v2
	v_div_scale_f32 v68, vcc, 1.0, v69, 1.0
	v_mul_f32_e32 v72, v68, v2
	v_fma_f32 v73, -v1, v72, v68
	v_fmac_f32_e32 v72, v73, v2
	v_fma_f32 v1, -v1, v72, v68
	v_div_fmas_f32 v1, v1, v2, v72
	v_div_fixup_f32 v228, v1, v69, 1.0
	v_div_scale_f32 v1, s[0:1], v70, v70, 1.0
	v_rcp_f32_e32 v2, v1
	s_nop 0
	v_fma_f32 v68, -v1, v2, 1.0
	v_fmac_f32_e32 v2, v68, v2
	v_div_scale_f32 v68, vcc, 1.0, v70, 1.0
	v_mul_f32_e32 v69, v68, v2
	v_fma_f32 v72, -v1, v69, v68
	v_fmac_f32_e32 v69, v72, v2
	v_fma_f32 v1, -v1, v69, v68
	v_div_fmas_f32 v1, v1, v2, v69
	v_div_fixup_f32 v230, v1, v70, 1.0
	v_div_scale_f32 v1, s[0:1], v71, v71, 1.0
	v_rcp_f32_e32 v2, v1
	v_readlane_b32 s0, v254, 32
	v_fma_f32 v68, -v1, v2, 1.0
	v_fmac_f32_e32 v2, v68, v2
	v_div_scale_f32 v68, vcc, 1.0, v71, 1.0
	v_mul_f32_e32 v69, v68, v2
	v_fma_f32 v70, -v1, v69, v68
	v_fmac_f32_e32 v69, v70, v2
	v_fma_f32 v1, -v1, v69, v68
	v_mov_b32_e32 v68, s0
	v_lshlrev_b32_e32 v68, 8, v68
	v_lshl_add_u32 v68, v238, 4, v68
	v_add_u32_e32 v68, 0x1000, v68
	v_div_fmas_f32 v1, v1, v2, v69
	v_ashrrev_i32_e32 v69, 31, v68
	v_readlane_b32 s0, v254, 26
	v_div_fixup_f32 v232, v1, v71, 1.0
	v_lshlrev_b64 v[70:71], 0, v[68:69]
	v_readlane_b32 s1, v254, 27
	s_nop 1
	v_lshl_add_u64 v[234:235], s[0:1], 0, v[70:71]
	s_mov_b64 s[0:1], -1
	s_cbranch_scc1 .LBB0_854
	s_mov_b32 s85, 0xffff0000
	s_andn2_b64 vcc, exec, s[0:1]
	s_cbranch_vccnz .LBB0_799
	s_branch .LBB0_1115
.LBB0_854:
	v_readlane_b32 s8, v252, 14
	v_readlane_b32 s9, v252, 15
	v_readlane_b32 s10, v252, 16
	v_readlane_b32 s11, v252, 17
	v_readlane_b32 s12, v252, 18
	v_readlane_b32 s13, v252, 19
	v_readlane_b32 s14, v252, 20
	v_readlane_b32 s15, v252, 21
	v_readlane_b32 s16, v252, 22
	v_readlane_b32 s17, v252, 23
	v_readlane_b32 s18, v252, 24
	v_readlane_b32 s19, v252, 25
	v_readlane_b32 s20, v252, 26
	v_readlane_b32 s21, v252, 27
	v_readlane_b32 s22, v252, 28
	v_readlane_b32 s23, v252, 29
	s_mov_b64 s[8:9], s[12:13]
	s_mov_b64 s[10:11], s[14:15]
	s_mov_b64 s[12:13], s[16:17]
	s_mov_b64 s[14:15], s[18:19]
	s_mov_b64 s[16:17], s[20:21]
	s_mov_b64 s[0:1], s[16:17]
	v_readlane_b32 s28, v254, 39
	s_mov_b64 s[18:19], s[22:23]
	v_readlane_b32 s29, v254, 40
	s_add_u32 s8, s0, s28
	s_addc_u32 s9, s1, s29
	s_mov_b64 s[0:1], s[18:19]
	s_add_u32 s10, s0, s28
	v_readlane_b32 s12, v252, 35
	v_ashrrev_i32_e32 v239, 31, v238
	v_lshrrev_b64 v[132:133], 2, v[68:69]
	s_addc_u32 s11, s1, s29
	v_readlane_b32 s13, v252, 36
	v_readlane_b32 s14, v252, 37
	v_readlane_b32 s15, v252, 38
	v_lshlrev_b64 v[68:69], 2, v[238:239]
	s_mov_b64 s[0:1], s[12:13]
	s_mov_b64 s[6:7], s[14:15]
	v_lshl_add_u64 v[70:71], s[8:9], 0, v[68:69]
	v_lshl_add_u64 v[74:75], s[10:11], 0, v[68:69]
	global_load_dword v72, v[70:71], off
	global_load_dword v76, v[74:75], off
	global_load_dword v73, v[70:71], off offset:256
	global_load_dword v77, v[74:75], off offset:256
	v_and_b32_e32 v1, 64, v229
	s_add_u32 s0, s0, s28
	s_addc_u32 s1, s1, s29
	s_add_u32 s6, s6, s28
	s_addc_u32 s7, s7, s29
	s_mov_b32 s2, 0x42b17218
	v_mov_b32_e32 v134, v36
	v_mov_b32_e32 v135, v20
	v_readlane_b32 s16, v252, 39
	v_readlane_b32 s17, v252, 40
	v_readlane_b32 s18, v252, 41
	v_readlane_b32 s19, v252, 42
	v_readlane_b32 s20, v252, 43
	v_readlane_b32 s21, v252, 44
	v_readlane_b32 s22, v252, 45
	v_readlane_b32 s23, v252, 46
	v_readlane_b32 s24, v252, 47
	v_readlane_b32 s25, v252, 48
	v_readlane_b32 s26, v252, 49
	v_readlane_b32 s27, v252, 50
	s_waitcnt vmcnt(0)
	v_pk_mul_f32 v[70:71], v[72:73], v[76:77]
	s_nop 0
	v_add_f32_e32 v2, v70, v71
	v_add_u32_e32 v70, 64, v1
	v_xor_b32_e32 v1, 1, v229
	v_cmp_lt_i32_e32 vcc, v1, v70
	s_nop 1
	v_cndmask_b32_e32 v1, v229, v1, vcc
	v_lshlrev_b32_e32 v1, 2, v1
	ds_bpermute_b32 v71, v1, v2
	s_waitcnt lgkmcnt(0)
	v_add_f32_e32 v2, v2, v71
	v_xor_b32_e32 v71, 2, v229
	v_cmp_lt_i32_e32 vcc, v71, v70
	s_nop 1
	v_cndmask_b32_e32 v71, v229, v71, vcc
	v_lshlrev_b32_e32 v246, 2, v71
	ds_bpermute_b32 v71, v246, v2
	s_waitcnt lgkmcnt(0)
	v_add_f32_e32 v2, v2, v71
	v_xor_b32_e32 v71, 4, v229
	v_cmp_lt_i32_e32 vcc, v71, v70
	s_nop 1
	v_cndmask_b32_e32 v71, v229, v71, vcc
	v_lshlrev_b32_e32 v247, 2, v71
	ds_bpermute_b32 v71, v247, v2
	s_waitcnt lgkmcnt(0)
	v_add_f32_e32 v2, v2, v71
	v_xor_b32_e32 v71, 8, v229
	v_cmp_lt_i32_e32 vcc, v71, v70
	s_nop 1
	v_cndmask_b32_e32 v71, v229, v71, vcc
	v_lshlrev_b32_e32 v248, 2, v71
	ds_bpermute_b32 v71, v248, v2
	s_waitcnt lgkmcnt(0)
	v_add_f32_e32 v2, v2, v71
	v_xor_b32_e32 v71, 16, v229
	v_cmp_lt_i32_e32 vcc, v71, v70
	s_nop 1
	v_cndmask_b32_e32 v71, v229, v71, vcc
	v_lshlrev_b32_e32 v249, 2, v71
	ds_bpermute_b32 v71, v249, v2
	s_waitcnt lgkmcnt(0)
	v_add_f32_e32 v2, v2, v71
	v_xor_b32_e32 v71, 32, v229
	v_cmp_lt_i32_e32 vcc, v71, v70
	s_nop 1
	v_cndmask_b32_e32 v70, v229, v71, vcc
	v_lshlrev_b32_e32 v76, 2, v70
	ds_bpermute_b32 v70, v76, v2
	s_waitcnt lgkmcnt(0)
	v_add_f32_e32 v2, v2, v70
	v_lshl_add_u64 v[70:71], s[0:1], 0, v[68:69]
	v_lshl_add_u64 v[68:69], s[6:7], 0, v[68:69]
	global_load_dword v72, v[70:71], off
	global_load_dword v74, v[68:69], off
	global_load_dword v73, v[70:71], off offset:256
	global_load_dword v75, v[68:69], off offset:256
	s_mov_b32 s0, 0x3fb8aa3b
	s_mov_b32 s1, 0xc2ce8ed0
	v_cmp_ngt_f32_e32 vcc, s1, v2
	s_waitcnt vmcnt(0)
; #define INP(k) launder_p(args.in[k])
; __global__ void __launch_bounds__(NWAVES * 64, 2) mega_fwd(Args args) {
;     ...
;                             const float* q1 = INP(6) + l * 128; const float* k1 = INP(7) + l * 128; const float* q2 = INP(8) + l * 128; const float* k2 = INP(9) + l * 128;
;                             const float s1 = wave_sum(q1[lane_p] * k1[lane_p] + q1[lane_p + 64] * k1[lane_p + 64]), s2 = wave_sum(q2[lane_p] * k2[lane_p] + q2[lane_p + 64] * k2[lane_p + 64]);
;                             const float lam = expf(s1) - expf(s2) + lam_init;
;                             asm volatile("s_waitcnt vmcnt(0)" ::: "memory");
;                             { f32x4 t[16];
; #pragma unroll
;                               for (int r = 0; r < 16; ++r) t[r] = *(const f32x4*)(sp + r * 4);
;                               asm volatile("" ::: "memory");
; #pragma unroll
;                               for (int r = 0; r < 16; ++r) { const float a_ = lam * rli[r];
; #pragma unroll
;                                   for (int d0 = 0; d0 < 4; ++d0) o[d0][r] = t[r][d0] - a_ * o[d0][r]; } }
	v_readlane_b32 s6, v253, 50
	v_readlane_b32 s7, v253, 51
	s_waitcnt vmcnt(0)
	v_pk_mul_f32 v[68:69], v[72:73], v[74:75]
	s_nop 0
	v_add_f32_e32 v68, v68, v69
	ds_bpermute_b32 v69, v1, v68
	s_waitcnt lgkmcnt(0)
	v_add_f32_e32 v68, v68, v69
	ds_bpermute_b32 v69, v246, v68
	s_waitcnt lgkmcnt(0)
	v_add_f32_e32 v68, v68, v69
	ds_bpermute_b32 v69, v247, v68
	s_waitcnt lgkmcnt(0)
	v_add_f32_e32 v68, v68, v69
	ds_bpermute_b32 v69, v248, v68
	s_waitcnt lgkmcnt(0)
	v_add_f32_e32 v68, v68, v69
	ds_bpermute_b32 v69, v249, v68
	s_waitcnt lgkmcnt(0)
	v_add_f32_e32 v68, v68, v69
	ds_bpermute_b32 v69, v76, v68
	s_waitcnt lgkmcnt(0)
	v_add_f32_e32 v68, v68, v69
	v_mul_f32_e32 v69, 0x3fb8aa3b, v2
	v_fma_f32 v70, v2, s0, -v69
	v_rndne_f32_e32 v71, v69
	v_fmac_f32_e32 v70, 0x32a5705f, v2
	v_sub_f32_e32 v69, v69, v71
	v_add_f32_e32 v69, v69, v70
	v_exp_f32_e32 v69, v69
	v_cvt_i32_f32_e32 v70, v71
	v_ldexp_f32 v69, v69, v70
	v_cndmask_b32_e32 v69, 0, v69, vcc
	v_cmp_nlt_f32_e32 vcc, s2, v2
	s_nop 1
	v_cndmask_b32_e32 v2, v243, v69, vcc
	v_mul_f32_e32 v69, 0x3fb8aa3b, v68
	v_fma_f32 v70, v68, s0, -v69
	v_rndne_f32_e32 v71, v69
	v_fmac_f32_e32 v70, 0x32a5705f, v68
	v_sub_f32_e32 v69, v69, v71
	v_add_f32_e32 v69, v69, v70
	v_exp_f32_e32 v69, v69
	v_cvt_i32_f32_e32 v70, v71
	v_cmp_ngt_f32_e32 vcc, s1, v68
	v_readlane_b32 s0, v254, 28
	v_readlane_b32 s1, v254, 29
	v_ldexp_f32 v69, v69, v70
	v_cndmask_b32_e32 v69, 0, v69, vcc
	v_cmp_nlt_f32_e32 vcc, s2, v68
	v_lshl_add_u64 v[236:237], v[132:133], 2, s[0:1]
	s_mov_b64 s[0:1], -1
	v_cndmask_b32_e32 v68, v243, v69, vcc
	v_sub_f32_e32 v2, v2, v68
	global_load_dwordx4 v[80:83], v[234:235], off offset:-1024
	global_load_dwordx4 v[76:79], v[234:235], off offset:-2048
	global_load_dwordx4 v[72:75], v[234:235], off offset:-3072
	global_load_dwordx4 v[68:71], v[234:235], off offset:-4096
	global_load_dwordx4 v[96:99], v[234:235], off offset:3072
	global_load_dwordx4 v[92:95], v[234:235], off offset:2048
	global_load_dwordx4 v[88:91], v[234:235], off offset:1024
	global_load_dwordx4 v[84:87], v[234:235], off
	s_mov_b64 s[100:101], 0x2000
	v_lshl_add_u64 v[234:235], v[234:235], 0, s[100:101]
	global_load_dwordx4 v[112:115], v[234:235], off offset:-1024
	global_load_dwordx4 v[108:111], v[234:235], off offset:-2048
	global_load_dwordx4 v[104:107], v[234:235], off offset:-3072
	global_load_dwordx4 v[100:103], v[234:235], off offset:-4096
	global_load_dwordx4 v[128:131], v[234:235], off offset:3072
	global_load_dwordx4 v[124:127], v[234:235], off offset:2048
	global_load_dwordx4 v[120:123], v[234:235], off offset:1024
	global_load_dwordx4 v[116:119], v[234:235], off
	s_mov_b32 s100, 0xffffe000
	s_mov_b32 s101, -1
	v_lshl_add_u64 v[234:235], v[234:235], 0, s[100:101]
	v_add_f32_e32 v136, v203, v2
	v_mul_f32_e32 v2, v136, v202
	s_and_b64 vcc, exec, s[6:7]
	s_waitcnt vmcnt(12)
	v_pk_fma_f32 v[68:69], v[2:3], v[134:135], v[68:69] op_sel_hi:[0,1,1] neg_lo:[1,0,0] neg_hi:[1,0,0]
	v_mov_b32_e32 v134, v52
	v_mov_b32_e32 v135, v4
	v_pk_fma_f32 v[70:71], v[2:3], v[134:135], v[70:71] op_sel_hi:[0,1,1] neg_lo:[1,0,0] neg_hi:[1,0,0]
	v_mul_f32_e32 v2, v136, v204
	v_mov_b32_e32 v134, v37
	v_mov_b32_e32 v135, v21
	v_pk_fma_f32 v[72:73], v[2:3], v[134:135], v[72:73] op_sel_hi:[0,1,1] neg_lo:[1,0,0] neg_hi:[1,0,0]
	v_mov_b32_e32 v134, v53
	v_mov_b32_e32 v135, v5
	v_pk_fma_f32 v[74:75], v[2:3], v[134:135], v[74:75] op_sel_hi:[0,1,1] neg_lo:[1,0,0] neg_hi:[1,0,0]
	v_mul_f32_e32 v2, v136, v206
	v_mov_b32_e32 v134, v38
	v_mov_b32_e32 v135, v22
	v_pk_fma_f32 v[76:77], v[2:3], v[134:135], v[76:77] op_sel_hi:[0,1,1] neg_lo:[1,0,0] neg_hi:[1,0,0]
	v_mov_b32_e32 v134, v54
	v_mov_b32_e32 v135, v6
	v_pk_fma_f32 v[78:79], v[2:3], v[134:135], v[78:79] op_sel_hi:[0,1,1] neg_lo:[1,0,0] neg_hi:[1,0,0]
	v_mul_f32_e32 v2, v136, v208
	v_mov_b32_e32 v134, v39
	v_mov_b32_e32 v135, v23
	v_pk_fma_f32 v[80:81], v[2:3], v[134:135], v[80:81] op_sel_hi:[0,1,1] neg_lo:[1,0,0] neg_hi:[1,0,0]
	v_mov_b32_e32 v134, v55
	v_mov_b32_e32 v135, v7
	v_pk_fma_f32 v[82:83], v[2:3], v[134:135], v[82:83] op_sel_hi:[0,1,1] neg_lo:[1,0,0] neg_hi:[1,0,0]
	v_mul_f32_e32 v2, v136, v210
	v_mov_b32_e32 v134, v40
	v_mov_b32_e32 v135, v24
	s_waitcnt vmcnt(8)
	v_pk_fma_f32 v[84:85], v[2:3], v[134:135], v[84:85] op_sel_hi:[0,1,1] neg_lo:[1,0,0] neg_hi:[1,0,0]
	v_mov_b32_e32 v134, v56
	v_mov_b32_e32 v135, v8
	v_pk_fma_f32 v[86:87], v[2:3], v[134:135], v[86:87] op_sel_hi:[0,1,1] neg_lo:[1,0,0] neg_hi:[1,0,0]
	v_mul_f32_e32 v2, v136, v212
	v_mov_b32_e32 v134, v41
	v_mov_b32_e32 v135, v25
	v_pk_fma_f32 v[88:89], v[2:3], v[134:135], v[88:89] op_sel_hi:[0,1,1] neg_lo:[1,0,0] neg_hi:[1,0,0]
	v_mov_b32_e32 v134, v57
	v_mov_b32_e32 v135, v9
	v_pk_fma_f32 v[90:91], v[2:3], v[134:135], v[90:91] op_sel_hi:[0,1,1] neg_lo:[1,0,0] neg_hi:[1,0,0]
	v_mul_f32_e32 v2, v136, v214
	v_mov_b32_e32 v134, v42
	v_mov_b32_e32 v135, v26
	v_pk_fma_f32 v[92:93], v[2:3], v[134:135], v[92:93] op_sel_hi:[0,1,1] neg_lo:[1,0,0] neg_hi:[1,0,0]
	v_mov_b32_e32 v134, v58
	v_mov_b32_e32 v135, v10
	v_pk_fma_f32 v[94:95], v[2:3], v[134:135], v[94:95] op_sel_hi:[0,1,1] neg_lo:[1,0,0] neg_hi:[1,0,0]
	v_mul_f32_e32 v2, v136, v216
	v_mov_b32_e32 v134, v43
	v_mov_b32_e32 v135, v27
	v_pk_fma_f32 v[96:97], v[2:3], v[134:135], v[96:97] op_sel_hi:[0,1,1] neg_lo:[1,0,0] neg_hi:[1,0,0]
	v_mov_b32_e32 v134, v59
	v_mov_b32_e32 v135, v11
	v_pk_fma_f32 v[98:99], v[2:3], v[134:135], v[98:99] op_sel_hi:[0,1,1] neg_lo:[1,0,0] neg_hi:[1,0,0]
	v_mul_f32_e32 v2, v136, v218
	v_mov_b32_e32 v134, v44
	v_mov_b32_e32 v135, v28
	s_waitcnt vmcnt(4)
; #define INP(k) launder_p(args.in[k])
; __global__ void __launch_bounds__(NWAVES * 64, 2) mega_fwd(Args args) {
;     ...
;                               for (int r = 0; r < 16; ++r) { const float a_ = lam * rli[r];
; #pragma unroll
;                                   for (int d0 = 0; d0 < 4; ++d0) o[d0][r] = t[r][d0] - a_ * o[d0][r]; } }
;                             float* sq = S2 + (size_t)(wave * 64 + lane_p) * 64;
;                             if (vh == 0) {
; #pragma unroll
;                                 for (int r = 0; r < 16; ++r) *(f32x4*)(sq + r * 4) = (f32x4){o[0][r], o[1][r], o[2][r], o[3][r]};
;                             } else { const float* subg = INP(10) + l * 256;
;                                 asm volatile("s_waitcnt vmcnt(0)" ::: "memory");
;                                 float sg[8];
; #pragma unroll
;                                 for (int i = 0; i < 8; ++i) sg[i] = subg[(i >> 2) * 128 + (i & 3) * 32 + r32];
;                                 { f32x4 t[16];
; #pragma unroll
;                                   for (int r = 0; r < 16; ++r) t[r] = *(const f32x4*)(sq + r * 4);
;                                   asm volatile("" ::: "memory");
; #pragma unroll
	v_pk_fma_f32 v[100:101], v[2:3], v[134:135], v[100:101] op_sel_hi:[0,1,1] neg_lo:[1,0,0] neg_hi:[1,0,0]
	v_mov_b32_e32 v134, v60
	v_mov_b32_e32 v135, v12
	v_pk_fma_f32 v[102:103], v[2:3], v[134:135], v[102:103] op_sel_hi:[0,1,1] neg_lo:[1,0,0] neg_hi:[1,0,0]
	v_mul_f32_e32 v2, v136, v220
	v_mov_b32_e32 v134, v45
	v_mov_b32_e32 v135, v29
	v_pk_fma_f32 v[104:105], v[2:3], v[134:135], v[104:105] op_sel_hi:[0,1,1] neg_lo:[1,0,0] neg_hi:[1,0,0]
	v_mov_b32_e32 v134, v61
	v_mov_b32_e32 v135, v13
	v_pk_fma_f32 v[106:107], v[2:3], v[134:135], v[106:107] op_sel_hi:[0,1,1] neg_lo:[1,0,0] neg_hi:[1,0,0]
	v_mul_f32_e32 v2, v136, v222
	v_mov_b32_e32 v134, v46
	v_mov_b32_e32 v135, v30
	v_pk_fma_f32 v[108:109], v[2:3], v[134:135], v[108:109] op_sel_hi:[0,1,1] neg_lo:[1,0,0] neg_hi:[1,0,0]
	v_mov_b32_e32 v134, v62
	v_mov_b32_e32 v135, v14
	v_pk_fma_f32 v[110:111], v[2:3], v[134:135], v[110:111] op_sel_hi:[0,1,1] neg_lo:[1,0,0] neg_hi:[1,0,0]
	v_mul_f32_e32 v2, v136, v224
	v_mov_b32_e32 v134, v47
	v_mov_b32_e32 v135, v31
	v_pk_fma_f32 v[112:113], v[2:3], v[134:135], v[112:113] op_sel_hi:[0,1,1] neg_lo:[1,0,0] neg_hi:[1,0,0]
	v_mov_b32_e32 v134, v63
	v_mov_b32_e32 v135, v15
	v_pk_fma_f32 v[114:115], v[2:3], v[134:135], v[114:115] op_sel_hi:[0,1,1] neg_lo:[1,0,0] neg_hi:[1,0,0]
	v_mul_f32_e32 v2, v136, v226
	v_mov_b32_e32 v134, v48
	v_mov_b32_e32 v135, v32
	s_waitcnt vmcnt(0)
	v_pk_fma_f32 v[116:117], v[2:3], v[134:135], v[116:117] op_sel_hi:[0,1,1] neg_lo:[1,0,0] neg_hi:[1,0,0]
	v_mov_b32_e32 v134, v64
	v_mov_b32_e32 v135, v16
	v_pk_fma_f32 v[118:119], v[2:3], v[134:135], v[118:119] op_sel_hi:[0,1,1] neg_lo:[1,0,0] neg_hi:[1,0,0]
	v_mul_f32_e32 v2, v136, v228
	v_mov_b32_e32 v134, v49
	v_mov_b32_e32 v135, v33
	v_pk_fma_f32 v[120:121], v[2:3], v[134:135], v[120:121] op_sel_hi:[0,1,1] neg_lo:[1,0,0] neg_hi:[1,0,0]
	v_mov_b32_e32 v134, v65
	v_mov_b32_e32 v135, v17
	v_pk_fma_f32 v[122:123], v[2:3], v[134:135], v[122:123] op_sel_hi:[0,1,1] neg_lo:[1,0,0] neg_hi:[1,0,0]
	v_mul_f32_e32 v2, v136, v230
	v_mov_b32_e32 v134, v50
	v_mov_b32_e32 v135, v34
	v_pk_fma_f32 v[124:125], v[2:3], v[134:135], v[124:125] op_sel_hi:[0,1,1] neg_lo:[1,0,0] neg_hi:[1,0,0]
	v_mov_b32_e32 v134, v66
	v_mov_b32_e32 v135, v18
	v_pk_fma_f32 v[126:127], v[2:3], v[134:135], v[126:127] op_sel_hi:[0,1,1] neg_lo:[1,0,0] neg_hi:[1,0,0]
	v_mul_f32_e32 v2, v136, v232
	v_mov_b32_e32 v134, v51
	v_mov_b32_e32 v135, v35
	v_pk_fma_f32 v[128:129], v[2:3], v[134:135], v[128:129] op_sel_hi:[0,1,1] neg_lo:[1,0,0] neg_hi:[1,0,0]
	v_mov_b32_e32 v134, v67
	v_mov_b32_e32 v135, v19
	v_pk_fma_f32 v[130:131], v[2:3], v[134:135], v[130:131] op_sel_hi:[0,1,1] neg_lo:[1,0,0] neg_hi:[1,0,0]
	s_cbranch_vccz .LBB0_1112
	v_readlane_b32 s8, v252, 35
	v_readlane_b32 s12, v252, 39
	v_readlane_b32 s13, v252, 40
	s_mov_b64 s[0:1], s[12:13]
	v_readlane_b32 s6, v254, 41
	v_and_b32_e32 v2, 31, v238
	v_readlane_b32 s7, v254, 42
	s_add_u32 s0, s0, s6
	s_addc_u32 s1, s1, s7
	s_waitcnt vmcnt(0)
	v_lshlrev_b32_e32 v132, 2, v2
	global_load_dword v245, v132, s[0:1]
	global_load_dword v244, v132, s[0:1] offset:128
	global_load_dword v239, v132, s[0:1] offset:256
	global_load_dword v217, v132, s[0:1] offset:384
	global_load_dword v213, v132, s[0:1] offset:512
	global_load_dword v211, v132, s[0:1] offset:640
	global_load_dword v209, v132, s[0:1] offset:768
	global_load_dword v197, v132, s[0:1] offset:896
	global_load_dwordx4 v[180:183], v[236:237], off offset:-1024
	global_load_dwordx4 v[184:187], v[236:237], off offset:-2048
	global_load_dwordx4 v[188:191], v[236:237], off offset:-3072
	global_load_dwordx4 v[192:195], v[236:237], off offset:-4096
	global_load_dwordx4 v[164:167], v[236:237], off offset:3072
	global_load_dwordx4 v[168:171], v[236:237], off offset:2048
	global_load_dwordx4 v[172:175], v[236:237], off offset:1024
	global_load_dwordx4 v[176:179], v[236:237], off
	s_mov_b64 s[100:101], 0x2000
	v_lshl_add_u64 v[236:237], v[236:237], 0, s[100:101]
	global_load_dwordx4 v[148:151], v[236:237], off offset:-1024
	global_load_dwordx4 v[152:155], v[236:237], off offset:-2048
	global_load_dwordx4 v[156:159], v[236:237], off offset:-3072
	global_load_dwordx4 v[160:163], v[236:237], off offset:-4096
	global_load_dwordx4 v[132:135], v[236:237], off offset:3072
	global_load_dwordx4 v[136:139], v[236:237], off offset:2048
	global_load_dwordx4 v[140:143], v[236:237], off offset:1024
	global_load_dwordx4 v[144:147], v[236:237], off
	s_mov_b32 s100, 0xffffe000
	s_mov_b32 s101, -1
	v_lshl_add_u64 v[236:237], v[236:237], 0, s[100:101]
	v_pk_mul_f32 v[250:251], v[68:69], v[68:69]
	v_readlane_b32 s11, v252, 38
	v_readlane_b32 s0, v254, 48
	v_readlane_b32 s11, v254, 24
	s_mov_b32 s8, 0xe800
	v_readlane_b32 s10, v252, 37
	s_mov_b64 s[12:13], 0x3800
	s_movk_i32 s10, 0x3000
	v_lshlrev_b32_e32 v2, 1, v2
	v_readlane_b32 s9, v252, 36
	v_readlane_b32 s14, v252, 41
	v_readlane_b32 s15, v252, 42
	v_readlane_b32 s16, v252, 43
	v_readlane_b32 s17, v252, 44
	v_readlane_b32 s18, v252, 45
	v_readlane_b32 s19, v252, 46
	v_readlane_b32 s20, v252, 47
	v_readlane_b32 s21, v252, 48
	v_readlane_b32 s22, v252, 49
	v_readlane_b32 s23, v252, 50
	s_waitcnt vmcnt(12)
	v_fma_f32 v192, v192, v192, v250
	v_fmac_f32_e32 v251, v193, v193
	v_add_f32_e32 v215, v192, v251
	v_pk_mul_f32 v[192:193], v[70:71], v[70:71]
	s_nop 0
	v_fma_f32 v192, v194, v194, v192
	v_add_f32_e32 v192, v215, v192
	v_fmac_f32_e32 v193, v195, v195
	v_add_f32_e32 v192, v192, v193
	ds_bpermute_b32 v193, v1, v192
	s_waitcnt lgkmcnt(0)
	v_add_f32_e32 v192, v192, v193
	ds_bpermute_b32 v193, v246, v192
	s_waitcnt lgkmcnt(0)
	v_add_f32_e32 v192, v192, v193
	ds_bpermute_b32 v193, v247, v192
	s_waitcnt lgkmcnt(0)
; __global__ void __launch_bounds__(NWAVES * 64, 2) mega_fwd(Args args) {
;     ...
;                                   for (int r = 0; r < 16; ++r) { float ssq = 0.f;
; #pragma unroll
;                                       for (int d0 = 0; d0 < 4; ++d0) ssq += t[r][d0] * t[r][d0] + o[d0][r] * o[d0][r];
; #pragma unroll
;                                       for (int off = 1; off < 32; off <<= 1) ssq += __shfl_xor(ssq, off);
;                                       rli[r] = __builtin_amdgcn_rsqf(ssq * (1.0f / 256.0f) + RMS_EPS) * (1.0f - lam_init); } }
	v_add_f32_e32 v192, v192, v193
	ds_bpermute_b32 v193, v248, v192
	s_waitcnt lgkmcnt(0)
	v_add_f32_e32 v192, v192, v193
	ds_bpermute_b32 v193, v249, v192
	s_waitcnt lgkmcnt(0)
	v_add_f32_e32 v192, v192, v193
	v_fmamk_f32 v192, v192, 0x3b800000, v221
	v_rsq_f32_e32 v192, v192
	s_nop 0
	v_mul_f32_e32 v215, v205, v192
	v_pk_mul_f32 v[192:193], v[72:73], v[72:73]
	s_nop 0
	v_fma_f32 v188, v188, v188, v192
	v_fmac_f32_e32 v193, v189, v189
	v_add_f32_e32 v192, v188, v193
	v_pk_mul_f32 v[188:189], v[74:75], v[74:75]
	s_nop 0
	v_fma_f32 v188, v190, v190, v188
	v_add_f32_e32 v188, v192, v188
	v_fmac_f32_e32 v189, v191, v191
	v_add_f32_e32 v188, v188, v189
	ds_bpermute_b32 v189, v1, v188
	s_waitcnt lgkmcnt(0)
	v_add_f32_e32 v188, v188, v189
	ds_bpermute_b32 v189, v246, v188
	s_waitcnt lgkmcnt(0)
	v_add_f32_e32 v188, v188, v189
	ds_bpermute_b32 v189, v247, v188
	s_waitcnt lgkmcnt(0)
	v_add_f32_e32 v188, v188, v189
	ds_bpermute_b32 v189, v248, v188
	s_waitcnt lgkmcnt(0)
	v_add_f32_e32 v251, v188, v189
	v_pk_mul_f32 v[188:189], v[76:77], v[76:77]
	ds_bpermute_b32 v223, v249, v251
	v_fma_f32 v184, v184, v184, v188
	v_fmac_f32_e32 v189, v185, v185
	v_add_f32_e32 v188, v184, v189
	v_pk_mul_f32 v[184:185], v[78:79], v[78:79]
	s_nop 0
	v_fma_f32 v184, v186, v186, v184
	v_add_f32_e32 v184, v188, v184
	v_fmac_f32_e32 v185, v187, v187
	v_add_f32_e32 v184, v184, v185
	ds_bpermute_b32 v185, v1, v184
	s_waitcnt lgkmcnt(0)
	v_add_f32_e32 v184, v184, v185
	ds_bpermute_b32 v185, v246, v184
	s_waitcnt lgkmcnt(0)
	v_add_f32_e32 v184, v184, v185
	ds_bpermute_b32 v185, v247, v184
	s_waitcnt lgkmcnt(0)
	v_add_f32_e32 v184, v184, v185
	ds_bpermute_b32 v185, v248, v184
	s_waitcnt lgkmcnt(0)
	v_add_f32_e32 v189, v184, v185
	v_pk_mul_f32 v[184:185], v[80:81], v[80:81]
	ds_bpermute_b32 v191, v249, v189
	v_fma_f32 v180, v180, v180, v184
	v_fmac_f32_e32 v185, v181, v181
	v_add_f32_e32 v184, v180, v185
	v_pk_mul_f32 v[180:181], v[82:83], v[82:83]
	s_nop 0
	v_fma_f32 v180, v182, v182, v180
	v_add_f32_e32 v180, v184, v180
	v_fmac_f32_e32 v181, v183, v183
	v_add_f32_e32 v180, v180, v181
	ds_bpermute_b32 v181, v1, v180
	s_waitcnt lgkmcnt(0)
	v_add_f32_e32 v180, v180, v181
	ds_bpermute_b32 v181, v246, v180
	s_waitcnt lgkmcnt(0)
	v_add_f32_e32 v180, v180, v181
	ds_bpermute_b32 v181, v247, v180
	s_waitcnt lgkmcnt(0)
	v_add_f32_e32 v180, v180, v181
	ds_bpermute_b32 v181, v248, v180
	s_waitcnt lgkmcnt(0)
	v_add_f32_e32 v187, v180, v181
	v_pk_mul_f32 v[180:181], v[84:85], v[84:85]
	ds_bpermute_b32 v188, v249, v187
	s_waitcnt vmcnt(8)
	v_fma_f32 v176, v176, v176, v180
	v_fmac_f32_e32 v181, v177, v177
	v_add_f32_e32 v180, v176, v181
	v_pk_mul_f32 v[176:177], v[86:87], v[86:87]
	s_nop 0
	v_fma_f32 v176, v178, v178, v176
	v_add_f32_e32 v176, v180, v176
	v_fmac_f32_e32 v177, v179, v179
	v_add_f32_e32 v176, v176, v177
	ds_bpermute_b32 v177, v1, v176
	v_pk_mul_f32 v[178:179], v[88:89], v[88:89]
	s_waitcnt lgkmcnt(0)
	v_add_f32_e32 v176, v176, v177
	ds_bpermute_b32 v177, v246, v176
	v_fma_f32 v172, v172, v172, v178
	v_fmac_f32_e32 v179, v173, v173
	s_waitcnt lgkmcnt(0)
	v_add_f32_e32 v176, v176, v177
	ds_bpermute_b32 v177, v247, v176
	s_waitcnt lgkmcnt(0)
	v_add_f32_e32 v176, v176, v177
	ds_bpermute_b32 v177, v248, v176
	s_waitcnt lgkmcnt(0)
	v_add_f32_e32 v176, v176, v177
	v_add_f32_e32 v177, v172, v179
	v_pk_mul_f32 v[172:173], v[90:91], v[90:91]
	ds_bpermute_b32 v186, v249, v176
	v_fma_f32 v172, v174, v174, v172
	v_add_f32_e32 v172, v177, v172
	v_fmac_f32_e32 v173, v175, v175
	v_add_f32_e32 v172, v172, v173
	ds_bpermute_b32 v173, v1, v172
	v_pk_mul_f32 v[174:175], v[92:93], v[92:93]
	s_waitcnt lgkmcnt(0)
	v_add_f32_e32 v172, v172, v173
	ds_bpermute_b32 v173, v246, v172
	v_fma_f32 v168, v168, v168, v174
	v_fmac_f32_e32 v175, v169, v169
	s_waitcnt lgkmcnt(0)
	v_add_f32_e32 v172, v172, v173
	ds_bpermute_b32 v173, v247, v172
	s_waitcnt lgkmcnt(0)
	v_add_f32_e32 v172, v172, v173
	ds_bpermute_b32 v173, v248, v172
	s_waitcnt lgkmcnt(0)
	v_add_f32_e32 v173, v172, v173
	v_add_f32_e32 v172, v168, v175
	v_pk_mul_f32 v[168:169], v[94:95], v[94:95]
	ds_bpermute_b32 v250, v249, v173
	v_fma_f32 v168, v170, v170, v168
	v_add_f32_e32 v168, v172, v168
	v_fmac_f32_e32 v169, v171, v171
	v_add_f32_e32 v168, v168, v169
	ds_bpermute_b32 v169, v1, v168
	s_waitcnt lgkmcnt(0)
	v_add_f32_e32 v168, v168, v169
	ds_bpermute_b32 v169, v246, v168
	s_waitcnt lgkmcnt(0)
	v_add_f32_e32 v168, v168, v169
	ds_bpermute_b32 v169, v247, v168
	s_waitcnt lgkmcnt(0)
	v_add_f32_e32 v168, v168, v169
	ds_bpermute_b32 v169, v248, v168
	s_waitcnt lgkmcnt(0)
	v_add_f32_e32 v174, v168, v169
	v_pk_mul_f32 v[168:169], v[96:97], v[96:97]
	ds_bpermute_b32 v190, v249, v174
	v_fma_f32 v164, v164, v164, v168
	v_fmac_f32_e32 v169, v165, v165
	v_add_f32_e32 v168, v164, v169
	v_pk_mul_f32 v[164:165], v[98:99], v[98:99]
	s_nop 0
	v_fma_f32 v164, v166, v166, v164
	v_add_f32_e32 v164, v168, v164
	v_fmac_f32_e32 v165, v167, v167
	v_add_f32_e32 v164, v164, v165
	ds_bpermute_b32 v165, v1, v164
	s_waitcnt lgkmcnt(0)
	v_add_f32_e32 v164, v164, v165
	ds_bpermute_b32 v165, v246, v164
	s_waitcnt lgkmcnt(0)
	v_add_f32_e32 v164, v164, v165
	ds_bpermute_b32 v165, v247, v164
	s_waitcnt lgkmcnt(0)
	v_add_f32_e32 v164, v164, v165
	ds_bpermute_b32 v165, v248, v164
	s_waitcnt lgkmcnt(0)
	v_add_f32_e32 v175, v164, v165
	v_pk_mul_f32 v[164:165], v[100:101], v[100:101]
	ds_bpermute_b32 v185, v249, v175
	s_waitcnt vmcnt(4)
	v_fma_f32 v160, v160, v160, v164
	v_fmac_f32_e32 v165, v161, v161
	v_add_f32_e32 v164, v160, v165
	v_pk_mul_f32 v[160:161], v[102:103], v[102:103]
	s_nop 0
	v_fma_f32 v160, v162, v162, v160
	v_add_f32_e32 v160, v164, v160
	v_fmac_f32_e32 v161, v163, v163
	v_add_f32_e32 v160, v160, v161
	ds_bpermute_b32 v161, v1, v160
	s_waitcnt lgkmcnt(0)
; __global__ void __launch_bounds__(NWAVES * 64, 2) mega_fwd(Args args) {
;     ...
;                                   for (int r = 0; r < 16; ++r) { float ssq = 0.f;
; #pragma unroll
;                                       for (int d0 = 0; d0 < 4; ++d0) ssq += t[r][d0] * t[r][d0] + o[d0][r] * o[d0][r];
; #pragma unroll
;                                       for (int off = 1; off < 32; off <<= 1) ssq += __shfl_xor(ssq, off);
;                                       rli[r] = __builtin_amdgcn_rsqf(ssq * (1.0f / 256.0f) + RMS_EPS) * (1.0f - lam_init); } }
	v_add_f32_e32 v160, v160, v161
	ds_bpermute_b32 v161, v246, v160
	s_waitcnt lgkmcnt(0)
	v_add_f32_e32 v160, v160, v161
	ds_bpermute_b32 v161, v247, v160
	s_waitcnt lgkmcnt(0)
	v_add_f32_e32 v160, v160, v161
	ds_bpermute_b32 v161, v248, v160
	s_waitcnt lgkmcnt(0)
	v_add_f32_e32 v168, v160, v161
	v_pk_mul_f32 v[160:161], v[104:105], v[104:105]
	ds_bpermute_b32 v180, v249, v168
	v_fma_f32 v156, v156, v156, v160
	v_fmac_f32_e32 v161, v157, v157
	v_add_f32_e32 v160, v156, v161
	v_pk_mul_f32 v[156:157], v[106:107], v[106:107]
	s_nop 0
	v_fma_f32 v156, v158, v158, v156
	v_add_f32_e32 v156, v160, v156
	v_fmac_f32_e32 v157, v159, v159
	v_add_f32_e32 v156, v156, v157
	ds_bpermute_b32 v157, v1, v156
	s_waitcnt lgkmcnt(0)
	v_add_f32_e32 v156, v156, v157
	ds_bpermute_b32 v157, v246, v156
	s_waitcnt lgkmcnt(0)
	v_add_f32_e32 v156, v156, v157
	ds_bpermute_b32 v157, v247, v156
	s_waitcnt lgkmcnt(0)
	v_add_f32_e32 v156, v156, v157
	ds_bpermute_b32 v157, v248, v156
	s_waitcnt lgkmcnt(0)
	v_add_f32_e32 v177, v156, v157
	v_pk_mul_f32 v[156:157], v[108:109], v[108:109]
	ds_bpermute_b32 v184, v249, v177
	v_fma_f32 v152, v152, v152, v156
	v_fmac_f32_e32 v157, v153, v153
	v_add_f32_e32 v156, v152, v157
	v_pk_mul_f32 v[152:153], v[110:111], v[110:111]
	s_nop 0
	v_fma_f32 v152, v154, v154, v152
	v_add_f32_e32 v152, v156, v152
	v_fmac_f32_e32 v153, v155, v155
	v_add_f32_e32 v152, v152, v153
	ds_bpermute_b32 v153, v1, v152
	s_waitcnt lgkmcnt(0)
	v_add_f32_e32 v152, v152, v153
	ds_bpermute_b32 v153, v246, v152
	s_waitcnt lgkmcnt(0)
	v_add_f32_e32 v152, v152, v153
	ds_bpermute_b32 v153, v247, v152
	s_waitcnt lgkmcnt(0)
	v_add_f32_e32 v152, v152, v153
	ds_bpermute_b32 v153, v248, v152
	s_waitcnt lgkmcnt(0)
	v_add_f32_e32 v178, v152, v153
	v_pk_mul_f32 v[152:153], v[112:113], v[112:113]
	ds_bpermute_b32 v183, v249, v178
	v_fma_f32 v148, v148, v148, v152
	v_fmac_f32_e32 v153, v149, v149
	v_add_f32_e32 v152, v148, v153
	v_pk_mul_f32 v[148:149], v[114:115], v[114:115]
	s_nop 0
	v_fma_f32 v148, v150, v150, v148
	v_add_f32_e32 v148, v152, v148
	v_fmac_f32_e32 v149, v151, v151
	v_add_f32_e32 v148, v148, v149
	ds_bpermute_b32 v149, v1, v148
	s_waitcnt lgkmcnt(0)
	v_add_f32_e32 v148, v148, v149
	ds_bpermute_b32 v149, v246, v148
	s_waitcnt lgkmcnt(0)
	v_add_f32_e32 v148, v148, v149
	ds_bpermute_b32 v149, v247, v148
	s_waitcnt lgkmcnt(0)
	v_add_f32_e32 v148, v148, v149
	ds_bpermute_b32 v149, v248, v148
	s_waitcnt lgkmcnt(0)
	v_add_f32_e32 v179, v148, v149
	v_pk_mul_f32 v[148:149], v[116:117], v[116:117]
	ds_bpermute_b32 v182, v249, v179
	s_waitcnt vmcnt(0)
	v_fma_f32 v144, v144, v144, v148
	v_fmac_f32_e32 v149, v145, v145
	v_add_f32_e32 v148, v144, v149
	v_pk_mul_f32 v[144:145], v[118:119], v[118:119]
	v_mov_b32_e32 v149, v3
	v_fma_f32 v144, v146, v146, v144
	v_add_f32_e32 v144, v148, v144
	v_fmac_f32_e32 v145, v147, v147
	v_add_f32_e32 v144, v144, v145
	ds_bpermute_b32 v145, v1, v144
	s_waitcnt lgkmcnt(0)
	v_add_f32_e32 v144, v144, v145
	ds_bpermute_b32 v145, v246, v144
	s_waitcnt lgkmcnt(0)
	v_add_f32_e32 v144, v144, v145
	ds_bpermute_b32 v145, v247, v144
	s_waitcnt lgkmcnt(0)
	v_add_f32_e32 v144, v144, v145
	ds_bpermute_b32 v145, v248, v144
	s_waitcnt lgkmcnt(0)
	v_add_f32_e32 v172, v144, v145
	v_pk_mul_f32 v[144:145], v[120:121], v[120:121]
	ds_bpermute_b32 v181, v249, v172
	v_fma_f32 v140, v140, v140, v144
	v_fmac_f32_e32 v145, v141, v141
	v_add_f32_e32 v144, v140, v145
	v_pk_mul_f32 v[140:141], v[122:123], v[122:123]
	s_nop 0
	v_fma_f32 v140, v142, v142, v140
	v_add_f32_e32 v140, v144, v140
	v_fmac_f32_e32 v141, v143, v143
	v_add_f32_e32 v140, v140, v141
	ds_bpermute_b32 v141, v1, v140
	s_waitcnt lgkmcnt(0)
	v_add_f32_e32 v140, v140, v141
	ds_bpermute_b32 v141, v246, v140
	s_waitcnt lgkmcnt(0)
	v_add_f32_e32 v140, v140, v141
	ds_bpermute_b32 v141, v247, v140
	s_waitcnt lgkmcnt(0)
	v_add_f32_e32 v140, v140, v141
	ds_bpermute_b32 v141, v248, v140
	s_waitcnt lgkmcnt(0)
	v_add_f32_e32 v166, v140, v141
	v_pk_mul_f32 v[140:141], v[124:125], v[124:125]
	ds_bpermute_b32 v167, v249, v166
	v_fma_f32 v136, v136, v136, v140
	v_fmac_f32_e32 v141, v137, v137
	v_add_f32_e32 v140, v136, v141
	v_pk_mul_f32 v[136:137], v[126:127], v[126:127]
	s_nop 0
	v_fma_f32 v136, v138, v138, v136
	v_add_f32_e32 v136, v140, v136
	v_fmac_f32_e32 v137, v139, v139
	v_add_f32_e32 v136, v136, v137
	ds_bpermute_b32 v137, v1, v136
	s_waitcnt lgkmcnt(0)
	v_add_f32_e32 v136, v136, v137
	ds_bpermute_b32 v137, v246, v136
	s_waitcnt lgkmcnt(0)
	v_add_f32_e32 v136, v136, v137
	ds_bpermute_b32 v137, v247, v136
	s_waitcnt lgkmcnt(0)
; __device__ __forceinline__ float bflo(unsigned w) { return __uint_as_float(w << 16); }
; __device__ __forceinline__ float bfhi(unsigned w) { return __uint_as_float(w & 0xffff0000u); }
; __device__ __forceinline__ unsigned pk2(float lo, float hi) { return f2bf(lo) | (f2bf(hi) << 16); }
; __device__ __forceinline__ int crow(int r, int hi) { return (r & 3) + 8 * (r >> 2) + 4 * hi; }
; __global__ void __launch_bounds__(NWAVES * 64, 2) mega_fwd(Args args) {
;     ...
;                                   for (int r = 0; r < 16; ++r) { float ssq = 0.f;
; #pragma unroll
;                                       for (int d0 = 0; d0 < 4; ++d0) ssq += t[r][d0] * t[r][d0] + o[d0][r] * o[d0][r];
; #pragma unroll
;                                       for (int off = 1; off < 32; off <<= 1) ssq += __shfl_xor(ssq, off);
;                                       rli[r] = __builtin_amdgcn_rsqf(ssq * (1.0f / 256.0f) + RMS_EPS) * (1.0f - lam_init); } }
;     ...
;                                   for (int rq = 0; rq < 4; ++rq) { unsigned zz[16]; f32x4 t[4];
;                                     int wv_ = wave; asm volatile("" : "+s"(wv_));
; #pragma unroll
;                                     for (int rr = 0; rr < 4; ++rr) { const int r = rq * 4 + rr; const bf16_t* zp = PROJ + (size_t)(b * SEQ + L * 256 + wv_ * 32 + att::crow(r, hi)) * NC + C_ZB + h * 256 + hv * 128 + (r32 & ~1);
; #pragma unroll
;                                         for (int d0 = 0; d0 < 4; ++d0) zz[rr * 4 + d0] = *(const unsigned*)(zp + d0 * 32);
;                                         if (hv == 0) t[rr] = *(const f32x4*)(sq + r * 4); else t[rr] = (f32x4){o[0][r], o[1][r], o[2][r], o[3][r]}; }
;                                     asm volatile("" ::: "memory");
; #pragma unroll
;                                     for (int rr = 0; rr < 4; ++rr) { const int r = rq * 4 + rr; bf16_t* yp = Y + (size_t)(b * SEQ + L * 256 + wv_ * 32 + att::crow(r, hi)) * YS + BW + h * 256 + hv * 128 + r32;
; #pragma unroll
;                                         for (int d0 = 0; d0 < 4; ++d0) { const float val = t[rr][d0] * rli[r] * sg[hv * 4 + d0], vn = __shfl_xor(val, 1);
;                                             if ((r32 & 1) == 0) *(unsigned*)(yp + d0 * 32) = pk2(val * bflo(zz[rr * 4 + d0]), vn * bfhi(zz[rr * 4 + d0])); } } }
	v_add_f32_e32 v136, v136, v137
	ds_bpermute_b32 v137, v248, v136
	s_waitcnt lgkmcnt(0)
	v_add_f32_e32 v163, v136, v137
	v_pk_mul_f32 v[136:137], v[128:129], v[128:129]
	ds_bpermute_b32 v164, v249, v163
	v_fma_f32 v132, v132, v132, v136
	v_fmac_f32_e32 v137, v133, v133
	v_add_f32_e32 v136, v132, v137
	v_pk_mul_f32 v[132:133], v[130:131], v[130:131]
	s_nop 0
	v_fma_f32 v132, v134, v134, v132
	v_add_f32_e32 v132, v136, v132
	v_fmac_f32_e32 v133, v135, v135
	v_add_f32_e32 v132, v132, v133
	ds_bpermute_b32 v133, v1, v132
	v_and_b32_e32 v134, 30, v238
	v_lshlrev_b32_e32 v148, 1, v134
	s_waitcnt lgkmcnt(0)
	v_add_f32_e32 v132, v132, v133
	ds_bpermute_b32 v133, v246, v132
	s_waitcnt lgkmcnt(0)
	v_add_f32_e32 v132, v132, v133
	ds_bpermute_b32 v133, v247, v132
	s_waitcnt lgkmcnt(0)
	v_add_f32_e32 v132, v132, v133
	ds_bpermute_b32 v133, v248, v132
	s_waitcnt lgkmcnt(0)
	v_add_f32_e32 v160, v132, v133
	v_ashrrev_i32_e32 v132, 3, v238
	v_and_b32_e32 v132, -4, v132
	v_add_u32_e32 v162, s0, v132
	s_mov_b32 s0, s11
	v_and_b32_e32 v132, 1, v238
	v_lshl_add_u32 v156, s0, 5, v162
	v_readlane_b32 s0, v253, 48
	v_readlane_b32 s1, v253, 49
	v_cmp_eq_u32_e64 s[6:7], 0, v132
	v_or_b32_e32 v154, 1, v156
	v_mov_b64_e32 v[158:159], s[0:1]
	v_mad_i64_i32 v[132:133], s[0:1], v156, s8, v[158:159]
	v_readlane_b32 s0, v254, 49
	s_lshl_b32 s2, s0, 1
	v_lshl_add_u64 v[132:133], v[132:133], 0, s[2:3]
	v_lshl_add_u64 v[132:133], v[132:133], 0, v[148:149]
	v_mad_i64_i32 v[150:151], s[0:1], v154, s8, v[158:159]
	v_lshl_add_u64 v[134:135], v[132:133], 0, s[12:13]
	v_add_co_u32_e32 v132, vcc, s10, v132
	v_lshl_add_u64 v[150:151], v[150:151], 0, s[2:3]
	s_nop 0
	v_addc_co_u32_e32 v133, vcc, 0, v133, vcc
	v_lshl_add_u64 v[150:151], v[150:151], 0, v[148:149]
	v_lshl_add_u64 v[152:153], v[150:151], 0, s[12:13]
	v_add_co_u32_e32 v150, vcc, s10, v150
	ds_bpermute_b32 v161, v249, v160
	s_nop 0
	v_addc_co_u32_e32 v151, vcc, 0, v151, vcc
	global_load_dword v192, v[132:133], off offset:2048
	global_load_dword v233, v[134:135], off offset:64
	global_load_dword v169, v[134:135], off offset:128
	global_load_dword v155, v[134:135], off offset:192
	s_nop 0
	global_load_dwordx4 v[132:135], v[236:237], off offset:-1024
	global_load_dwordx4 v[136:139], v[236:237], off offset:-2048
	global_load_dwordx4 v[140:143], v[236:237], off offset:-3072
	global_load_dwordx4 v[144:147], v[236:237], off offset:-4096
	global_load_dword v240, v[150:151], off offset:2048
	global_load_dword v249, v[152:153], off offset:64
	global_load_dword v170, v[152:153], off offset:128
	s_nop 0
	global_load_dword v153, v[152:153], off offset:192
	v_or_b32_e32 v152, 2, v156
	v_mad_i64_i32 v[150:151], s[0:1], v152, s8, v[158:159]
	v_lshl_add_u64 v[150:151], v[150:151], 0, s[2:3]
	v_lshl_add_u64 v[150:151], v[150:151], 0, v[148:149]
	v_lshl_add_u64 v[194:195], v[150:151], 0, s[12:13]
	v_add_co_u32_e32 v150, vcc, s10, v150
	v_ashrrev_i32_e32 v157, 31, v156
	s_nop 0
	v_addc_co_u32_e32 v151, vcc, 0, v151, vcc
	global_load_dword v248, v[150:151], off offset:2048
	global_load_dword v247, v[194:195], off offset:64
	global_load_dword v171, v[194:195], off offset:128
	s_nop 0
	global_load_dword v151, v[194:195], off offset:192
	v_or_b32_e32 v150, 3, v156
	v_mad_i64_i32 v[158:159], s[0:1], v150, s8, v[158:159]
	v_lshl_add_u64 v[158:159], v[158:159], 0, s[2:3]
	v_lshl_add_u64 v[158:159], v[158:159], 0, v[148:149]
	v_lshl_add_u64 v[194:195], v[158:159], 0, s[12:13]
	v_add_co_u32_e32 v158, vcc, s10, v158
	v_lshlrev_b64 v[156:157], 13, v[156:157]
	s_nop 0
	v_addc_co_u32_e32 v159, vcc, 0, v159, vcc
	global_load_dword v246, v[158:159], off offset:2048
	global_load_dword v238, v[194:195], off offset:64
	global_load_dword v165, v[194:195], off offset:128
	global_load_dword v149, v[194:195], off offset:192
	v_lshl_add_u64 v[156:157], s[4:5], 0, v[156:157]
	v_lshl_add_u64 v[156:157], v[156:157], 0, v[2:3]
	s_waitcnt vmcnt(12)
	v_mul_f32_e32 v144, v215, v144
	v_mul_f32_e32 v159, v144, v245
	ds_bpermute_b32 v158, v1, v159
	s_and_saveexec_b64 s[0:1], s[6:7]
	s_cbranch_execz .LBB0_857
	v_lshlrev_b32_e32 v193, 16, v192
	v_and_b32_e32 v192, 0xffff0000, v192
	s_waitcnt lgkmcnt(0)
	v_pk_mul_f32 v[158:159], v[158:159], v[192:193]
	s_nop 0
	v_and_b32_sdwa v144, v159, v227 dst_sel:DWORD dst_unused:UNUSED_PAD src0_sel:WORD_1 src1_sel:DWORD
	v_and_b32_sdwa v192, v158, v227 dst_sel:DWORD dst_unused:UNUSED_PAD src0_sel:WORD_1 src1_sel:DWORD
	v_add3_u32 v144, v159, v144, s97
	v_add3_u32 v158, v158, v192, s97
	v_lshrrev_b32_e32 v144, 16, v144
	v_and_or_b32 v144, v158, s66, v144
	global_store_dword v[156:157], v144, off offset:2048

; __device__ __forceinline__ float bflo(unsigned w) { return __uint_as_float(w << 16); }
; __device__ __forceinline__ float bfhi(unsigned w) { return __uint_as_float(w & 0xffff0000u); }
; __device__ __forceinline__ unsigned pk2(float lo, float hi) { return f2bf(lo) | (f2bf(hi) << 16); }
; __device__ __forceinline__ int crow(int r, int hi) { return (r & 3) + 8 * (r >> 2) + 4 * hi; }
; __global__ void __launch_bounds__(NWAVES * 64, 2) mega_fwd(Args args) {
;     ...
;                                       rli[r] = __builtin_amdgcn_rsqf(ssq * (1.0f / 256.0f) + RMS_EPS) * (1.0f - lam_init); } }
;     ...
;                                   for (int rq = 0; rq < 4; ++rq) { unsigned zz[16]; f32x4 t[4];
;                                     int wv_ = wave; asm volatile("" : "+s"(wv_));
; #pragma unroll
;                                     for (int rr = 0; rr < 4; ++rr) { const int r = rq * 4 + rr; const bf16_t* zp = PROJ + (size_t)(b * SEQ + L * 256 + wv_ * 32 + att::crow(r, hi)) * NC + C_ZB + h * 256 + hv * 128 + (r32 & ~1);
; #pragma unroll
;                                         for (int d0 = 0; d0 < 4; ++d0) zz[rr * 4 + d0] = *(const unsigned*)(zp + d0 * 32);
;                                         if (hv == 0) t[rr] = *(const f32x4*)(sq + r * 4); else t[rr] = (f32x4){o[0][r], o[1][r], o[2][r], o[3][r]}; }
;                                     asm volatile("" ::: "memory");
; #pragma unroll
;                                     for (int rr = 0; rr < 4; ++rr) { const int r = rq * 4 + rr; bf16_t* yp = Y + (size_t)(b * SEQ + L * 256 + wv_ * 32 + att::crow(r, hi)) * YS + BW + h * 256 + hv * 128 + r32;
; #pragma unroll
;                                         for (int d0 = 0; d0 < 4; ++d0) { const float val = t[rr][d0] * rli[r] * sg[hv * 4 + d0], vn = __shfl_xor(val, 1);
;                                             if ((r32 & 1) == 0) *(unsigned*)(yp + d0 * 32) = pk2(val * bflo(zz[rr * 4 + d0]), vn * bfhi(zz[rr * 4 + d0])); } } }
.LBB0_887:
	s_or_b64 exec, exec, s[0:1]
	s_waitcnt lgkmcnt(0)
	v_add_f32_e32 v132, v176, v186
	v_fmamk_f32 v132, v132, 0x3b800000, v221
	s_mov_b32 s0, s11
	v_rsq_f32_e32 v132, v132
	v_add_u32_e32 v176, 8, v162
	v_lshl_add_u32 v156, s0, 5, v176
	v_readlane_b32 s0, v253, 48
	v_readlane_b32 s1, v253, 49
	s_waitcnt vmcnt(1)
	v_mul_f32_e32 v165, v205, v132
	s_waitcnt vmcnt(0)
	v_mov_b32_e32 v149, v3
	v_mov_b64_e32 v[158:159], s[0:1]
	v_mad_i64_i32 v[132:133], s[0:1], v156, s8, v[158:159]
	v_lshl_add_u64 v[132:133], v[132:133], 0, s[2:3]
	v_or_b32_e32 v154, 1, v156
	v_lshl_add_u64 v[132:133], v[132:133], 0, v[148:149]
	v_mad_i64_i32 v[150:151], s[0:1], v154, s8, v[158:159]
	v_lshl_add_u64 v[134:135], v[132:133], 0, s[12:13]
	v_add_co_u32_e32 v132, vcc, s10, v132
	v_lshl_add_u64 v[150:151], v[150:151], 0, s[2:3]
	s_nop 0
	v_addc_co_u32_e32 v133, vcc, 0, v133, vcc
	v_lshl_add_u64 v[150:151], v[150:151], 0, v[148:149]
	v_lshl_add_u64 v[152:153], v[150:151], 0, s[12:13]
	v_add_co_u32_e32 v150, vcc, s10, v150
	global_load_dword v246, v[132:133], off offset:2048
	global_load_dword v240, v[134:135], off offset:64
	global_load_dword v238, v[134:135], off offset:128
	global_load_dword v155, v[134:135], off offset:192
	s_nop 0
	global_load_dwordx4 v[132:135], v[236:237], off offset:3072
	global_load_dwordx4 v[136:139], v[236:237], off offset:2048
	global_load_dwordx4 v[140:143], v[236:237], off offset:1024
	global_load_dwordx4 v[144:147], v[236:237], off
	v_addc_co_u32_e32 v151, vcc, 0, v151, vcc
	global_load_dword v233, v[150:151], off offset:2048
	global_load_dword v223, v[152:153], off offset:64
	global_load_dword v193, v[152:153], off offset:128
	s_nop 0
	global_load_dword v153, v[152:153], off offset:192
	v_or_b32_e32 v152, 2, v156
	v_mad_i64_i32 v[150:151], s[0:1], v152, s8, v[158:159]
	v_lshl_add_u64 v[150:151], v[150:151], 0, s[2:3]
	v_lshl_add_u64 v[150:151], v[150:151], 0, v[148:149]
	v_lshl_add_u64 v[186:187], v[150:151], 0, s[12:13]
	v_add_co_u32_e32 v150, vcc, s10, v150
	v_ashrrev_i32_e32 v157, 31, v156
	s_nop 0
	v_addc_co_u32_e32 v151, vcc, 0, v151, vcc
	global_load_dword v192, v[150:151], off offset:2048
	global_load_dword v191, v[186:187], off offset:64
	global_load_dword v189, v[186:187], off offset:128
	s_nop 0
	global_load_dword v151, v[186:187], off offset:192
	v_or_b32_e32 v150, 3, v156
	v_mad_i64_i32 v[158:159], s[0:1], v150, s8, v[158:159]
	v_lshl_add_u64 v[158:159], v[158:159], 0, s[2:3]
	v_lshl_add_u64 v[158:159], v[158:159], 0, v[148:149]
	v_lshl_add_u64 v[194:195], v[158:159], 0, s[12:13]
	v_add_co_u32_e32 v158, vcc, s10, v158
	v_lshlrev_b64 v[156:157], 13, v[156:157]
	s_nop 0
	v_addc_co_u32_e32 v159, vcc, 0, v159, vcc
	global_load_dword v188, v[158:159], off offset:2048
	global_load_dword v187, v[194:195], off offset:64
	global_load_dword v186, v[194:195], off offset:128
	global_load_dword v149, v[194:195], off offset:192
	v_lshl_add_u64 v[156:157], s[4:5], 0, v[156:157]
	v_lshl_add_u64 v[156:157], v[156:157], 0, v[2:3]
	s_waitcnt vmcnt(12)
	v_mul_f32_e32 v144, v165, v144
	v_mul_f32_e32 v159, v144, v245
	ds_bpermute_b32 v158, v1, v159
	s_and_saveexec_b64 s[0:1], s[6:7]
	s_cbranch_execz .LBB0_889
	v_lshlrev_b32_e32 v195, 16, v246
	v_and_b32_e32 v194, 0xffff0000, v246
	s_waitcnt lgkmcnt(0)
	v_pk_mul_f32 v[158:159], v[158:159], v[194:195]
	s_nop 0
	v_and_b32_sdwa v144, v159, v227 dst_sel:DWORD dst_unused:UNUSED_PAD src0_sel:WORD_1 src1_sel:DWORD
	v_and_b32_sdwa v194, v158, v227 dst_sel:DWORD dst_unused:UNUSED_PAD src0_sel:WORD_1 src1_sel:DWORD
	v_add3_u32 v144, v159, v144, s97
	v_add3_u32 v158, v158, v194, s97
	v_lshrrev_b32_e32 v144, 16, v144
	v_and_or_b32 v144, v158, s66, v144
	global_store_dword v[156:157], v144, off offset:2048

; __device__ __forceinline__ float bflo(unsigned w) { return __uint_as_float(w << 16); }
; __device__ __forceinline__ float bfhi(unsigned w) { return __uint_as_float(w & 0xffff0000u); }
; __device__ __forceinline__ unsigned pk2(float lo, float hi) { return f2bf(lo) | (f2bf(hi) << 16); }
; __device__ __forceinline__ int crow(int r, int hi) { return (r & 3) + 8 * (r >> 2) + 4 * hi; }
; __global__ void __launch_bounds__(NWAVES * 64, 2) mega_fwd(Args args) {
;     ...
;                                       rli[r] = __builtin_amdgcn_rsqf(ssq * (1.0f / 256.0f) + RMS_EPS) * (1.0f - lam_init); } }
;     ...
;                                   for (int rq = 0; rq < 4; ++rq) { unsigned zz[16]; f32x4 t[4];
;                                     int wv_ = wave; asm volatile("" : "+s"(wv_));
; #pragma unroll
;                                     for (int rr = 0; rr < 4; ++rr) { const int r = rq * 4 + rr; const bf16_t* zp = PROJ + (size_t)(b * SEQ + L * 256 + wv_ * 32 + att::crow(r, hi)) * NC + C_ZB + h * 256 + hv * 128 + (r32 & ~1);
; #pragma unroll
;                                         for (int d0 = 0; d0 < 4; ++d0) zz[rr * 4 + d0] = *(const unsigned*)(zp + d0 * 32);
;                                         if (hv == 0) t[rr] = *(const f32x4*)(sq + r * 4); else t[rr] = (f32x4){o[0][r], o[1][r], o[2][r], o[3][r]}; }
;                                     asm volatile("" ::: "memory");
; #pragma unroll
;                                     for (int rr = 0; rr < 4; ++rr) { const int r = rq * 4 + rr; bf16_t* yp = Y + (size_t)(b * SEQ + L * 256 + wv_ * 32 + att::crow(r, hi)) * YS + BW + h * 256 + hv * 128 + r32;
; #pragma unroll
;                                         for (int d0 = 0; d0 < 4; ++d0) { const float val = t[rr][d0] * rli[r] * sg[hv * 4 + d0], vn = __shfl_xor(val, 1);
;                                             if ((r32 & 1) == 0) *(unsigned*)(yp + d0 * 32) = pk2(val * bflo(zz[rr * 4 + d0]), vn * bfhi(zz[rr * 4 + d0])); } } }
.LBB0_919:
	s_or_b64 exec, exec, s[0:1]
	s_waitcnt lgkmcnt(0)
	v_add_f32_e32 v132, v168, v180
	v_fmamk_f32 v132, v132, 0x3b800000, v221
	s_mov_b32 s0, s11
	v_rsq_f32_e32 v132, v132
	v_add_u32_e32 v180, 16, v162
	v_lshl_add_u32 v156, s0, 5, v180
	v_readlane_b32 s0, v253, 48
	v_readlane_b32 s1, v253, 49
	v_mul_f32_e32 v168, v205, v132
	s_waitcnt vmcnt(0)
	v_mov_b32_e32 v149, v3
	v_mov_b64_e32 v[158:159], s[0:1]
	v_mad_i64_i32 v[132:133], s[0:1], v156, s8, v[158:159]
	v_lshl_add_u64 v[132:133], v[132:133], 0, s[2:3]
	v_or_b32_e32 v154, 1, v156
	v_lshl_add_u64 v[132:133], v[132:133], 0, v[148:149]
	v_mad_i64_i32 v[150:151], s[0:1], v154, s8, v[158:159]
	v_lshl_add_u64 v[134:135], v[132:133], 0, s[12:13]
	v_add_co_u32_e32 v132, vcc, s10, v132
	v_lshl_add_u64 v[150:151], v[150:151], 0, s[2:3]
	s_nop 0
	v_addc_co_u32_e32 v133, vcc, 0, v133, vcc
	v_lshl_add_u64 v[150:151], v[150:151], 0, v[148:149]
	v_lshl_add_u64 v[152:153], v[150:151], 0, s[12:13]
	v_add_co_u32_e32 v150, vcc, s10, v150
	global_load_dword v238, v[132:133], off offset:2048
	global_load_dword v233, v[134:135], off offset:64
	global_load_dword v223, v[134:135], off offset:128
	global_load_dword v155, v[134:135], off offset:192
	s_nop 0
	s_mov_b64 s[100:101], 0x2000
	v_lshl_add_u64 v[236:237], v[236:237], 0, s[100:101]
	global_load_dwordx4 v[132:135], v[236:237], off offset:-1024
	global_load_dwordx4 v[136:139], v[236:237], off offset:-2048
	global_load_dwordx4 v[140:143], v[236:237], off offset:-3072
	global_load_dwordx4 v[144:147], v[236:237], off offset:-4096
	s_mov_b32 s100, 0xffffe000
	s_mov_b32 s101, -1
	v_lshl_add_u64 v[236:237], v[236:237], 0, s[100:101]
	v_addc_co_u32_e32 v151, vcc, 0, v151, vcc
	global_load_dword v193, v[150:151], off offset:2048
	global_load_dword v192, v[152:153], off offset:64
	global_load_dword v191, v[152:153], off offset:128
	s_nop 0
	global_load_dword v153, v[152:153], off offset:192
	v_or_b32_e32 v152, 2, v156
	v_mad_i64_i32 v[150:151], s[0:1], v152, s8, v[158:159]
	v_lshl_add_u64 v[150:151], v[150:151], 0, s[2:3]
	v_lshl_add_u64 v[150:151], v[150:151], 0, v[148:149]
	v_lshl_add_u64 v[186:187], v[150:151], 0, s[12:13]
	v_add_co_u32_e32 v150, vcc, s10, v150
	v_ashrrev_i32_e32 v157, 31, v156
	s_nop 0
	v_addc_co_u32_e32 v151, vcc, 0, v151, vcc
	global_load_dword v190, v[150:151], off offset:2048
	global_load_dword v189, v[186:187], off offset:64
	global_load_dword v188, v[186:187], off offset:128
	s_nop 0
	global_load_dword v151, v[186:187], off offset:192
	v_or_b32_e32 v150, 3, v156
	v_mad_i64_i32 v[158:159], s[0:1], v150, s8, v[158:159]
	v_lshl_add_u64 v[158:159], v[158:159], 0, s[2:3]
	v_lshl_add_u64 v[158:159], v[158:159], 0, v[148:149]
	v_lshl_add_u64 v[194:195], v[158:159], 0, s[12:13]
	v_add_co_u32_e32 v158, vcc, s10, v158
	v_lshlrev_b64 v[156:157], 13, v[156:157]
	s_nop 0
	v_addc_co_u32_e32 v159, vcc, 0, v159, vcc
	global_load_dword v187, v[158:159], off offset:2048
	global_load_dword v186, v[194:195], off offset:64
	global_load_dword v185, v[194:195], off offset:128
	global_load_dword v149, v[194:195], off offset:192
	v_lshl_add_u64 v[156:157], s[4:5], 0, v[156:157]
	v_lshl_add_u64 v[156:157], v[156:157], 0, v[2:3]
	s_waitcnt vmcnt(12)
	v_mul_f32_e32 v144, v168, v144
	v_mul_f32_e32 v159, v144, v245
	ds_bpermute_b32 v158, v1, v159
	s_and_saveexec_b64 s[0:1], s[6:7]
	s_cbranch_execz .LBB0_921
	v_lshlrev_b32_e32 v195, 16, v238
	v_and_b32_e32 v194, 0xffff0000, v238
	s_waitcnt lgkmcnt(0)
	v_pk_mul_f32 v[158:159], v[158:159], v[194:195]
	s_nop 0
	v_and_b32_sdwa v144, v159, v227 dst_sel:DWORD dst_unused:UNUSED_PAD src0_sel:WORD_1 src1_sel:DWORD
	v_and_b32_sdwa v194, v158, v227 dst_sel:DWORD dst_unused:UNUSED_PAD src0_sel:WORD_1 src1_sel:DWORD
	v_add3_u32 v144, v159, v144, s97
	v_add3_u32 v158, v158, v194, s97
	v_lshrrev_b32_e32 v144, 16, v144
	v_and_or_b32 v144, v158, s66, v144
	global_store_dword v[156:157], v144, off offset:2048

; __device__ __forceinline__ float bflo(unsigned w) { return __uint_as_float(w << 16); }
; __device__ __forceinline__ float bfhi(unsigned w) { return __uint_as_float(w & 0xffff0000u); }
; __device__ __forceinline__ unsigned pk2(float lo, float hi) { return f2bf(lo) | (f2bf(hi) << 16); }
; __device__ __forceinline__ int crow(int r, int hi) { return (r & 3) + 8 * (r >> 2) + 4 * hi; }
; __global__ void __launch_bounds__(NWAVES * 64, 2) mega_fwd(Args args) {
;     ...
;                                       rli[r] = __builtin_amdgcn_rsqf(ssq * (1.0f / 256.0f) + RMS_EPS) * (1.0f - lam_init); } }
;     ...
;                                   for (int rq = 0; rq < 4; ++rq) { unsigned zz[16]; f32x4 t[4];
;                                     int wv_ = wave; asm volatile("" : "+s"(wv_));
; #pragma unroll
;                                     for (int rr = 0; rr < 4; ++rr) { const int r = rq * 4 + rr; const bf16_t* zp = PROJ + (size_t)(b * SEQ + L * 256 + wv_ * 32 + att::crow(r, hi)) * NC + C_ZB + h * 256 + hv * 128 + (r32 & ~1);
; #pragma unroll
;                                         for (int d0 = 0; d0 < 4; ++d0) zz[rr * 4 + d0] = *(const unsigned*)(zp + d0 * 32);
;                                         if (hv == 0) t[rr] = *(const f32x4*)(sq + r * 4); else t[rr] = (f32x4){o[0][r], o[1][r], o[2][r], o[3][r]}; }
;                                     asm volatile("" ::: "memory");
; #pragma unroll
;                                     for (int rr = 0; rr < 4; ++rr) { const int r = rq * 4 + rr; bf16_t* yp = Y + (size_t)(b * SEQ + L * 256 + wv_ * 32 + att::crow(r, hi)) * YS + BW + h * 256 + hv * 128 + r32;
; #pragma unroll
;                                         for (int d0 = 0; d0 < 4; ++d0) { const float val = t[rr][d0] * rli[r] * sg[hv * 4 + d0], vn = __shfl_xor(val, 1);
;                                             if ((r32 & 1) == 0) *(unsigned*)(yp + d0 * 32) = pk2(val * bflo(zz[rr * 4 + d0]), vn * bfhi(zz[rr * 4 + d0])); } } }
.LBB0_951:
	s_or_b64 exec, exec, s[0:1]
	s_waitcnt lgkmcnt(0)
	v_add_f32_e32 v132, v172, v181
	v_fmamk_f32 v132, v132, 0x3b800000, v221
	s_mov_b32 s0, s11
	v_rsq_f32_e32 v132, v132
	v_add_u32_e32 v181, 24, v162
	v_lshl_add_u32 v156, s0, 5, v181
	v_readlane_b32 s0, v253, 48
	v_readlane_b32 s1, v253, 49
	v_mul_f32_e32 v172, v205, v132
	s_waitcnt vmcnt(0)
	v_mov_b32_e32 v149, v3
	v_mov_b64_e32 v[158:159], s[0:1]
	v_mad_i64_i32 v[132:133], s[0:1], v156, s8, v[158:159]
	v_lshl_add_u64 v[132:133], v[132:133], 0, s[2:3]
	v_or_b32_e32 v154, 1, v156
	v_lshl_add_u64 v[132:133], v[132:133], 0, v[148:149]
	v_mad_i64_i32 v[150:151], s[0:1], v154, s8, v[158:159]
	v_lshl_add_u64 v[134:135], v[132:133], 0, s[12:13]
	v_add_co_u32_e32 v132, vcc, s10, v132
	v_lshl_add_u64 v[150:151], v[150:151], 0, s[2:3]
	s_nop 0
	v_addc_co_u32_e32 v133, vcc, 0, v133, vcc
	v_lshl_add_u64 v[150:151], v[150:151], 0, v[148:149]
	v_lshl_add_u64 v[152:153], v[150:151], 0, s[12:13]
	v_add_co_u32_e32 v150, vcc, s10, v150
	global_load_dword v193, v[132:133], off offset:2048
	global_load_dword v192, v[134:135], off offset:64
	global_load_dword v191, v[134:135], off offset:128
	global_load_dword v155, v[134:135], off offset:192
	s_nop 0
	s_mov_b64 s[100:101], 0x2000
	v_lshl_add_u64 v[236:237], v[236:237], 0, s[100:101]
	global_load_dwordx4 v[132:135], v[236:237], off offset:3072
	global_load_dwordx4 v[136:139], v[236:237], off offset:2048
	global_load_dwordx4 v[140:143], v[236:237], off offset:1024
	global_load_dwordx4 v[144:147], v[236:237], off
	s_mov_b32 s100, 0xffffe000
	s_mov_b32 s101, -1
	v_lshl_add_u64 v[236:237], v[236:237], 0, s[100:101]
	v_addc_co_u32_e32 v151, vcc, 0, v151, vcc
	global_load_dword v190, v[150:151], off offset:2048
	global_load_dword v189, v[152:153], off offset:64
	global_load_dword v188, v[152:153], off offset:128
	s_nop 0
	global_load_dword v153, v[152:153], off offset:192
	v_or_b32_e32 v152, 2, v156
	v_mad_i64_i32 v[150:151], s[0:1], v152, s8, v[158:159]
	v_lshl_add_u64 v[150:151], v[150:151], 0, s[2:3]
	v_lshl_add_u64 v[150:151], v[150:151], 0, v[148:149]
	v_lshl_add_u64 v[182:183], v[150:151], 0, s[12:13]
	v_add_co_u32_e32 v150, vcc, s10, v150
	v_ashrrev_i32_e32 v157, 31, v156
	s_nop 0
	v_addc_co_u32_e32 v151, vcc, 0, v151, vcc
	global_load_dword v187, v[150:151], off offset:2048
	global_load_dword v186, v[182:183], off offset:64
	global_load_dword v185, v[182:183], off offset:128
	s_nop 0
	global_load_dword v151, v[182:183], off offset:192
	v_or_b32_e32 v150, 3, v156
	v_mad_i64_i32 v[158:159], s[0:1], v150, s8, v[158:159]
	v_lshl_add_u64 v[158:159], v[158:159], 0, s[2:3]
	v_lshl_add_u64 v[158:159], v[158:159], 0, v[148:149]
	v_lshl_add_u64 v[194:195], v[158:159], 0, s[12:13]
	v_add_co_u32_e32 v158, vcc, s10, v158
	v_lshlrev_b64 v[156:157], 13, v[156:157]
	s_nop 0
	v_addc_co_u32_e32 v159, vcc, 0, v159, vcc
	global_load_dword v184, v[158:159], off offset:2048
	global_load_dword v183, v[194:195], off offset:64
	global_load_dword v182, v[194:195], off offset:128
	global_load_dword v149, v[194:195], off offset:192
	v_lshl_add_u64 v[156:157], s[4:5], 0, v[156:157]
	v_lshl_add_u64 v[156:157], v[156:157], 0, v[2:3]
	s_waitcnt vmcnt(12)
	v_mul_f32_e32 v144, v172, v144
	v_mul_f32_e32 v159, v144, v245
	ds_bpermute_b32 v158, v1, v159
	s_and_saveexec_b64 s[0:1], s[6:7]
	s_cbranch_execz .LBB0_953
	v_lshlrev_b32_e32 v195, 16, v193
	v_and_b32_e32 v194, 0xffff0000, v193
	s_waitcnt lgkmcnt(0)
	v_pk_mul_f32 v[158:159], v[158:159], v[194:195]
	s_nop 0
	v_and_b32_sdwa v144, v159, v227 dst_sel:DWORD dst_unused:UNUSED_PAD src0_sel:WORD_1 src1_sel:DWORD
	v_and_b32_sdwa v193, v158, v227 dst_sel:DWORD dst_unused:UNUSED_PAD src0_sel:WORD_1 src1_sel:DWORD
	v_add3_u32 v144, v159, v144, s97
	v_add3_u32 v158, v158, v193, s97
	v_lshrrev_b32_e32 v144, 16, v144
	v_and_or_b32 v144, v158, s66, v144
	global_store_dword v[156:157], v144, off offset:2048

; __global__ void __launch_bounds__(NWAVES * 64, 2) mega_fwd(Args args) {
;     ...
;                             if (vh == 0) {
; #pragma unroll
;                                 for (int r = 0; r < 16; ++r) *(f32x4*)(sq + r * 4) = (f32x4){o[0][r], o[1][r], o[2][r], o[3][r]};
.LBB0_1112:
	s_and_b64 vcc, exec, s[0:1]
	s_cbranch_vccz .LBB0_1114
	global_store_dwordx4 v[236:237], v[68:71], off offset:-4096
	global_store_dwordx4 v[236:237], v[72:75], off offset:-3072
	global_store_dwordx4 v[236:237], v[76:79], off offset:-2048
	global_store_dwordx4 v[236:237], v[80:83], off offset:-1024
	global_store_dwordx4 v[236:237], v[84:87], off
	global_store_dwordx4 v[236:237], v[88:91], off offset:1024
	global_store_dwordx4 v[236:237], v[92:95], off offset:2048
	global_store_dwordx4 v[236:237], v[96:99], off offset:3072
	s_mov_b64 s[100:101], 0x2000
	v_lshl_add_u64 v[236:237], v[236:237], 0, s[100:101]
	global_store_dwordx4 v[236:237], v[100:103], off offset:-4096
	global_store_dwordx4 v[236:237], v[104:107], off offset:-3072
	global_store_dwordx4 v[236:237], v[108:111], off offset:-2048
	global_store_dwordx4 v[236:237], v[112:115], off offset:-1024
	global_store_dwordx4 v[236:237], v[116:119], off
	global_store_dwordx4 v[236:237], v[120:123], off offset:1024
	global_store_dwordx4 v[236:237], v[124:127], off offset:2048
	global_store_dwordx4 v[236:237], v[128:131], off offset:3072
	s_mov_b32 s100, 0xffffe000
	s_mov_b32 s101, -1
	v_lshl_add_u64 v[236:237], v[236:237], 0, s[100:101]

; __global__ void __launch_bounds__(NWAVES * 64, 2) mega_fwd(Args args) {
;     ...
;                         if (mp == 0) {
; #pragma unroll
;                             for (int r = 0; r < 16; ++r) *(f32x4*)(sp + r * 4) = (f32x4){o[0][r], o[1][r], o[2][r], o[3][r]} * rli[r];
.LBB0_1115:
	v_mov_b32_e32 v68, v52
	v_mov_b32_e32 v69, v4
	v_pk_mul_f32 v[70:71], v[202:203], v[68:69] op_sel_hi:[0,1]
	v_mov_b32_e32 v68, v36
	v_mov_b32_e32 v69, v20
	v_pk_mul_f32 v[68:69], v[202:203], v[68:69] op_sel_hi:[0,1]
	v_mov_b32_e32 v4, v53
	v_mov_b32_e32 v20, v37
	global_store_dwordx4 v[234:235], v[68:71], off offset:-4096
	s_nop 1
	v_pk_mul_f32 v[70:71], v[204:205], v[4:5] op_sel_hi:[0,1]
	v_pk_mul_f32 v[68:69], v[204:205], v[20:21] op_sel_hi:[0,1]
	v_mov_b32_e32 v4, v54
	v_mov_b32_e32 v5, v6
	global_store_dwordx4 v[234:235], v[68:71], off offset:-3072
	v_mov_b32_e32 v6, v55
	v_pk_mul_f32 v[6:7], v[208:209], v[6:7] op_sel_hi:[0,1]
	v_pk_mul_f32 v[70:71], v[206:207], v[4:5] op_sel_hi:[0,1]
	v_mov_b32_e32 v4, v38
	v_mov_b32_e32 v5, v22
	v_mov_b32_e32 v22, v39
	v_pk_mul_f32 v[68:69], v[206:207], v[4:5] op_sel_hi:[0,1]
	v_pk_mul_f32 v[4:5], v[208:209], v[22:23] op_sel_hi:[0,1]
	global_store_dwordx4 v[234:235], v[4:7], off offset:-1024
	global_store_dwordx4 v[234:235], v[68:71], off offset:-2048
	s_nop 0
	v_mov_b32_e32 v4, v56
	v_mov_b32_e32 v5, v8
	v_pk_mul_f32 v[6:7], v[210:211], v[4:5] op_sel_hi:[0,1]
	v_mov_b32_e32 v4, v40
	v_mov_b32_e32 v5, v24
	v_pk_mul_f32 v[4:5], v[210:211], v[4:5] op_sel_hi:[0,1]
	v_mov_b32_e32 v8, v57
	v_mov_b32_e32 v24, v41
	global_store_dwordx4 v[234:235], v[4:7], off
	s_nop 1
	v_pk_mul_f32 v[6:7], v[212:213], v[8:9] op_sel_hi:[0,1]
	v_pk_mul_f32 v[4:5], v[212:213], v[24:25] op_sel_hi:[0,1]
	global_store_dwordx4 v[234:235], v[4:7], off offset:1024
	s_nop 1
	v_mov_b32_e32 v4, v58
	v_mov_b32_e32 v5, v10
	v_pk_mul_f32 v[6:7], v[214:215], v[4:5] op_sel_hi:[0,1]
	v_mov_b32_e32 v4, v42
	v_mov_b32_e32 v5, v26
	v_pk_mul_f32 v[4:5], v[214:215], v[4:5] op_sel_hi:[0,1]
	v_mov_b32_e32 v10, v59
	v_mov_b32_e32 v26, v43
	global_store_dwordx4 v[234:235], v[4:7], off offset:2048
	s_nop 1
	v_pk_mul_f32 v[6:7], v[216:217], v[10:11] op_sel_hi:[0,1]
	v_pk_mul_f32 v[4:5], v[216:217], v[26:27] op_sel_hi:[0,1]
	global_store_dwordx4 v[234:235], v[4:7], off offset:3072
	s_nop 1
	v_mov_b32_e32 v4, v60
	v_mov_b32_e32 v5, v12
	v_pk_mul_f32 v[6:7], v[218:219], v[4:5] op_sel_hi:[0,1]
	v_mov_b32_e32 v4, v44
	v_mov_b32_e32 v5, v28
	v_pk_mul_f32 v[4:5], v[218:219], v[4:5] op_sel_hi:[0,1]
	v_mov_b32_e32 v12, v61
	v_mov_b32_e32 v28, v45
	s_mov_b64 s[100:101], 0x2000
	v_lshl_add_u64 v[234:235], v[234:235], 0, s[100:101]
	global_store_dwordx4 v[234:235], v[4:7], off offset:-4096
	s_mov_b32 s100, 0xffffe000
	s_mov_b32 s101, -1
	v_lshl_add_u64 v[234:235], v[234:235], 0, s[100:101]
	s_nop 1
	v_pk_mul_f32 v[6:7], v[220:221], v[12:13] op_sel_hi:[0,1]
	v_pk_mul_f32 v[4:5], v[220:221], v[28:29] op_sel_hi:[0,1]
	s_mov_b64 s[100:101], 0x2000
	v_lshl_add_u64 v[234:235], v[234:235], 0, s[100:101]
	global_store_dwordx4 v[234:235], v[4:7], off offset:-3072
	s_mov_b32 s100, 0xffffe000
	s_mov_b32 s101, -1
	v_lshl_add_u64 v[234:235], v[234:235], 0, s[100:101]
	s_nop 1
	v_mov_b32_e32 v4, v62
	v_mov_b32_e32 v5, v14
	v_pk_mul_f32 v[6:7], v[222:223], v[4:5] op_sel_hi:[0,1]
	v_mov_b32_e32 v4, v46
	v_mov_b32_e32 v5, v30
	v_pk_mul_f32 v[4:5], v[222:223], v[4:5] op_sel_hi:[0,1]
	v_mov_b32_e32 v14, v63
	v_mov_b32_e32 v30, v47
	s_mov_b64 s[100:101], 0x2000
	v_lshl_add_u64 v[234:235], v[234:235], 0, s[100:101]
	global_store_dwordx4 v[234:235], v[4:7], off offset:-2048
	s_mov_b32 s100, 0xffffe000
	s_mov_b32 s101, -1
	v_lshl_add_u64 v[234:235], v[234:235], 0, s[100:101]
	s_nop 1
	v_pk_mul_f32 v[6:7], v[224:225], v[14:15] op_sel_hi:[0,1]
	v_pk_mul_f32 v[4:5], v[224:225], v[30:31] op_sel_hi:[0,1]
	s_mov_b64 s[100:101], 0x2000
	v_lshl_add_u64 v[234:235], v[234:235], 0, s[100:101]
	global_store_dwordx4 v[234:235], v[4:7], off offset:-1024
	s_mov_b32 s100, 0xffffe000
	s_mov_b32 s101, -1
	v_lshl_add_u64 v[234:235], v[234:235], 0, s[100:101]
	s_nop 1
	v_mov_b32_e32 v4, v64
	v_mov_b32_e32 v5, v16
	v_pk_mul_f32 v[6:7], v[226:227], v[4:5] op_sel_hi:[0,1]
	v_mov_b32_e32 v4, v48
	v_mov_b32_e32 v5, v32
	v_pk_mul_f32 v[4:5], v[226:227], v[4:5] op_sel_hi:[0,1]
	v_mov_b32_e32 v16, v65
	v_mov_b32_e32 v32, v49
	s_mov_b64 s[100:101], 0x2000
	v_lshl_add_u64 v[234:235], v[234:235], 0, s[100:101]
	global_store_dwordx4 v[234:235], v[4:7], off
	s_mov_b32 s100, 0xffffe000
	s_mov_b32 s101, -1
	v_lshl_add_u64 v[234:235], v[234:235], 0, s[100:101]
	s_nop 1
	v_pk_mul_f32 v[6:7], v[228:229], v[16:17] op_sel_hi:[0,1]
	v_pk_mul_f32 v[4:5], v[228:229], v[32:33] op_sel_hi:[0,1]
	s_mov_b64 s[100:101], 0x2000
	v_lshl_add_u64 v[234:235], v[234:235], 0, s[100:101]
	global_store_dwordx4 v[234:235], v[4:7], off offset:1024
	s_mov_b32 s100, 0xffffe000
	s_mov_b32 s101, -1
	v_lshl_add_u64 v[234:235], v[234:235], 0, s[100:101]
	s_nop 1
	v_mov_b32_e32 v4, v66
	v_mov_b32_e32 v5, v18
	v_pk_mul_f32 v[6:7], v[230:231], v[4:5] op_sel_hi:[0,1]
	v_mov_b32_e32 v4, v50
	v_mov_b32_e32 v5, v34
	v_pk_mul_f32 v[4:5], v[230:231], v[4:5] op_sel_hi:[0,1]
	v_mov_b32_e32 v18, v67
	v_mov_b32_e32 v34, v51
	s_mov_b64 s[100:101], 0x2000
	v_lshl_add_u64 v[234:235], v[234:235], 0, s[100:101]
	global_store_dwordx4 v[234:235], v[4:7], off offset:2048
	s_mov_b32 s100, 0xffffe000
	s_mov_b32 s101, -1
	v_lshl_add_u64 v[234:235], v[234:235], 0, s[100:101]
	s_nop 1
	v_pk_mul_f32 v[6:7], v[232:233], v[18:19] op_sel_hi:[0,1]
	v_pk_mul_f32 v[4:5], v[232:233], v[34:35] op_sel_hi:[0,1]
	s_mov_b64 s[100:101], 0x2000
	v_lshl_add_u64 v[234:235], v[234:235], 0, s[100:101]
	global_store_dwordx4 v[234:235], v[4:7], off offset:3072
	s_mov_b32 s100, 0xffffe000
	s_mov_b32 s101, -1
	v_lshl_add_u64 v[234:235], v[234:235], 0, s[100:101]
	s_branch .LBB0_799

;     __device__ __forceinline__ void operator()(const f32x4 (&acc)[2][2][4][2], const Unit& u, int wr, int wc, int fr, int fq) const {
;     ...
;         const int row0 = u.pm * BM + wr * 64 + fr, col0 = u.pn * BM + wc * 32 + 4 * fq;
; #pragma unroll
; template <class Epi, class Sched, bool ALIGN_EPI = false, bool SP2 = false>
; __device__ __forceinline__ void gemm_phase(PG8_LAS unsigned char* lds, const Gemm g, const Sched& S, const Epi& E) {
;     ...
;     for (int i = 0; i < 2; ++i) { int R, C; stage_rc(tid * 16 + i * 8192, R, C); const int Rb = Epi::PERM ? ((R & ~31) + perm32(R & 31)) : R;
;         voffA[i] = (unsigned)(R * K + C) * 2u; voffB[i] = (unsigned)(Rb * K + C) * 2u; }
;     const size_t kstep = (size_t)(BK * 2);
;     const size_t hstep = (size_t)HALF * K * 2;
;     const size_t tstep = 2 * hstep;
;     const unsigned ldsw = (unsigned)wid * 1024u;
;     const int aoff = lds_byte(wr * 64 + fr, fq * 8), boff = lds_byte(wc * 32 + fr, fq * 8);
;     ...
;     Unit cur, nxt; int ui = 0;
;     if (!S.next(0, cur)) return;
;     f32x4 acc[2][2][4][2];
; #pragma unroll
;     for (int a = 0; a < 2; ++a)
; #pragma unroll
;         for (int b = 0; b < 2; ++b)
; #pragma unroll
;             for (int m = 0; m < 4; ++m)
; #pragma unroll
;                 for (int n = 0; n < 2; ++n) acc[a][b][m][n] = (f32x4){0.f, 0.f, 0.f, 0.f};
;     bf16x8 At[4][2], B0[2][2], B1[2][2];
;     const char* cA = (const char*)g.A + (size_t)cur.pm * tstep; const char* cB = (const char*)g.Bt + (size_t)cur.pn * tstep;
;     S.a_ready(cur);
;     if constexpr (SP2) {
;         PG8_STAGE(PG8_SB(0, 0), cB, voffB); PG8_STAGE(PG8_SB(0, 1), cB + hstep, voffB); PG8_STAGE(PG8_SA(0, 0), cA, voffA); PG8_STAGE(PG8_SA(0, 1), cA + hstep, voffA);
;         if (wr == 1) PG8_BAR;
;         PG8_WAIT_V(2); PG8_BAR;
;         PG8_STAGE(PG8_SB(1, 0), cB + kstep, voffB); PG8_STAGE(PG8_SA(1, 0), cA + kstep, voffA); PG8_STAGE(PG8_SB(1, 1), cB + hstep + kstep, voffB);
;         PG8_WAIT_V(6); PG8_BAR;
;     } else {
;         PG8_STAGE(PG8_SB(0, 0), cB, voffB); PG8_STAGE(PG8_SA(0, 0), cA, voffA); PG8_STAGE(PG8_SB(0, 1), cB + hstep, voffB); PG8_STAGE(PG8_SA(0, 1), cA + hstep, voffA);
;         if (wr == 1) PG8_BAR;
;         PG8_WAIT_V(4); PG8_BAR;
;         PG8_STAGE(PG8_SB(1, 0), cB + kstep, voffB); PG8_STAGE(PG8_SA(1, 0), cA + kstep, voffA); PG8_STAGE(PG8_SB(1, 1), cB + hstep + kstep, voffB);
;         PG8_WAIT_V(6); PG8_BAR;
.LBB0_1670:
	v_readlane_b32 s4, v253, 34
	v_readlane_b32 s5, v253, 35
	s_and_b64 s[4:5], s[4:5], exec
	s_mov_b32 s4, 0x90000
	s_cselect_b32 s4, 0x80000, s4
	s_add_u32 s8, s0, 0x27100000
	v_and_b32_e32 v19, 15, v18
	s_addc_u32 s9, s1, 0
	v_bfe_u32 v20, v18, 4, 2
	v_lshl_or_b32 v1, s10, 6, v19
	s_add_u32 s4, s0, s4
	v_lshlrev_b32_e32 v21, 4, v20
	v_lshlrev_b32_e32 v23, 2, v1
	s_addc_u32 s5, s1, 0
	s_and_b32 s15, s11, 3
	v_lshl_or_b32 v22, v19, 6, v21
	s_lshl_b32 s0, s10, 13
	v_and_b32_e32 v24, 32, v23
	v_lshlrev_b32_e32 v18, 2, v18
	s_add_i32 m0, s30, 0x18000
	v_lshl_add_u64 v[10:11], v[10:11], 0, s[78:79]
	v_bitop3_b32 v24, v22, s0, v24 bitop3:0xde
	s_lshl_b32 s0, s15, 12
	v_and_b32_e32 v18, 32, v18
	s_waitcnt vmcnt(2)
	s_barrier
	global_load_lds_dwordx4 v[10:11], off
	v_lshl_add_u64 v[8:9], v[8:9], 0, s[78:79]
	s_add_i32 m0, s30, 0x1a000
	s_add_i32 s37, s30, 0x8000
	s_add_i32 s38, s30, 0xa000
	v_and_b32_e32 v176, 3, v19
	v_lshlrev_b32_e32 v176, 6, v176
	v_or_b32_e32 v176, v176, v21
	v_bfe_u32 v18, v19, 2, 1
	v_lshl_or_b32 v176, v18, 9, v176
	v_lshlrev_b32_e32 v18, 5, v18
	v_xor_b32_e32 v176, v176, v18
	v_bfe_u32 v18, v19, 3, 1
	v_lshl_or_b32 v176, v18, 11, v176
	v_or_b32_e32 v176, s0, v176
	global_load_lds_dwordx4 v[8:9], off
	v_lshl_add_u64 v[4:5], v[4:5], 0, s[78:79]
	s_mov_b32 m0, s37
	s_add_u32 s0, s22, 0x100080
	global_load_lds_dwordx4 v[4:5], off
	v_lshl_add_u64 v[4:5], v[6:7], 0, s[78:79]
	s_mov_b32 m0, s38
	s_addc_u32 s1, s23, 0
	global_load_lds_dwordx4 v[4:5], off
	s_add_i32 m0, s30, 0x1c000
	v_lshl_add_u64 v[4:5], s[0:1], 0, v[2:3]
	global_load_lds_dwordx4 v[4:5], off
	v_lshl_add_u64 v[4:5], s[0:1], 0, v[132:133]
	s_add_i32 m0, s30, 0x1e000
	s_cmpk_lt_u32 s14, 0x100
	global_load_lds_dwordx4 v[4:5], off
	s_cselect_b64 s[10:11], -1, 0
	v_lshlrev_b32_e32 v4, 3, v20
	s_and_b32 s14, s14, 0xc0
	v_lshl_or_b32 v177, s15, 5, v4
	v_or3_b32 v4, s14, v19, v21
	v_lshlrev_b32_e32 v4, 2, v4
	v_mov_b32_e32 v5, v3
	v_lshl_add_u64 v[134:135], s[4:5], 0, v[4:5]
	v_readlane_b32 s5, v253, 33
	v_and_b32_e32 v5, 1, v15
	s_lshl_b32 s15, s15, 10
	v_add_u32_e32 v179, s5, v4
	v_lshlrev_b32_e32 v4, 16, v15
	v_and_b32_e32 v4, 0xfffe0000, v4
	v_lshl_add_u32 v4, v16, 13, v4
	v_lshl_or_b32 v4, v5, 6, v4
	v_lshl_add_u32 v136, v17, 1, v4
	v_lshlrev_b32_e32 v4, 16, v12
	v_and_b32_e32 v4, 0xfffe0000, v4
	s_waitcnt vmcnt(6)
	s_add_i32 s4, s5, s15
	v_lshl_add_u32 v4, v13, 13, v4
	v_and_b32_e32 v5, 1, v12
	v_add_u32_e32 v178, s4, v23
	v_lshl_or_b32 v4, v5, 6, v4
	v_readlane_b32 s4, v253, 1
	s_mov_b32 s36, 0
	v_cmp_eq_u32_e64 s[0:1], 0, v20
	v_mov_b32_e32 v137, v3
	v_lshl_add_u32 v138, v14, 1, v4
	v_mov_b32_e32 v139, v3
	v_add_u32_e32 v180, 0, v24
	v_readlane_b32 s39, v253, 0
	s_mov_b32 s40, s4
	s_barrier
	v_readlane_b32 s5, v253, 2
	s_branch .LBB0_1673

; #define PG8_STAGE(bufoff, gbase, voff) do { _Pragma("unroll") for (int _i = 0; _i < 2; ++_i) \
;         __builtin_amdgcn_global_load_lds((const unsigned*)((const char*)(gbase) + (voff)[_i]), (PG8_LAS unsigned*)(lds + (bufoff) + ldsw + _i * 8192), 16, 0, 0); } while (0)
; #define PG8_LDA(dst, b, h) do { _Pragma("unroll") for (int m = 0; m < 4; ++m) _Pragma("unroll") for (int k = 0; k < 2; ++k) dst[m][k] = *(const PG8_LAS bf16x8*)(lds + PG8_SA(b, h) + aoff + m * 2048 + k * 1024); } while (0)
; #define PG8_LDB(dst, b, h) do { _Pragma("unroll") for (int n = 0; n < 2; ++n) _Pragma("unroll") for (int k = 0; k < 2; ++k) dst[n][k] = *(const PG8_LAS bf16x8*)(lds + PG8_SB(b, h) + boff + n * 2048 + k * 1024); } while (0)
; #define PG8_MMA(ai, bj, At, Bt) do { __builtin_amdgcn_s_setprio(1); _Pragma("unroll") for (int m = 0; m < 4; ++m) _Pragma("unroll") for (int n = 0; n < 2; ++n) _Pragma("unroll") for (int k = 0; k < 2; ++k) \
;         acc[ai][bj][m][n] = __builtin_amdgcn_mfma_f32_16x16x32_bf16(Bt[n][k], At[m][k], acc[ai][bj][m][n], 0, 0, 0); __builtin_amdgcn_s_setprio(0); } while (0)
; #define PG8_WAIT_V(n) asm volatile("s_waitcnt vmcnt(" #n ")" ::: "memory")
; template <class Epi, class Sched, bool ALIGN_EPI = false, bool SP2 = false>
; __device__ __forceinline__ void gemm_phase(PG8_LAS unsigned char* lds, const Gemm g, const Sched& S, const Epi& E) {
;     ...
;             PG8_LDB(B0, 0, 0); PG8_LDB(B1, 0, 1); PG8_SCHED; PG8_LDA(At, 0, 0); PG8_STAGE(PG8_SA(1, 1), a1 + hstep, voffA);
;             PG8_WAIT_V(8); PG8_WAIT_L(0); PG8_BAR; PG8_MMA(0, 0, At, B0); PG8_MMA(0, 1, At, B1); PG8_BAR; PG8_SCHED;
;             PG8_LDA(At, 0, 1); PG8_STAGE(PG8_SB(0, 0), b2, voffB); PG8_STAGE(PG8_SB(0, 1), b2 + hstep, voffB); PG8_STAGE(PG8_SA(0, 0), a2, voffA);
;             PG8_WAIT_V(8); PG8_WAIT_L(0); PG8_BAR; PG8_MMA(1, 0, At, B0); PG8_MMA(1, 1, At, B1); PG8_BAR; PG8_SCHED;
;             PG8_LDB(B0, 1, 0); PG8_LDB(B1, 1, 1); PG8_SCHED; PG8_LDA(At, 1, 0); PG8_STAGE(PG8_SA(0, 1), a2 + hstep, voffA);
;             PG8_WAIT_V(8); PG8_WAIT_L(0); PG8_BAR; PG8_MMA(0, 0, At, B0); PG8_MMA(0, 1, At, B1); PG8_BAR; PG8_SCHED;
;             PG8_LDA(At, 1, 1); PG8_STAGE(PG8_SB(1, 0), b3, voffB); PG8_STAGE(PG8_SB(1, 1), b3 + hstep, voffB); PG8_STAGE(PG8_SA(1, 0), a3, voffA);
;             PG8_WAIT_V(8); PG8_WAIT_L(0); PG8_BAR; PG8_MMA(1, 0, At, B0); PG8_MMA(1, 1, At, B1); PG8_BAR; PG8_SCHED;
.LBB0_1680:
	s_add_u32 s22, s12, 0xfff00080
	s_addc_u32 s23, s13, -1
	s_add_i32 s46, 0, 0x10000
	s_cmp_eq_u32 s45, 60
	s_cselect_b32 s25, s17, s23
	s_cselect_b32 s24, s41, s22
	s_cselect_b32 s23, s15, s44
	s_cselect_b32 s22, s42, s43
	s_add_i32 s48, 0, 0x14000
	v_add_u32_e32 v152, s46, v176
	v_add_u32_e32 v168, s48, v176
	ds_read_b128 v[140:143], v152
	ds_read_b128 v[144:147], v152 offset:1024
	ds_read_b128 v[148:151], v152 offset:256
	ds_read_b128 v[152:155], v152 offset:1280
	ds_read_b128 v[156:159], v168
	ds_read_b128 v[160:163], v168 offset:1024
	ds_read_b128 v[164:167], v168 offset:256
	ds_read_b128 v[168:171], v168 offset:1280
	v_lshl_add_u64 v[210:211], s[12:13], 0, v[136:137]
	s_add_i32 m0, s30, 0xc000
	ds_read_b128 v[172:175], v180
	ds_read_b128 v[182:185], v180 offset:1024
	ds_read_b128 v[186:189], v180 offset:2048
	ds_read_b128 v[190:193], v180 offset:3072
	ds_read_b128 v[194:197], v180 offset:4096
	ds_read_b128 v[198:201], v180 offset:5120
	ds_read_b128 v[202:205], v180 offset:6144
	ds_read_b128 v[206:209], v180 offset:7168
	global_load_lds_dwordx4 v[210:211], off
	v_lshl_add_u64 v[210:211], s[12:13], 0, v[138:139]
	s_add_i32 m0, s30, 0xe000
	s_nop 0
	global_load_lds_dwordx4 v[210:211], off
	s_waitcnt vmcnt(8)
	s_waitcnt lgkmcnt(0)
	s_barrier
	s_setprio 1
	s_waitcnt lgkmcnt(0)
	v_mfma_f32_16x16x32_bf16 v[128:131], v[140:143], v[172:175], v[128:131]
	v_mfma_f32_16x16x32_bf16 v[124:127], v[148:151], v[172:175], v[124:127]
	v_mfma_f32_16x16x32_bf16 v[112:115], v[140:143], v[186:189], v[112:115]
	v_mfma_f32_16x16x32_bf16 v[108:111], v[148:151], v[186:189], v[108:111]
	v_mfma_f32_16x16x32_bf16 v[96:99], v[140:143], v[194:197], v[96:99]
	v_mfma_f32_16x16x32_bf16 v[92:95], v[148:151], v[194:197], v[92:95]
	v_mfma_f32_16x16x32_bf16 v[80:83], v[140:143], v[202:205], v[80:83]
	v_mfma_f32_16x16x32_bf16 v[76:79], v[148:151], v[202:205], v[76:79]
	v_mfma_f32_16x16x32_bf16 v[128:131], v[144:147], v[182:185], v[128:131]
	v_mfma_f32_16x16x32_bf16 v[124:127], v[152:155], v[182:185], v[124:127]
	v_mfma_f32_16x16x32_bf16 v[112:115], v[144:147], v[190:193], v[112:115]
	v_mfma_f32_16x16x32_bf16 v[108:111], v[152:155], v[190:193], v[108:111]
	v_mfma_f32_16x16x32_bf16 v[96:99], v[144:147], v[198:201], v[96:99]
	v_mfma_f32_16x16x32_bf16 v[92:95], v[152:155], v[198:201], v[92:95]
	v_mfma_f32_16x16x32_bf16 v[80:83], v[144:147], v[206:209], v[80:83]
	v_mfma_f32_16x16x32_bf16 v[76:79], v[152:155], v[206:209], v[76:79]
	s_setprio 0
	s_setprio 1
	v_mfma_f32_16x16x32_bf16 v[120:123], v[156:159], v[172:175], v[120:123]
	v_mfma_f32_16x16x32_bf16 v[116:119], v[164:167], v[172:175], v[116:119]
	v_mfma_f32_16x16x32_bf16 v[104:107], v[156:159], v[186:189], v[104:107]
	v_mfma_f32_16x16x32_bf16 v[100:103], v[164:167], v[186:189], v[100:103]
	v_mfma_f32_16x16x32_bf16 v[88:91], v[156:159], v[194:197], v[88:91]
	v_mfma_f32_16x16x32_bf16 v[84:87], v[164:167], v[194:197], v[84:87]
	v_mfma_f32_16x16x32_bf16 v[72:75], v[156:159], v[202:205], v[72:75]
	v_mfma_f32_16x16x32_bf16 v[68:71], v[164:167], v[202:205], v[68:71]
	v_mfma_f32_16x16x32_bf16 v[120:123], v[160:163], v[182:185], v[120:123]
	v_mfma_f32_16x16x32_bf16 v[116:119], v[168:171], v[182:185], v[116:119]
	v_mfma_f32_16x16x32_bf16 v[104:107], v[160:163], v[190:193], v[104:107]
	v_mfma_f32_16x16x32_bf16 v[100:103], v[168:171], v[190:193], v[100:103]
	v_mfma_f32_16x16x32_bf16 v[88:91], v[160:163], v[198:201], v[88:91]
	v_mfma_f32_16x16x32_bf16 v[84:87], v[168:171], v[198:201], v[84:87]
	v_mfma_f32_16x16x32_bf16 v[72:75], v[160:163], v[206:209], v[72:75]
	v_mfma_f32_16x16x32_bf16 v[68:71], v[168:171], v[206:209], v[68:71]
	s_setprio 0
	s_barrier
	s_add_i32 s46, s46, s29
	v_lshl_add_u64 v[210:211], s[22:23], 0, v[2:3]
	s_mov_b32 m0, s46
	ds_read_b128 v[172:175], v180 offset:16384
	ds_read_b128 v[182:185], v180 offset:17408
	ds_read_b128 v[186:189], v180 offset:18432
	ds_read_b128 v[190:193], v180 offset:19456
	ds_read_b128 v[194:197], v180 offset:20480
	ds_read_b128 v[198:201], v180 offset:21504
	ds_read_b128 v[202:205], v180 offset:22528
	ds_read_b128 v[206:209], v180 offset:23552
	global_load_lds_dwordx4 v[210:211], off
	s_add_i32 m0, s46, 0x2000
	s_add_u32 s46, s22, 0x100000
	v_lshl_add_u64 v[212:213], s[22:23], 0, v[132:133]
	s_addc_u32 s47, s23, 0
	s_add_i32 s48, s48, s29
	global_load_lds_dwordx4 v[212:213], off
	v_lshl_add_u64 v[214:215], s[46:47], 0, v[2:3]
	s_mov_b32 m0, s48
	v_lshl_add_u64 v[216:217], s[24:25], 0, v[132:133]
	global_load_lds_dwordx4 v[214:215], off
	v_lshl_add_u64 v[214:215], s[46:47], 0, v[132:133]
	s_add_i32 m0, s48, 0x2000
	s_nop 0
	global_load_lds_dwordx4 v[214:215], off
	v_lshl_add_u64 v[214:215], s[24:25], 0, v[2:3]
	s_mov_b32 m0, s30
	s_nop 0
	global_load_lds_dwordx4 v[214:215], off
	s_mov_b32 m0, s31
	s_nop 0
	global_load_lds_dwordx4 v[216:217], off
	s_waitcnt vmcnt(8)
	s_waitcnt lgkmcnt(0)
	s_barrier
; #define PG8_STAGE(bufoff, gbase, voff) do { _Pragma("unroll") for (int _i = 0; _i < 2; ++_i) \
;         __builtin_amdgcn_global_load_lds((const unsigned*)((const char*)(gbase) + (voff)[_i]), (PG8_LAS unsigned*)(lds + (bufoff) + ldsw + _i * 8192), 16, 0, 0); } while (0)
; #define PG8_LDA(dst, b, h) do { _Pragma("unroll") for (int m = 0; m < 4; ++m) _Pragma("unroll") for (int k = 0; k < 2; ++k) dst[m][k] = *(const PG8_LAS bf16x8*)(lds + PG8_SA(b, h) + aoff + m * 2048 + k * 1024); } while (0)
; #define PG8_LDB(dst, b, h) do { _Pragma("unroll") for (int n = 0; n < 2; ++n) _Pragma("unroll") for (int k = 0; k < 2; ++k) dst[n][k] = *(const PG8_LAS bf16x8*)(lds + PG8_SB(b, h) + boff + n * 2048 + k * 1024); } while (0)
; #define PG8_MMA(ai, bj, At, Bt) do { __builtin_amdgcn_s_setprio(1); _Pragma("unroll") for (int m = 0; m < 4; ++m) _Pragma("unroll") for (int n = 0; n < 2; ++n) _Pragma("unroll") for (int k = 0; k < 2; ++k) \
;         acc[ai][bj][m][n] = __builtin_amdgcn_mfma_f32_16x16x32_bf16(Bt[n][k], At[m][k], acc[ai][bj][m][n], 0, 0, 0); __builtin_amdgcn_s_setprio(0); } while (0)
; #define PG8_WAIT_V(n) asm volatile("s_waitcnt vmcnt(" #n ")" ::: "memory")
; #define PG8_WAIT_L(n) asm volatile("s_waitcnt lgkmcnt(" #n ")" ::: "memory")
; #define PG8_BAR __builtin_amdgcn_s_barrier()
; #define PG8_SCHED __builtin_amdgcn_sched_barrier(0)
; template <class Epi, class Sched, bool ALIGN_EPI = false, bool SP2 = false>
; __device__ __forceinline__ void gemm_phase(PG8_LAS unsigned char* lds, const Gemm g, const Sched& S, const Epi& E) {
;     ...
;             PG8_LDA(At, 0, 1); PG8_STAGE(PG8_SB(0, 0), b2, voffB); PG8_STAGE(PG8_SB(0, 1), b2 + hstep, voffB); PG8_STAGE(PG8_SA(0, 0), a2, voffA);
;             PG8_WAIT_V(8); PG8_WAIT_L(0); PG8_BAR; PG8_MMA(1, 0, At, B0); PG8_MMA(1, 1, At, B1); PG8_BAR; PG8_SCHED;
;             PG8_LDB(B0, 1, 0); PG8_LDB(B1, 1, 1); PG8_SCHED; PG8_LDA(At, 1, 0); PG8_STAGE(PG8_SA(0, 1), a2 + hstep, voffA);
;             PG8_WAIT_V(8); PG8_WAIT_L(0); PG8_BAR; PG8_MMA(0, 0, At, B0); PG8_MMA(0, 1, At, B1); PG8_BAR; PG8_SCHED;
	s_setprio 1
	s_waitcnt lgkmcnt(0)
	v_mfma_f32_16x16x32_bf16 v[64:67], v[140:143], v[172:175], v[64:67]
	v_mfma_f32_16x16x32_bf16 v[60:63], v[148:151], v[172:175], v[60:63]
	v_mfma_f32_16x16x32_bf16 v[48:51], v[140:143], v[186:189], v[48:51]
	v_mfma_f32_16x16x32_bf16 v[44:47], v[148:151], v[186:189], v[44:47]
	v_mfma_f32_16x16x32_bf16 v[32:35], v[140:143], v[194:197], v[32:35]
	v_mfma_f32_16x16x32_bf16 v[28:31], v[148:151], v[194:197], v[28:31]
	v_mfma_f32_16x16x32_bf16 v[16:19], v[140:143], v[202:205], v[16:19]
	v_mfma_f32_16x16x32_bf16 v[12:15], v[148:151], v[202:205], v[12:15]
	v_mfma_f32_16x16x32_bf16 v[64:67], v[144:147], v[182:185], v[64:67]
	v_mfma_f32_16x16x32_bf16 v[60:63], v[152:155], v[182:185], v[60:63]
	v_mfma_f32_16x16x32_bf16 v[48:51], v[144:147], v[190:193], v[48:51]
	v_mfma_f32_16x16x32_bf16 v[44:47], v[152:155], v[190:193], v[44:47]
	v_mfma_f32_16x16x32_bf16 v[32:35], v[144:147], v[198:201], v[32:35]
	v_mfma_f32_16x16x32_bf16 v[28:31], v[152:155], v[198:201], v[28:31]
	v_mfma_f32_16x16x32_bf16 v[16:19], v[144:147], v[206:209], v[16:19]
	v_mfma_f32_16x16x32_bf16 v[12:15], v[152:155], v[206:209], v[12:15]
	s_setprio 0
	s_setprio 1
	v_mfma_f32_16x16x32_bf16 v[56:59], v[156:159], v[172:175], v[56:59]
	v_mfma_f32_16x16x32_bf16 v[52:55], v[164:167], v[172:175], v[52:55]
	v_mfma_f32_16x16x32_bf16 v[40:43], v[156:159], v[186:189], v[40:43]
	v_mfma_f32_16x16x32_bf16 v[36:39], v[164:167], v[186:189], v[36:39]
	v_mfma_f32_16x16x32_bf16 v[24:27], v[156:159], v[194:197], v[24:27]
	v_mfma_f32_16x16x32_bf16 v[20:23], v[164:167], v[194:197], v[20:23]
	v_mfma_f32_16x16x32_bf16 v[8:11], v[156:159], v[202:205], v[8:11]
	v_mfma_f32_16x16x32_bf16 v[4:7], v[164:167], v[202:205], v[4:7]
	v_mfma_f32_16x16x32_bf16 v[56:59], v[160:163], v[182:185], v[56:59]
	v_mfma_f32_16x16x32_bf16 v[52:55], v[168:171], v[182:185], v[52:55]
	v_mfma_f32_16x16x32_bf16 v[40:43], v[160:163], v[190:193], v[40:43]
	v_mfma_f32_16x16x32_bf16 v[36:39], v[168:171], v[190:193], v[36:39]
	v_mfma_f32_16x16x32_bf16 v[24:27], v[160:163], v[198:201], v[24:27]
	v_mfma_f32_16x16x32_bf16 v[20:23], v[168:171], v[198:201], v[20:23]
	v_mfma_f32_16x16x32_bf16 v[8:11], v[160:163], v[206:209], v[8:11]
	v_mfma_f32_16x16x32_bf16 v[4:7], v[168:171], v[206:209], v[4:7]
	s_setprio 0
	s_barrier
	s_add_i32 s46, 0, 0x18000
	s_add_i32 s47, 0, 0x1c000
	v_add_u32_e32 v152, s46, v176
	v_add_u32_e32 v168, s47, v176
	ds_read_b128 v[140:143], v152
	ds_read_b128 v[144:147], v152 offset:1024
	ds_read_b128 v[148:151], v152 offset:256
	ds_read_b128 v[152:155], v152 offset:1280
	ds_read_b128 v[156:159], v168
	ds_read_b128 v[160:163], v168 offset:1024
	ds_read_b128 v[164:167], v168 offset:256
	ds_read_b128 v[168:171], v168 offset:1280
	s_add_u32 s24, s24, 0x100000
	s_addc_u32 s25, s25, 0
	s_mov_b32 m0, s34
	v_lshl_add_u64 v[222:223], s[24:25], 0, v[2:3]
	ds_read_b128 v[172:175], v180 offset:32768
	ds_read_b128 v[182:185], v180 offset:33792
	ds_read_b128 v[186:189], v180 offset:34816
	ds_read_b128 v[190:193], v180 offset:35840
	ds_read_b128 v[194:197], v180 offset:36864
	ds_read_b128 v[198:201], v180 offset:37888
	ds_read_b128 v[202:205], v180 offset:38912
	ds_read_b128 v[206:209], v180 offset:39936
	global_load_lds_dwordx4 v[222:223], off
	v_lshl_add_u64 v[222:223], s[24:25], 0, v[132:133]
	s_mov_b32 m0, s35
	s_nop 0
	global_load_lds_dwordx4 v[222:223], off
	s_waitcnt vmcnt(8)
	s_waitcnt lgkmcnt(0)
	s_barrier
	s_setprio 1
	s_waitcnt lgkmcnt(0)
	v_mfma_f32_16x16x32_bf16 v[128:131], v[140:143], v[172:175], v[128:131]
	v_mfma_f32_16x16x32_bf16 v[124:127], v[148:151], v[172:175], v[124:127]
	v_mfma_f32_16x16x32_bf16 v[112:115], v[140:143], v[186:189], v[112:115]
	v_mfma_f32_16x16x32_bf16 v[108:111], v[148:151], v[186:189], v[108:111]
	v_mfma_f32_16x16x32_bf16 v[96:99], v[140:143], v[194:197], v[96:99]
	v_mfma_f32_16x16x32_bf16 v[92:95], v[148:151], v[194:197], v[92:95]
	v_mfma_f32_16x16x32_bf16 v[80:83], v[140:143], v[202:205], v[80:83]
	v_mfma_f32_16x16x32_bf16 v[76:79], v[148:151], v[202:205], v[76:79]
	v_mfma_f32_16x16x32_bf16 v[128:131], v[144:147], v[182:185], v[128:131]
	v_mfma_f32_16x16x32_bf16 v[124:127], v[152:155], v[182:185], v[124:127]
	v_mfma_f32_16x16x32_bf16 v[112:115], v[144:147], v[190:193], v[112:115]
	v_mfma_f32_16x16x32_bf16 v[108:111], v[152:155], v[190:193], v[108:111]
	v_mfma_f32_16x16x32_bf16 v[96:99], v[144:147], v[198:201], v[96:99]
	v_mfma_f32_16x16x32_bf16 v[92:95], v[152:155], v[198:201], v[92:95]
	v_mfma_f32_16x16x32_bf16 v[80:83], v[144:147], v[206:209], v[80:83]
	v_mfma_f32_16x16x32_bf16 v[76:79], v[152:155], v[206:209], v[76:79]
	s_setprio 0
	s_setprio 1
	v_mfma_f32_16x16x32_bf16 v[120:123], v[156:159], v[172:175], v[120:123]
	v_mfma_f32_16x16x32_bf16 v[116:119], v[164:167], v[172:175], v[116:119]
	v_mfma_f32_16x16x32_bf16 v[104:107], v[156:159], v[186:189], v[104:107]
	v_mfma_f32_16x16x32_bf16 v[100:103], v[164:167], v[186:189], v[100:103]
	v_mfma_f32_16x16x32_bf16 v[88:91], v[156:159], v[194:197], v[88:91]
	v_mfma_f32_16x16x32_bf16 v[84:87], v[164:167], v[194:197], v[84:87]
	v_mfma_f32_16x16x32_bf16 v[72:75], v[156:159], v[202:205], v[72:75]
	v_mfma_f32_16x16x32_bf16 v[68:71], v[164:167], v[202:205], v[68:71]
	v_mfma_f32_16x16x32_bf16 v[120:123], v[160:163], v[182:185], v[120:123]
	v_mfma_f32_16x16x32_bf16 v[116:119], v[168:171], v[182:185], v[116:119]
	v_mfma_f32_16x16x32_bf16 v[104:107], v[160:163], v[190:193], v[104:107]
	v_mfma_f32_16x16x32_bf16 v[100:103], v[168:171], v[190:193], v[100:103]
	v_mfma_f32_16x16x32_bf16 v[88:91], v[160:163], v[198:201], v[88:91]
	v_mfma_f32_16x16x32_bf16 v[84:87], v[168:171], v[198:201], v[84:87]
	v_mfma_f32_16x16x32_bf16 v[72:75], v[160:163], v[206:209], v[72:75]
	v_mfma_f32_16x16x32_bf16 v[68:71], v[168:171], v[206:209], v[68:71]
	s_setprio 0
	s_barrier
; __device__ __forceinline__ float bf_lo(unsigned w) { return __uint_as_float(w << 16); }
; __device__ __forceinline__ float bf_hi(unsigned w) { return __uint_as_float(w & 0xffff0000u); }
; #define PG8_STAGE(bufoff, gbase, voff) do { _Pragma("unroll") for (int _i = 0; _i < 2; ++_i) \
;         __builtin_amdgcn_global_load_lds((const unsigned*)((const char*)(gbase) + (voff)[_i]), (PG8_LAS unsigned*)(lds + (bufoff) + ldsw + _i * 8192), 16, 0, 0); } while (0)
; #define PG8_LDA(dst, b, h) do { _Pragma("unroll") for (int m = 0; m < 4; ++m) _Pragma("unroll") for (int k = 0; k < 2; ++k) dst[m][k] = *(const PG8_LAS bf16x8*)(lds + PG8_SA(b, h) + aoff + m * 2048 + k * 1024); } while (0)
; #define PG8_MMA(ai, bj, At, Bt) do { __builtin_amdgcn_s_setprio(1); _Pragma("unroll") for (int m = 0; m < 4; ++m) _Pragma("unroll") for (int n = 0; n < 2; ++n) _Pragma("unroll") for (int k = 0; k < 2; ++k) \
;         acc[ai][bj][m][n] = __builtin_amdgcn_mfma_f32_16x16x32_bf16(Bt[n][k], At[m][k], acc[ai][bj][m][n], 0, 0, 0); __builtin_amdgcn_s_setprio(0); } while (0)
;     __device__ __forceinline__ void operator()(const f32x4 (&acc)[2][2][4][2], const Unit& u, int wr, int wc, int fr, int fq) const {
;     ...
;         const int row0 = u.pm * BM + wr * 64 + fr, col0 = u.pn * BM + wc * 32 + 4 * fq;
; #pragma unroll
;         for (int ai = 0; ai < 2; ++ai) {
;             f32x4 xo[16];
; #pragma unroll
;             for (int i = 0; i < 16; ++i) { const int m = i >> 2, bj = (i >> 1) & 1, n = i & 1; const size_t o = (size_t)(row0 + ai * HALF + m * 16) * cfg::DM + col0 + bj * HALF + n * 16;
;                 if (OLD_BF16) { const u32x2 ww = *(const u32x2*)(xoldb + o); xo[i] = (f32x4){bf_lo(ww.x), bf_hi(ww.x), bf_lo(ww.y), bf_hi(ww.y)}; } else xo[i] = *(const f32x4*)(xold + o); }
; template <class Epi, class Sched, bool ALIGN_EPI = false, bool SP2 = false>
; __device__ __forceinline__ void gemm_phase(PG8_LAS unsigned char* lds, const Gemm g, const Sched& S, const Epi& E) {
;     ...
;             PG8_WAIT_V(8); PG8_WAIT_L(0); PG8_BAR; PG8_MMA(0, 0, At, B0); PG8_MMA(0, 1, At, B1); PG8_BAR; PG8_SCHED;
;             PG8_LDA(At, 1, 1); PG8_STAGE(PG8_SB(1, 0), b3, voffB); PG8_STAGE(PG8_SB(1, 1), b3 + hstep, voffB); PG8_STAGE(PG8_SA(1, 0), a3, voffA);
;             PG8_WAIT_V(8); PG8_WAIT_L(0); PG8_BAR; PG8_MMA(1, 0, At, B0); PG8_MMA(1, 1, At, B1); PG8_BAR; PG8_SCHED;
	s_add_i32 s24, s46, s29
	v_lshl_add_u64 v[210:211], v[210:211], 0, s[78:79]
	s_mov_b32 m0, s24
	ds_read_b128 v[172:175], v180 offset:49152
	ds_read_b128 v[182:185], v180 offset:50176
	ds_read_b128 v[186:189], v180 offset:51200
	ds_read_b128 v[190:193], v180 offset:52224
	ds_read_b128 v[194:197], v180 offset:53248
	ds_read_b128 v[198:201], v180 offset:54272
	ds_read_b128 v[202:205], v180 offset:55296
	ds_read_b128 v[206:209], v180 offset:56320
	global_load_lds_dwordx4 v[210:211], off
	s_add_i32 m0, s24, 0x2000
	s_add_u32 s22, s22, 0x100080
	v_lshl_add_u64 v[210:211], v[212:213], 0, s[78:79]
	s_addc_u32 s23, s23, 0
	s_add_i32 s24, s47, s29
	global_load_lds_dwordx4 v[210:211], off
	v_lshl_add_u64 v[210:211], s[22:23], 0, v[2:3]
	s_mov_b32 m0, s24
	s_nop 0
	global_load_lds_dwordx4 v[210:211], off
	v_lshl_add_u64 v[210:211], s[22:23], 0, v[132:133]
	s_add_i32 m0, s24, 0x2000
	s_nop 0
	global_load_lds_dwordx4 v[210:211], off
	v_lshl_add_u64 v[210:211], v[214:215], 0, s[78:79]
	s_mov_b32 m0, s37
	s_nop 0
	global_load_lds_dwordx4 v[210:211], off
	v_lshl_add_u64 v[210:211], v[216:217], 0, s[78:79]
	s_mov_b32 m0, s38
	s_nop 0
	global_load_lds_dwordx4 v[210:211], off
	s_waitcnt vmcnt(8)
	s_waitcnt lgkmcnt(0)
	s_barrier
	s_setprio 1
	s_waitcnt lgkmcnt(0)
	v_mfma_f32_16x16x32_bf16 v[64:67], v[140:143], v[172:175], v[64:67]
	v_mfma_f32_16x16x32_bf16 v[60:63], v[148:151], v[172:175], v[60:63]
	v_mfma_f32_16x16x32_bf16 v[48:51], v[140:143], v[186:189], v[48:51]
	v_mfma_f32_16x16x32_bf16 v[44:47], v[148:151], v[186:189], v[44:47]
	v_mfma_f32_16x16x32_bf16 v[32:35], v[140:143], v[194:197], v[32:35]
	v_mfma_f32_16x16x32_bf16 v[28:31], v[148:151], v[194:197], v[28:31]
	v_mfma_f32_16x16x32_bf16 v[16:19], v[140:143], v[202:205], v[16:19]
	v_mfma_f32_16x16x32_bf16 v[12:15], v[148:151], v[202:205], v[12:15]
	v_mfma_f32_16x16x32_bf16 v[64:67], v[144:147], v[182:185], v[64:67]
	v_mfma_f32_16x16x32_bf16 v[60:63], v[152:155], v[182:185], v[60:63]
	v_mfma_f32_16x16x32_bf16 v[48:51], v[144:147], v[190:193], v[48:51]
	v_mfma_f32_16x16x32_bf16 v[44:47], v[152:155], v[190:193], v[44:47]
	v_mfma_f32_16x16x32_bf16 v[32:35], v[144:147], v[198:201], v[32:35]
	v_mfma_f32_16x16x32_bf16 v[28:31], v[152:155], v[198:201], v[28:31]
	v_mfma_f32_16x16x32_bf16 v[16:19], v[144:147], v[206:209], v[16:19]
	v_mfma_f32_16x16x32_bf16 v[12:15], v[152:155], v[206:209], v[12:15]
	s_setprio 0
	s_setprio 1
	v_mfma_f32_16x16x32_bf16 v[56:59], v[156:159], v[172:175], v[56:59]
	v_mfma_f32_16x16x32_bf16 v[52:55], v[164:167], v[172:175], v[52:55]
	v_mfma_f32_16x16x32_bf16 v[40:43], v[156:159], v[186:189], v[40:43]
	v_mfma_f32_16x16x32_bf16 v[36:39], v[164:167], v[186:189], v[36:39]
	v_mfma_f32_16x16x32_bf16 v[24:27], v[156:159], v[194:197], v[24:27]
	v_mfma_f32_16x16x32_bf16 v[20:23], v[164:167], v[194:197], v[20:23]
	v_mfma_f32_16x16x32_bf16 v[8:11], v[156:159], v[202:205], v[8:11]
	v_mfma_f32_16x16x32_bf16 v[4:7], v[164:167], v[202:205], v[4:7]
	v_mfma_f32_16x16x32_bf16 v[56:59], v[160:163], v[182:185], v[56:59]
	v_mfma_f32_16x16x32_bf16 v[52:55], v[168:171], v[182:185], v[52:55]
	v_mfma_f32_16x16x32_bf16 v[40:43], v[160:163], v[190:193], v[40:43]
	v_mfma_f32_16x16x32_bf16 v[36:39], v[168:171], v[190:193], v[36:39]
	v_mfma_f32_16x16x32_bf16 v[24:27], v[160:163], v[198:201], v[24:27]
	v_mfma_f32_16x16x32_bf16 v[20:23], v[168:171], v[198:201], v[20:23]
	v_mfma_f32_16x16x32_bf16 v[8:11], v[160:163], v[206:209], v[8:11]
	v_mfma_f32_16x16x32_bf16 v[4:7], v[168:171], v[206:209], v[4:7]
	s_setprio 0
	s_barrier
	s_add_i32 s45, s45, 2
	s_add_u32 s12, s12, 0x100
	s_addc_u32 s13, s13, 0
	s_add_u32 s43, s43, 0x100
	s_addc_u32 s44, s44, 0
	s_cmp_gt_u32 s45, 61
	s_cbranch_scc0 .LBB0_1680
	s_and_b64 vcc, exec, s[10:11]
	s_cbranch_vccz .LBB0_1683
	s_barrier
.LBB0_1683:
	s_lshl_b32 s12, s40, 8
	v_lshl_or_b32 v140, s39, 8, v177
	v_add_u32_e32 v142, s12, v1
	v_ashrrev_i32_e32 v141, 31, v140
	v_lshlrev_b64 v[184:185], 1, v[140:141]
	v_ashrrev_i32_e32 v143, 31, v142
	v_lshl_add_u64 v[144:145], s[8:9], 0, v[184:185]
	v_lshlrev_b64 v[186:187], 13, v[142:143]
	v_lshl_add_u64 v[146:147], v[144:145], 0, v[186:187]
	global_load_dwordx4 v[188:191], v[146:147], off
	global_load_dwordx4 v[192:195], v[146:147], off offset:256
	v_or_b32_e32 v146, 16, v142
	v_or_b32_e32 v148, 32, v142
	v_or_b32_e32 v150, 48, v142
	v_ashrrev_i32_e32 v147, 31, v146
	v_ashrrev_i32_e32 v149, 31, v148
	v_ashrrev_i32_e32 v151, 31, v150
	v_lshlrev_b64 v[166:167], 13, v[146:147]
	v_lshlrev_b64 v[156:157], 13, v[148:149]
	v_lshlrev_b64 v[146:147], 13, v[150:151]
	v_lshl_add_u64 v[148:149], v[144:145], 0, v[166:167]
	v_lshl_add_u64 v[150:151], v[144:145], 0, v[156:157]
	v_lshl_add_u64 v[182:183], v[144:145], 0, v[146:147]
	global_load_dwordx4 v[172:175], v[148:149], off
	global_load_dwordx4 v[168:171], v[148:149], off offset:256
	global_load_dwordx4 v[162:165], v[150:151], off
	global_load_dwordx4 v[158:161], v[150:151], off offset:256
	global_load_dwordx4 v[152:155], v[182:183], off
	s_nop 0
	global_load_dwordx4 v[148:151], v[182:183], off offset:256
	v_and_b32_e32 v182, 64, v229
	v_xor_b32_e32 v181, 16, v229
	v_add_u32_e32 v182, 64, v182
	v_xor_b32_e32 v183, 32, v229
	v_cmp_lt_i32_e32 vcc, v181, v182
	v_lshl_add_u64 v[186:187], s[8:9], 0, v[186:187]
	v_lshl_add_u64 v[184:185], v[186:187], 0, v[184:185]
	v_cndmask_b32_e32 v181, v229, v181, vcc
	v_cmp_lt_i32_e32 vcc, v183, v182
	v_lshlrev_b32_e32 v182, 2, v181
	s_waitcnt vmcnt(0)
; __device__ __forceinline__ unsigned cvt_pk_bf16(float lo, float hi) { f32x2_t v = {lo, hi}; bf16x2_t b = __builtin_convertvector(v, bf16x2_t); return __builtin_bit_cast(unsigned, b); }
; __device__ __forceinline__ float bf_lo(unsigned w) { return __uint_as_float(w << 16); }
; __device__ __forceinline__ float bf_hi(unsigned w) { return __uint_as_float(w & 0xffff0000u); }
;     __device__ __forceinline__ void operator()(const f32x4 (&acc)[2][2][4][2], const Unit& u, int wr, int wc, int fr, int fq) const {
;     ...
;         for (int ai = 0; ai < 2; ++ai) {
;             f32x4 xo[16];
; #pragma unroll
;             for (int i = 0; i < 16; ++i) { const int m = i >> 2, bj = (i >> 1) & 1, n = i & 1; const size_t o = (size_t)(row0 + ai * HALF + m * 16) * cfg::DM + col0 + bj * HALF + n * 16;
;                 if (OLD_BF16) { const u32x2 ww = *(const u32x2*)(xoldb + o); xo[i] = (f32x4){bf_lo(ww.x), bf_hi(ww.x), bf_lo(ww.y), bf_hi(ww.y)}; } else xo[i] = *(const f32x4*)(xold + o); }
;             asm volatile("" ::: "memory");
; #pragma unroll
;             for (int m = 0; m < 4; ++m) { const int r = row0 + ai * HALF + m * 16; float s = 0.f;
; #pragma unroll
;                 for (int bj = 0; bj < 2; ++bj)
; #pragma unroll
;                     for (int n = 0; n < 2; ++n) { const size_t o = (size_t)r * cfg::DM + col0 + bj * HALF + n * 16; const f32x4 xn = xo[m * 4 + bj * 2 + n] + acc[ai][bj][m][n];
;                         if (W_F32) *(f32x4*)(xnew + o) = xn;
;                         if (W_BF16) { u32x2 w; w.x = cvt_pk_bf16(xn[0], xn[1]); w.y = cvt_pk_bf16(xn[2], xn[3]); *(u32x2*)(xb + o) = w; }
;                         s += (xn[0] * xn[0] + xn[1] * xn[1]) + (xn[2] * xn[2] + xn[3] * xn[3]); }
;                 s += __shfl_xor(s, 16); s += __shfl_xor(s, 32);
;                 if (fq == 0) red[wc * 256 + (r - u.pm * BM)] = s; }
	v_swap_b32 v172, v174
	v_swap_b32 v173, v175
	v_swap_b32 v168, v170
	v_swap_b32 v169, v171
	v_swap_b32 v162, v164
	v_swap_b32 v163, v165
	v_swap_b32 v158, v160
	v_swap_b32 v159, v161
	v_swap_b32 v152, v154
	v_swap_b32 v153, v155
	v_swap_b32 v148, v150
	v_swap_b32 v149, v151
	v_lshlrev_b32_e32 v186, 16, v188
	v_and_b32_e32 v187, 0xffff0000, v188
	v_lshlrev_b32_e32 v188, 16, v189
	v_and_b32_e32 v189, 0xffff0000, v189
	v_lshlrev_b32_e32 v196, 16, v190
	v_and_b32_e32 v197, 0xffff0000, v190
	v_lshlrev_b32_e32 v190, 16, v191
	v_and_b32_e32 v191, 0xffff0000, v191
	v_cndmask_b32_e32 v183, v229, v183, vcc
	v_lshlrev_b32_e32 v198, 16, v192
	v_and_b32_e32 v199, 0xffff0000, v192
	v_lshlrev_b32_e32 v192, 16, v193
	v_and_b32_e32 v193, 0xffff0000, v193
	v_pk_add_f32 v[130:131], v[130:131], v[188:189]
	v_pk_add_f32 v[128:129], v[128:129], v[186:187]
	v_pk_add_f32 v[126:127], v[126:127], v[190:191]
	v_pk_add_f32 v[124:125], v[124:125], v[196:197]
	v_lshlrev_b32_e32 v181, 2, v183
	v_pk_add_f32 v[122:123], v[122:123], v[192:193]
	v_pk_add_f32 v[120:121], v[120:121], v[198:199]
	v_cvt_pk_bf16_f32 v186, v128, v129
	v_cvt_pk_bf16_f32 v187, v130, v131
	v_mul_f32_e32 v129, v129, v129
	v_mul_f32_e32 v131, v131, v131
	v_cvt_pk_bf16_f32 v188, v124, v125
	v_mul_f32_e32 v125, v125, v125
	v_mul_f32_e32 v183, v127, v127
	v_mul_f32_e32 v189, v121, v121
	v_mul_f32_e32 v190, v123, v123
	v_fmac_f32_e32 v129, v128, v128
	v_fmac_f32_e32 v131, v130, v130
	v_fmac_f32_e32 v125, v124, v124
	v_fmac_f32_e32 v183, v126, v126
	v_fmac_f32_e32 v189, v120, v120
	v_fmac_f32_e32 v190, v122, v122
	v_add_f32_e32 v124, v129, v131
	v_add_f32_e32 v125, v125, v183
	v_lshlrev_b32_e32 v200, 16, v194
	v_and_b32_e32 v201, 0xffff0000, v194
	v_lshlrev_b32_e32 v194, 16, v195
	v_and_b32_e32 v195, 0xffff0000, v195
	v_add_f32_e32 v124, v124, v125
	v_add_f32_e32 v125, v189, v190
	v_add_f32_e32 v128, v124, v125
	v_pk_add_f32 v[118:119], v[118:119], v[194:195]
	v_pk_add_f32 v[124:125], v[116:117], v[200:201]
	v_mul_f32_e32 v117, v119, v119
	v_mul_f32_e32 v116, v125, v125
	v_fmac_f32_e32 v116, v124, v124
	v_fmac_f32_e32 v117, v118, v118
	v_add_f32_e32 v116, v116, v117
	v_add_f32_e32 v116, v128, v116
	ds_bpermute_b32 v117, v182, v116
	v_cvt_pk_bf16_f32 v120, v120, v121
	v_cvt_pk_bf16_f32 v121, v122, v123
	v_cvt_pk_bf16_f32 v189, v126, v127
	v_mov_b32_e32 v206, v120
	v_mov_b32_e32 v207, v121
	s_waitcnt lgkmcnt(0)
	v_add_f32_e32 v116, v116, v117
	ds_bpermute_b32 v117, v181, v116
	v_cvt_pk_bf16_f32 v120, v124, v125
	v_cvt_pk_bf16_f32 v121, v118, v119
	v_mov_b32_e32 v202, v186
	v_mov_b32_e32 v203, v187
	v_mov_b32_e32 v204, v188
	v_mov_b32_e32 v205, v189
	global_store_dwordx4 v[184:185], v[202:205], off
	v_mov_b32_e32 v208, v120
	v_mov_b32_e32 v209, v121
	global_store_dwordx4 v[184:185], v[206:209], off offset:256
	s_and_saveexec_b64 s[22:23], s[0:1]
	s_cbranch_execz .LBB0_1685
	s_waitcnt lgkmcnt(0)
	v_add_f32_e32 v116, v116, v117
	ds_write_b32 v178, v116
.LBB0_1685:
	s_or_b64 exec, exec, s[22:23]
	v_lshlrev_b32_e32 v116, 16, v174
	s_waitcnt lgkmcnt(0)
	v_and_b32_e32 v117, 0xffff0000, v174
	v_lshlrev_b32_e32 v118, 16, v175
	v_and_b32_e32 v119, 0xffff0000, v175
	v_pk_add_f32 v[112:113], v[112:113], v[116:117]
	v_pk_add_f32 v[114:115], v[114:115], v[118:119]
	v_cvt_pk_bf16_f32 v116, v112, v113
	v_mul_f32_e32 v113, v113, v113
	v_lshlrev_b32_e32 v120, 16, v172
	v_and_b32_e32 v121, 0xffff0000, v172
	v_fmac_f32_e32 v113, v112, v112
	v_mul_f32_e32 v112, v115, v115
	v_lshlrev_b32_e32 v122, 16, v173
	v_and_b32_e32 v123, 0xffff0000, v173
	v_fmac_f32_e32 v112, v114, v114
	v_pk_add_f32 v[108:109], v[108:109], v[120:121]
	v_add_f32_e32 v113, v113, v112
	v_pk_add_f32 v[110:111], v[110:111], v[122:123]
	v_cvt_pk_bf16_f32 v112, v108, v109
	v_mul_f32_e32 v109, v109, v109
	v_fmac_f32_e32 v109, v108, v108
	v_mul_f32_e32 v108, v111, v111
	v_lshlrev_b32_e32 v124, 16, v170
	v_and_b32_e32 v125, 0xffff0000, v170
	v_lshlrev_b32_e32 v126, 16, v171
	v_and_b32_e32 v127, 0xffff0000, v171
	v_fmac_f32_e32 v108, v110, v110
	v_add_f32_e32 v108, v109, v108
	v_pk_add_f32 v[106:107], v[106:107], v[126:127]
	v_pk_add_f32 v[104:105], v[104:105], v[124:125]
	v_add_f32_e32 v108, v113, v108
	v_mul_f32_e32 v109, v105, v105
	v_mul_f32_e32 v113, v107, v107
	v_fmac_f32_e32 v109, v104, v104
	v_fmac_f32_e32 v113, v106, v106
	v_lshlrev_b32_e32 v128, 16, v168
	v_and_b32_e32 v129, 0xffff0000, v168
	v_lshlrev_b32_e32 v130, 16, v169
	v_and_b32_e32 v131, 0xffff0000, v169
	v_add_f32_e32 v109, v109, v113
	v_add_f32_e32 v113, v108, v109
	v_pk_add_f32 v[102:103], v[102:103], v[130:131]
	v_pk_add_f32 v[108:109], v[100:101], v[128:129]
	v_mul_f32_e32 v101, v103, v103
	v_mul_f32_e32 v100, v109, v109
	v_fmac_f32_e32 v100, v108, v108
	v_fmac_f32_e32 v101, v102, v102
	v_add_f32_e32 v100, v100, v101
	v_add_f32_e32 v100, v113, v100
	ds_bpermute_b32 v101, v182, v100
	v_lshl_add_u64 v[118:119], s[8:9], 0, v[166:167]
	v_lshl_add_u64 v[118:119], v[140:141], 1, v[118:119]
	v_cvt_pk_bf16_f32 v104, v104, v105
	v_cvt_pk_bf16_f32 v105, v106, v107
	s_waitcnt lgkmcnt(0)
	v_add_f32_e32 v100, v100, v101
	ds_bpermute_b32 v101, v181, v100
	v_cvt_pk_bf16_f32 v117, v114, v115
	v_cvt_pk_bf16_f32 v113, v110, v111
	v_mov_b32_e32 v214, v104
	v_mov_b32_e32 v215, v105
	v_cvt_pk_bf16_f32 v104, v108, v109
	v_cvt_pk_bf16_f32 v105, v102, v103
	v_mov_b32_e32 v210, v116
	v_mov_b32_e32 v211, v117
	v_mov_b32_e32 v212, v112
	v_mov_b32_e32 v213, v113
	global_store_dwordx4 v[118:119], v[210:213], off
	v_mov_b32_e32 v216, v104
	v_mov_b32_e32 v217, v105
	global_store_dwordx4 v[118:119], v[214:217], off offset:256
	s_and_saveexec_b64 s[22:23], s[0:1]
	s_cbranch_execz .LBB0_1687
	s_waitcnt lgkmcnt(0)
	v_add_f32_e32 v100, v100, v101
	ds_write_b32 v178, v100 offset:64
; __device__ __forceinline__ unsigned cvt_pk_bf16(float lo, float hi) { f32x2_t v = {lo, hi}; bf16x2_t b = __builtin_convertvector(v, bf16x2_t); return __builtin_bit_cast(unsigned, b); }
;     __device__ __forceinline__ void operator()(const f32x4 (&acc)[2][2][4][2], const Unit& u, int wr, int wc, int fr, int fq) const {
;     ...
;             for (int m = 0; m < 4; ++m) { const int r = row0 + ai * HALF + m * 16; float s = 0.f;
; #pragma unroll
;                 for (int bj = 0; bj < 2; ++bj)
; #pragma unroll
;                     for (int n = 0; n < 2; ++n) { const size_t o = (size_t)r * cfg::DM + col0 + bj * HALF + n * 16; const f32x4 xn = xo[m * 4 + bj * 2 + n] + acc[ai][bj][m][n];
;                         if (W_F32) *(f32x4*)(xnew + o) = xn;
;                         if (W_BF16) { u32x2 w; w.x = cvt_pk_bf16(xn[0], xn[1]); w.y = cvt_pk_bf16(xn[2], xn[3]); *(u32x2*)(xb + o) = w; }
;                         s += (xn[0] * xn[0] + xn[1] * xn[1]) + (xn[2] * xn[2] + xn[3] * xn[3]); }
;                 s += __shfl_xor(s, 16); s += __shfl_xor(s, 32);
;                 if (fq == 0) red[wc * 256 + (r - u.pm * BM)] = s; }
.LBB0_1687:
	s_or_b64 exec, exec, s[22:23]
	v_lshlrev_b32_e32 v100, 16, v164
	s_waitcnt lgkmcnt(0)
	v_and_b32_e32 v101, 0xffff0000, v164
	v_lshlrev_b32_e32 v102, 16, v165
	v_and_b32_e32 v103, 0xffff0000, v165
	v_pk_add_f32 v[96:97], v[96:97], v[100:101]
	v_pk_add_f32 v[98:99], v[98:99], v[102:103]
	v_cvt_pk_bf16_f32 v100, v96, v97
	v_mul_f32_e32 v97, v97, v97
	v_lshlrev_b32_e32 v104, 16, v162
	v_and_b32_e32 v105, 0xffff0000, v162
	v_fmac_f32_e32 v97, v96, v96
	v_mul_f32_e32 v96, v99, v99
	v_lshlrev_b32_e32 v106, 16, v163
	v_and_b32_e32 v107, 0xffff0000, v163
	v_fmac_f32_e32 v96, v98, v98
	v_pk_add_f32 v[92:93], v[92:93], v[104:105]
	v_add_f32_e32 v97, v97, v96
	v_pk_add_f32 v[94:95], v[94:95], v[106:107]
	v_cvt_pk_bf16_f32 v96, v92, v93
	v_mul_f32_e32 v93, v93, v93
	v_fmac_f32_e32 v93, v92, v92
	v_mul_f32_e32 v92, v95, v95
	v_lshlrev_b32_e32 v108, 16, v160
	v_and_b32_e32 v109, 0xffff0000, v160
	v_lshlrev_b32_e32 v110, 16, v161
	v_and_b32_e32 v111, 0xffff0000, v161
	v_fmac_f32_e32 v92, v94, v94
	v_add_f32_e32 v92, v93, v92
	v_pk_add_f32 v[90:91], v[90:91], v[110:111]
	v_pk_add_f32 v[88:89], v[88:89], v[108:109]
	v_add_f32_e32 v92, v97, v92
	v_mul_f32_e32 v93, v89, v89
	v_mul_f32_e32 v97, v91, v91
	v_fmac_f32_e32 v93, v88, v88
	v_fmac_f32_e32 v97, v90, v90
	v_lshlrev_b32_e32 v112, 16, v158
	v_and_b32_e32 v113, 0xffff0000, v158
	v_lshlrev_b32_e32 v114, 16, v159
	v_and_b32_e32 v115, 0xffff0000, v159
	v_add_f32_e32 v93, v93, v97
	v_add_f32_e32 v97, v92, v93
	v_pk_add_f32 v[86:87], v[86:87], v[114:115]
	v_pk_add_f32 v[92:93], v[84:85], v[112:113]
	v_mul_f32_e32 v85, v87, v87
	v_mul_f32_e32 v84, v93, v93
	v_fmac_f32_e32 v84, v92, v92
	v_fmac_f32_e32 v85, v86, v86
	v_add_f32_e32 v84, v84, v85
	v_add_f32_e32 v84, v97, v84
	ds_bpermute_b32 v85, v182, v84
	v_lshl_add_u64 v[102:103], s[8:9], 0, v[156:157]
	v_lshl_add_u64 v[102:103], v[140:141], 1, v[102:103]
	v_cvt_pk_bf16_f32 v88, v88, v89
	v_cvt_pk_bf16_f32 v89, v90, v91
	s_waitcnt lgkmcnt(0)
	v_add_f32_e32 v84, v84, v85
	ds_bpermute_b32 v85, v181, v84
	v_cvt_pk_bf16_f32 v101, v98, v99
	v_cvt_pk_bf16_f32 v97, v94, v95
	v_mov_b32_e32 v206, v88
	v_mov_b32_e32 v207, v89
	v_cvt_pk_bf16_f32 v88, v92, v93
	v_cvt_pk_bf16_f32 v89, v86, v87
	v_mov_b32_e32 v202, v100
	v_mov_b32_e32 v203, v101
	v_mov_b32_e32 v204, v96
	v_mov_b32_e32 v205, v97
	global_store_dwordx4 v[102:103], v[202:205], off
	v_mov_b32_e32 v208, v88
	v_mov_b32_e32 v209, v89
	global_store_dwordx4 v[102:103], v[206:209], off offset:256
	s_and_saveexec_b64 s[22:23], s[0:1]
	s_cbranch_execz .LBB0_1689
	s_waitcnt lgkmcnt(0)
	v_add_f32_e32 v84, v84, v85
	ds_write_b32 v178, v84 offset:128
.LBB0_1689:
	s_or_b64 exec, exec, s[22:23]
	v_lshlrev_b32_e32 v84, 16, v154
	s_waitcnt lgkmcnt(0)
	v_and_b32_e32 v85, 0xffff0000, v154
	v_lshlrev_b32_e32 v86, 16, v155
	v_and_b32_e32 v87, 0xffff0000, v155
	v_pk_add_f32 v[80:81], v[80:81], v[84:85]
	v_pk_add_f32 v[82:83], v[82:83], v[86:87]
	v_cvt_pk_bf16_f32 v84, v80, v81
	v_mul_f32_e32 v81, v81, v81
	v_lshlrev_b32_e32 v88, 16, v152
	v_and_b32_e32 v89, 0xffff0000, v152
	v_fmac_f32_e32 v81, v80, v80
	v_mul_f32_e32 v80, v83, v83
	v_lshlrev_b32_e32 v90, 16, v153
	v_and_b32_e32 v91, 0xffff0000, v153
	v_fmac_f32_e32 v80, v82, v82
	v_pk_add_f32 v[76:77], v[76:77], v[88:89]
	v_add_f32_e32 v81, v81, v80
	v_pk_add_f32 v[78:79], v[78:79], v[90:91]
	v_cvt_pk_bf16_f32 v80, v76, v77
	v_mul_f32_e32 v77, v77, v77
	v_fmac_f32_e32 v77, v76, v76
	v_mul_f32_e32 v76, v79, v79
	v_lshlrev_b32_e32 v92, 16, v150
	v_and_b32_e32 v93, 0xffff0000, v150
	v_lshlrev_b32_e32 v94, 16, v151
	v_and_b32_e32 v95, 0xffff0000, v151
	v_fmac_f32_e32 v76, v78, v78
	v_add_f32_e32 v76, v77, v76
	v_pk_add_f32 v[74:75], v[74:75], v[94:95]
	v_pk_add_f32 v[72:73], v[72:73], v[92:93]
	v_add_f32_e32 v76, v81, v76
	v_mul_f32_e32 v77, v73, v73
	v_mul_f32_e32 v81, v75, v75
	v_fmac_f32_e32 v77, v72, v72
	v_fmac_f32_e32 v81, v74, v74
	v_lshlrev_b32_e32 v96, 16, v148
	v_and_b32_e32 v97, 0xffff0000, v148
	v_lshlrev_b32_e32 v98, 16, v149
	v_and_b32_e32 v99, 0xffff0000, v149
	v_add_f32_e32 v77, v77, v81
	v_add_f32_e32 v81, v76, v77
	v_pk_add_f32 v[70:71], v[70:71], v[98:99]
	v_pk_add_f32 v[76:77], v[68:69], v[96:97]
	v_mul_f32_e32 v69, v71, v71
	v_mul_f32_e32 v68, v77, v77
	v_fmac_f32_e32 v68, v76, v76
	v_fmac_f32_e32 v69, v70, v70
	v_add_f32_e32 v68, v68, v69
	v_add_f32_e32 v68, v81, v68
	ds_bpermute_b32 v69, v182, v68
	v_lshl_add_u64 v[86:87], s[8:9], 0, v[146:147]
	v_lshl_add_u64 v[86:87], v[140:141], 1, v[86:87]
	v_cvt_pk_bf16_f32 v72, v72, v73
	v_cvt_pk_bf16_f32 v73, v74, v75
	s_waitcnt lgkmcnt(0)
	v_add_f32_e32 v68, v68, v69
	ds_bpermute_b32 v69, v181, v68
	v_cvt_pk_bf16_f32 v85, v82, v83
	v_cvt_pk_bf16_f32 v81, v78, v79
	v_mov_b32_e32 v214, v72
	v_mov_b32_e32 v215, v73
	v_cvt_pk_bf16_f32 v72, v76, v77
	v_cvt_pk_bf16_f32 v73, v70, v71
	v_mov_b32_e32 v210, v84
	v_mov_b32_e32 v211, v85
	v_mov_b32_e32 v212, v80
	v_mov_b32_e32 v213, v81
	global_store_dwordx4 v[86:87], v[210:213], off
	v_mov_b32_e32 v216, v72
	v_mov_b32_e32 v217, v73
	global_store_dwordx4 v[86:87], v[214:217], off offset:256
	s_and_saveexec_b64 s[22:23], s[0:1]
	s_cbranch_execz .LBB0_1691
	s_waitcnt lgkmcnt(0)
	v_add_f32_e32 v68, v68, v69
	ds_write_b32 v178, v68 offset:192
; __device__ __forceinline__ unsigned cvt_pk_bf16(float lo, float hi) { f32x2_t v = {lo, hi}; bf16x2_t b = __builtin_convertvector(v, bf16x2_t); return __builtin_bit_cast(unsigned, b); }
; __device__ __forceinline__ float bf_lo(unsigned w) { return __uint_as_float(w << 16); }
; __device__ __forceinline__ float bf_hi(unsigned w) { return __uint_as_float(w & 0xffff0000u); }
;     __device__ __forceinline__ void operator()(const f32x4 (&acc)[2][2][4][2], const Unit& u, int wr, int wc, int fr, int fq) const {
;     ...
;         for (int ai = 0; ai < 2; ++ai) {
;             f32x4 xo[16];
; #pragma unroll
;             for (int i = 0; i < 16; ++i) { const int m = i >> 2, bj = (i >> 1) & 1, n = i & 1; const size_t o = (size_t)(row0 + ai * HALF + m * 16) * cfg::DM + col0 + bj * HALF + n * 16;
;                 if (OLD_BF16) { const u32x2 ww = *(const u32x2*)(xoldb + o); xo[i] = (f32x4){bf_lo(ww.x), bf_hi(ww.x), bf_lo(ww.y), bf_hi(ww.y)}; } else xo[i] = *(const f32x4*)(xold + o); }
;             asm volatile("" ::: "memory");
; #pragma unroll
;             for (int m = 0; m < 4; ++m) { const int r = row0 + ai * HALF + m * 16; float s = 0.f;
; #pragma unroll
;                 for (int bj = 0; bj < 2; ++bj)
; #pragma unroll
;                     for (int n = 0; n < 2; ++n) { const size_t o = (size_t)r * cfg::DM + col0 + bj * HALF + n * 16; const f32x4 xn = xo[m * 4 + bj * 2 + n] + acc[ai][bj][m][n];
;                         if (W_F32) *(f32x4*)(xnew + o) = xn;
;                         if (W_BF16) { u32x2 w; w.x = cvt_pk_bf16(xn[0], xn[1]); w.y = cvt_pk_bf16(xn[2], xn[3]); *(u32x2*)(xb + o) = w; }
;                         s += (xn[0] * xn[0] + xn[1] * xn[1]) + (xn[2] * xn[2] + xn[3] * xn[3]); }
;                 s += __shfl_xor(s, 16); s += __shfl_xor(s, 32);
;                 if (fq == 0) red[wc * 256 + (r - u.pm * BM)] = s; }
.LBB0_1691:
	s_or_b64 exec, exec, s[22:23]
	v_lshlrev_b64 v[84:85], 13, v[142:143]
	s_mov_b64 s[22:23], 0x100000
	v_lshl_add_u64 v[94:95], v[84:85], 0, s[22:23]
	s_waitcnt lgkmcnt(0)
	v_lshl_add_u64 v[68:69], v[144:145], 0, v[94:95]
	global_load_dwordx4 v[96:99], v[68:69], off
	global_load_dwordx4 v[100:103], v[68:69], off offset:256
	v_add_u32_e32 v68, 0x90, v142
	v_add_u32_e32 v70, 0xa0, v142
	v_add_u32_e32 v72, 0xb0, v142
	v_ashrrev_i32_e32 v69, 31, v68
	v_ashrrev_i32_e32 v71, 31, v70
	v_ashrrev_i32_e32 v73, 31, v72
	v_lshlrev_b64 v[68:69], 13, v[68:69]
	v_lshlrev_b64 v[70:71], 13, v[70:71]
	v_lshlrev_b64 v[72:73], 13, v[72:73]
	v_lshl_add_u64 v[68:69], v[144:145], 0, v[68:69]
	v_lshl_add_u64 v[70:71], v[144:145], 0, v[70:71]
	v_lshl_add_u64 v[104:105], v[144:145], 0, v[72:73]
	global_load_dwordx4 v[90:93], v[68:69], off
	global_load_dwordx4 v[86:89], v[68:69], off offset:256
	global_load_dwordx4 v[80:83], v[70:71], off
	global_load_dwordx4 v[76:79], v[70:71], off offset:256
	global_load_dwordx4 v[72:75], v[104:105], off
	s_nop 0
	global_load_dwordx4 v[68:71], v[104:105], off offset:256
	v_lshl_add_u64 v[94:95], s[8:9], 0, v[94:95]
	v_lshl_add_u64 v[94:95], v[140:141], 1, v[94:95]
	s_waitcnt vmcnt(7)
	v_lshlrev_b32_e32 v104, 16, v96
	v_and_b32_e32 v105, 0xffff0000, v96
	v_lshlrev_b32_e32 v96, 16, v97
	v_and_b32_e32 v97, 0xffff0000, v97
	v_lshlrev_b32_e32 v106, 16, v98
	v_and_b32_e32 v107, 0xffff0000, v98
	v_lshlrev_b32_e32 v98, 16, v99
	v_and_b32_e32 v99, 0xffff0000, v99
	s_waitcnt vmcnt(6)
	v_lshlrev_b32_e32 v108, 16, v100
	v_and_b32_e32 v109, 0xffff0000, v100
	v_lshlrev_b32_e32 v100, 16, v101
	v_and_b32_e32 v101, 0xffff0000, v101
	v_lshlrev_b32_e32 v110, 16, v102
	v_and_b32_e32 v111, 0xffff0000, v102
	v_pk_add_f32 v[66:67], v[66:67], v[96:97]
	v_pk_add_f32 v[64:65], v[64:65], v[104:105]
	v_pk_add_f32 v[62:63], v[62:63], v[98:99]
	v_pk_add_f32 v[60:61], v[60:61], v[106:107]
	v_lshlrev_b32_e32 v102, 16, v103
	v_and_b32_e32 v103, 0xffff0000, v103
	v_pk_add_f32 v[58:59], v[58:59], v[100:101]
	v_pk_add_f32 v[56:57], v[56:57], v[108:109]
	v_pk_add_f32 v[96:97], v[52:53], v[110:111]
	v_cvt_pk_bf16_f32 v52, v64, v65
	v_cvt_pk_bf16_f32 v53, v66, v67
	v_mul_f32_e32 v65, v65, v65
	v_mul_f32_e32 v67, v67, v67
	v_cvt_pk_bf16_f32 v98, v60, v61
	v_mul_f32_e32 v61, v61, v61
	v_mul_f32_e32 v99, v63, v63
	v_pk_add_f32 v[54:55], v[54:55], v[102:103]
	v_mul_f32_e32 v100, v57, v57
	v_mul_f32_e32 v101, v59, v59
	v_fmac_f32_e32 v65, v64, v64
	v_fmac_f32_e32 v67, v66, v66
	v_fmac_f32_e32 v61, v60, v60
	v_fmac_f32_e32 v99, v62, v62
	v_mul_f32_e32 v102, v97, v97
	v_mul_f32_e32 v103, v55, v55
	v_mov_b32_e32 v202, v52
	v_mov_b32_e32 v203, v53
	v_fmac_f32_e32 v100, v56, v56
	v_fmac_f32_e32 v101, v58, v58
	v_add_f32_e32 v52, v65, v67
	v_add_f32_e32 v53, v61, v99
	v_fmac_f32_e32 v102, v96, v96
	v_fmac_f32_e32 v103, v54, v54
	v_add_f32_e32 v60, v100, v101
	v_add_f32_e32 v52, v52, v53
	v_add_f32_e32 v52, v52, v60
	v_add_f32_e32 v53, v102, v103
	v_add_f32_e32 v52, v52, v53
	ds_bpermute_b32 v53, v182, v52
	v_cvt_pk_bf16_f32 v56, v56, v57
	v_cvt_pk_bf16_f32 v57, v58, v59
	v_cvt_pk_bf16_f32 v99, v62, v63
	v_mov_b32_e32 v206, v56
	v_mov_b32_e32 v207, v57
	s_waitcnt lgkmcnt(0)
	v_add_f32_e32 v52, v52, v53
	ds_bpermute_b32 v53, v181, v52
	v_cvt_pk_bf16_f32 v56, v96, v97
	v_cvt_pk_bf16_f32 v57, v54, v55
	v_mov_b32_e32 v204, v98
	v_mov_b32_e32 v205, v99
	global_store_dwordx4 v[94:95], v[202:205], off
	v_mov_b32_e32 v208, v56
	v_mov_b32_e32 v209, v57
	global_store_dwordx4 v[94:95], v[206:209], off offset:256
	s_and_saveexec_b64 s[22:23], s[0:1]
	s_cbranch_execz .LBB0_1693
	s_waitcnt lgkmcnt(0)
	v_add_f32_e32 v52, v52, v53
	ds_write_b32 v178, v52 offset:512
.LBB0_1693:
	s_or_b64 exec, exec, s[22:23]
	s_waitcnt vmcnt(7)
	v_swap_b32 v90, v92
	v_swap_b32 v91, v93
	v_lshlrev_b32_e32 v52, 16, v92
	s_waitcnt lgkmcnt(0)
	v_and_b32_e32 v53, 0xffff0000, v92
	v_lshlrev_b32_e32 v54, 16, v93
	v_and_b32_e32 v55, 0xffff0000, v93
	v_pk_add_f32 v[48:49], v[48:49], v[52:53]
	v_pk_add_f32 v[50:51], v[50:51], v[54:55]
	v_cvt_pk_bf16_f32 v52, v48, v49
	v_mul_f32_e32 v49, v49, v49
	v_lshlrev_b32_e32 v56, 16, v90
	v_and_b32_e32 v57, 0xffff0000, v90
	v_fmac_f32_e32 v49, v48, v48
	v_mul_f32_e32 v48, v51, v51
	v_lshlrev_b32_e32 v58, 16, v91
	v_and_b32_e32 v59, 0xffff0000, v91
	v_fmac_f32_e32 v48, v50, v50
	v_pk_add_f32 v[44:45], v[44:45], v[56:57]
	v_add_f32_e32 v49, v49, v48
	v_pk_add_f32 v[46:47], v[46:47], v[58:59]
	v_cvt_pk_bf16_f32 v48, v44, v45
	v_mul_f32_e32 v45, v45, v45
	v_fmac_f32_e32 v45, v44, v44
	v_mul_f32_e32 v44, v47, v47
	s_waitcnt vmcnt(6)
	v_swap_b32 v86, v88
	v_swap_b32 v87, v89
	v_lshlrev_b32_e32 v60, 16, v88
	v_and_b32_e32 v61, 0xffff0000, v88
	v_lshlrev_b32_e32 v62, 16, v89
	v_and_b32_e32 v63, 0xffff0000, v89
	v_fmac_f32_e32 v44, v46, v46
	v_add_f32_e32 v44, v45, v44
	v_pk_add_f32 v[42:43], v[42:43], v[62:63]
	v_pk_add_f32 v[40:41], v[40:41], v[60:61]
	v_add_f32_e32 v44, v49, v44
	v_mul_f32_e32 v45, v41, v41
	v_mul_f32_e32 v49, v43, v43
	v_fmac_f32_e32 v45, v40, v40
	v_fmac_f32_e32 v49, v42, v42
	v_lshlrev_b32_e32 v64, 16, v86
	v_and_b32_e32 v65, 0xffff0000, v86
	v_lshlrev_b32_e32 v66, 16, v87
	v_and_b32_e32 v67, 0xffff0000, v87
	v_add_f32_e32 v45, v45, v49
	v_add_f32_e32 v49, v44, v45
	v_pk_add_f32 v[38:39], v[38:39], v[66:67]
	v_pk_add_f32 v[44:45], v[36:37], v[64:65]
	v_mul_f32_e32 v37, v39, v39
	v_mul_f32_e32 v36, v45, v45
	v_fmac_f32_e32 v36, v44, v44
	v_fmac_f32_e32 v37, v38, v38
	v_add_f32_e32 v36, v36, v37
	v_add_f32_e32 v36, v49, v36
	ds_bpermute_b32 v37, v182, v36
	v_lshl_add_u64 v[54:55], s[8:9], 0, v[84:85]
	v_lshl_add_u64 v[54:55], v[140:141], 1, v[54:55]
	s_mov_b64 s[22:23], 0x120000
	s_mov_b32 s13, 0x120000
	s_waitcnt lgkmcnt(0)
	v_add_f32_e32 v36, v36, v37
	ds_bpermute_b32 v37, v181, v36
	v_lshl_add_u64 v[84:85], v[54:55], 0, s[22:23]
	v_add_co_u32_e32 v54, vcc, s13, v54
	v_cvt_pk_bf16_f32 v40, v40, v41
	v_cvt_pk_bf16_f32 v41, v42, v43
	v_cvt_pk_bf16_f32 v53, v50, v51
	v_addc_co_u32_e32 v55, vcc, 0, v55, vcc
	v_cvt_pk_bf16_f32 v49, v46, v47
	v_mov_b32_e32 v214, v40
	v_mov_b32_e32 v215, v41
	v_cvt_pk_bf16_f32 v40, v44, v45
	v_cvt_pk_bf16_f32 v41, v38, v39
	v_mov_b32_e32 v210, v52
	v_mov_b32_e32 v211, v53
	v_mov_b32_e32 v212, v48
	v_mov_b32_e32 v213, v49
	global_store_dwordx4 v[84:85], v[210:213], off
	v_mov_b32_e32 v216, v40
	v_mov_b32_e32 v217, v41
	global_store_dwordx4 v[84:85], v[214:217], off offset:256
	s_and_saveexec_b64 s[22:23], s[0:1]
	s_cbranch_execz .LBB0_1695
	s_waitcnt lgkmcnt(0)
	v_add_f32_e32 v36, v36, v37
	ds_write_b32 v178, v36 offset:576
; __device__ __forceinline__ unsigned cvt_pk_bf16(float lo, float hi) { f32x2_t v = {lo, hi}; bf16x2_t b = __builtin_convertvector(v, bf16x2_t); return __builtin_bit_cast(unsigned, b); }
;     __device__ __forceinline__ void operator()(const f32x4 (&acc)[2][2][4][2], const Unit& u, int wr, int wc, int fr, int fq) const {
;     ...
;             for (int m = 0; m < 4; ++m) { const int r = row0 + ai * HALF + m * 16; float s = 0.f;
; #pragma unroll
;                 for (int bj = 0; bj < 2; ++bj)
; #pragma unroll
;                     for (int n = 0; n < 2; ++n) { const size_t o = (size_t)r * cfg::DM + col0 + bj * HALF + n * 16; const f32x4 xn = xo[m * 4 + bj * 2 + n] + acc[ai][bj][m][n];
;                         if (W_F32) *(f32x4*)(xnew + o) = xn;
;                         if (W_BF16) { u32x2 w; w.x = cvt_pk_bf16(xn[0], xn[1]); w.y = cvt_pk_bf16(xn[2], xn[3]); *(u32x2*)(xb + o) = w; }
;                         s += (xn[0] * xn[0] + xn[1] * xn[1]) + (xn[2] * xn[2] + xn[3] * xn[3]); }
;                 s += __shfl_xor(s, 16); s += __shfl_xor(s, 32);
;                 if (fq == 0) red[wc * 256 + (r - u.pm * BM)] = s; }
.LBB0_1695:
	s_or_b64 exec, exec, s[22:23]
	s_waitcnt vmcnt(7)
	v_swap_b32 v80, v82
	v_swap_b32 v81, v83
	v_lshlrev_b32_e32 v38, 16, v83
	v_and_b32_e32 v39, 0xffff0000, v83
	v_lshlrev_b32_e32 v40, 16, v80
	v_and_b32_e32 v41, 0xffff0000, v80
	v_pk_add_f32 v[34:35], v[34:35], v[38:39]
	v_lshlrev_b32_e32 v36, 16, v82
	s_waitcnt lgkmcnt(0)
	v_and_b32_e32 v37, 0xffff0000, v82
	v_lshlrev_b32_e32 v42, 16, v81
	v_and_b32_e32 v43, 0xffff0000, v81
	v_cvt_pk_bf16_f32 v39, v34, v35
	v_mul_f32_e32 v35, v35, v35
	v_pk_add_f32 v[28:29], v[28:29], v[40:41]
	v_pk_add_f32 v[36:37], v[32:33], v[36:37]
	v_fmac_f32_e32 v35, v34, v34
	v_pk_add_f32 v[30:31], v[30:31], v[42:43]
	v_cvt_pk_bf16_f32 v34, v28, v29
	v_mul_f32_e32 v29, v29, v29
	v_cvt_pk_bf16_f32 v38, v36, v37
	v_mul_f32_e32 v37, v37, v37
	v_fmac_f32_e32 v29, v28, v28
	v_mul_f32_e32 v28, v31, v31
	s_waitcnt vmcnt(6)
	v_swap_b32 v76, v78
	v_swap_b32 v77, v79
	v_lshlrev_b32_e32 v44, 16, v78
	v_and_b32_e32 v45, 0xffff0000, v78
	v_lshlrev_b32_e32 v46, 16, v79
	v_and_b32_e32 v47, 0xffff0000, v79
	v_fmac_f32_e32 v37, v36, v36
	v_fmac_f32_e32 v28, v30, v30
	v_add_f32_e32 v35, v37, v35
	v_add_f32_e32 v28, v29, v28
	v_pk_add_f32 v[26:27], v[26:27], v[46:47]
	v_pk_add_f32 v[24:25], v[24:25], v[44:45]
	v_add_f32_e32 v28, v35, v28
	v_mul_f32_e32 v29, v25, v25
	v_mul_f32_e32 v35, v27, v27
	v_fmac_f32_e32 v29, v24, v24
	v_fmac_f32_e32 v35, v26, v26
	v_lshlrev_b32_e32 v48, 16, v76
	v_and_b32_e32 v49, 0xffff0000, v76
	v_lshlrev_b32_e32 v50, 16, v77
	v_and_b32_e32 v51, 0xffff0000, v77
	v_add_f32_e32 v29, v29, v35
	v_add_f32_e32 v35, v28, v29
	v_pk_add_f32 v[22:23], v[22:23], v[50:51]
	v_pk_add_f32 v[28:29], v[20:21], v[48:49]
	v_mul_f32_e32 v21, v23, v23
	v_mul_f32_e32 v20, v29, v29
	v_fmac_f32_e32 v20, v28, v28
	v_fmac_f32_e32 v21, v22, v22
	v_add_f32_e32 v20, v20, v21
	v_add_f32_e32 v20, v35, v20
	ds_bpermute_b32 v21, v182, v20
	v_lshlrev_b64 v[52:53], 13, v[142:143]
	v_lshl_add_u64 v[32:33], s[8:9], 0, v[52:53]
	v_lshl_add_u64 v[32:33], v[140:141], 1, v[32:33]
	s_mov_b64 s[22:23], 0x140000
	s_waitcnt lgkmcnt(0)
	v_add_f32_e32 v20, v20, v21
	ds_bpermute_b32 v21, v181, v20
	s_mov_b32 s13, 0x140000
	v_lshl_add_u64 v[52:53], v[32:33], 0, s[22:23]
	v_add_co_u32_e32 v54, vcc, s13, v32
	v_cvt_pk_bf16_f32 v24, v24, v25
	v_cvt_pk_bf16_f32 v25, v26, v27
	v_addc_co_u32_e32 v55, vcc, 0, v33, vcc
	v_cvt_pk_bf16_f32 v35, v30, v31
	v_mov_b32_e32 v206, v24
	v_mov_b32_e32 v207, v25
	v_cvt_pk_bf16_f32 v24, v28, v29
	v_cvt_pk_bf16_f32 v25, v22, v23
	v_mov_b32_e32 v202, v38
	v_mov_b32_e32 v203, v39
	v_mov_b32_e32 v204, v34
	v_mov_b32_e32 v205, v35
	global_store_dwordx4 v[52:53], v[202:205], off
	v_mov_b32_e32 v208, v24
	v_mov_b32_e32 v209, v25
	global_store_dwordx4 v[52:53], v[206:209], off offset:256
	s_and_saveexec_b64 s[22:23], s[0:1]
	s_cbranch_execz .LBB0_1697
	s_waitcnt lgkmcnt(0)
	v_add_f32_e32 v20, v20, v21
	ds_write_b32 v178, v20 offset:640
.LBB0_1697:
	s_or_b64 exec, exec, s[22:23]
	s_waitcnt vmcnt(7)
	v_swap_b32 v72, v74
	v_swap_b32 v73, v75
	v_lshlrev_b32_e32 v20, 16, v74
	s_waitcnt lgkmcnt(0)
	v_and_b32_e32 v21, 0xffff0000, v74
	v_lshlrev_b32_e32 v22, 16, v75
	v_and_b32_e32 v23, 0xffff0000, v75
	v_pk_add_f32 v[16:17], v[16:17], v[20:21]
	v_pk_add_f32 v[18:19], v[18:19], v[22:23]
	v_cvt_pk_bf16_f32 v20, v16, v17
	v_mul_f32_e32 v17, v17, v17
	v_lshlrev_b32_e32 v24, 16, v72
	v_and_b32_e32 v25, 0xffff0000, v72
	v_fmac_f32_e32 v17, v16, v16
	v_mul_f32_e32 v16, v19, v19
	v_lshlrev_b32_e32 v26, 16, v73
	v_and_b32_e32 v27, 0xffff0000, v73
	v_fmac_f32_e32 v16, v18, v18
	v_pk_add_f32 v[12:13], v[12:13], v[24:25]
	v_add_f32_e32 v17, v17, v16
	v_pk_add_f32 v[14:15], v[14:15], v[26:27]
	v_cvt_pk_bf16_f32 v16, v12, v13
	v_mul_f32_e32 v13, v13, v13
	v_fmac_f32_e32 v13, v12, v12
	v_mul_f32_e32 v12, v15, v15
	s_waitcnt vmcnt(6)
	v_swap_b32 v68, v70
	v_swap_b32 v69, v71
	v_lshlrev_b32_e32 v28, 16, v70
	v_and_b32_e32 v29, 0xffff0000, v70
	v_lshlrev_b32_e32 v30, 16, v71
	v_and_b32_e32 v31, 0xffff0000, v71
	v_fmac_f32_e32 v12, v14, v14
	v_add_f32_e32 v12, v13, v12
	v_pk_add_f32 v[10:11], v[10:11], v[30:31]
	v_pk_add_f32 v[8:9], v[8:9], v[28:29]
	v_add_f32_e32 v12, v17, v12
	v_mul_f32_e32 v13, v9, v9
	v_mul_f32_e32 v17, v11, v11
	v_fmac_f32_e32 v13, v8, v8
	v_fmac_f32_e32 v17, v10, v10
	v_lshlrev_b32_e32 v34, 16, v68
	v_and_b32_e32 v35, 0xffff0000, v68
	v_lshlrev_b32_e32 v36, 16, v69
	v_and_b32_e32 v37, 0xffff0000, v69
	v_add_f32_e32 v13, v13, v17
	v_add_f32_e32 v17, v12, v13
	v_pk_add_f32 v[6:7], v[6:7], v[36:37]
	v_pk_add_f32 v[12:13], v[4:5], v[34:35]
	v_mul_f32_e32 v5, v7, v7
	v_mul_f32_e32 v4, v13, v13
	v_fmac_f32_e32 v4, v12, v12
	v_fmac_f32_e32 v5, v6, v6
	v_add_f32_e32 v4, v4, v5
	v_add_f32_e32 v4, v17, v4
	ds_bpermute_b32 v5, v182, v4
	s_mov_b64 s[22:23], 0x160000
	s_mov_b32 s13, 0x160000
	v_lshl_add_u64 v[22:23], v[32:33], 0, s[22:23]
	v_add_co_u32_e32 v32, vcc, s13, v32
	s_waitcnt lgkmcnt(0)
	v_add_f32_e32 v4, v4, v5
	ds_bpermute_b32 v5, v181, v4
	v_cvt_pk_bf16_f32 v8, v8, v9
	v_cvt_pk_bf16_f32 v9, v10, v11
	v_cvt_pk_bf16_f32 v21, v18, v19
	v_addc_co_u32_e32 v33, vcc, 0, v33, vcc
	v_cvt_pk_bf16_f32 v17, v14, v15
	v_mov_b32_e32 v214, v8
	v_mov_b32_e32 v215, v9
	v_cvt_pk_bf16_f32 v8, v12, v13
	v_cvt_pk_bf16_f32 v9, v6, v7
	v_mov_b32_e32 v210, v20
	v_mov_b32_e32 v211, v21
	v_mov_b32_e32 v212, v16
	v_mov_b32_e32 v213, v17
	global_store_dwordx4 v[22:23], v[210:213], off
	v_mov_b32_e32 v216, v8
	v_mov_b32_e32 v217, v9
	global_store_dwordx4 v[22:23], v[214:217], off offset:256
	s_and_saveexec_b64 s[22:23], s[0:1]
	s_cbranch_execz .LBB0_1699
	s_waitcnt lgkmcnt(0)
	v_add_f32_e32 v4, v4, v5
	ds_write_b32 v178, v4 offset:704
